# v60 + removed the 44 repeated lgkmcnt(0) waits in front of the GEMM MFMA blocks (provably satisfied by the asm wait before the barrier)
# baseline (speedup 1.0000x reference)
; #define PG8_STAGE(bufoff, gbase, voff) do { _Pragma("unroll") for (int _i = 0; _i < 2; ++_i) \
;         __builtin_amdgcn_global_load_lds((const unsigned*)(wsb + (size_t)(gbase) + (voff)[_i]), (LAS unsigned*)(lds + (bufoff) + ldsw + _i * 8192), 16, 0, 0); } while (0)
; #define PG8_WAIT_V(n) asm volatile("s_waitcnt vmcnt(" #n ")" ::: "memory")
; #define PG8_WAIT_L(n) asm volatile("s_waitcnt lgkmcnt(" #n ")" ::: "memory")
; template <class Epi, class Sched, bool PERM, bool FP8 = false, bool GATHER = false>
; DI void gemm_phase(LAS unsigned char* lds, const unsigned char* wsb, const unsigned lda, const unsigned ldb, const int nt, const Sched& S, const Epi& E) {
;     ...
;         for (int t = 0; t < nt; t += 2) {
;             const bool last = (t == nt - 2);
;             const unsigned b2 = last ? nB : cB + (unsigned)(t + 2) * kstep, b3 = b2 + kstep;
;             const int k2 = last ? 0 : t + 2, k3 = k2 + 1;
;             PG8_LDB(B0, 0, 0); PG8_LDB(B1, 0, 1); PG8_SCHED; PG8_LDA(At, 0, 0); PG8_STAGEA(PG8_SA(1, 1), t + 1, 1, false);
;             if constexpr (GATHER) { if (last) {
;                 int tz = tid; asm volatile("" : "+v"(tz));
; #pragma unroll
;                 for (int i = 0; i < 2; ++i) { int R, C; stage_rc(tz * 16 + i * 8192, R, C);
; #pragma unroll
;                     for (int h = 0; h < 2; ++h) { const unsigned tk = (unsigned)tokt[h * HALF + R]; offC[h][i] = (tk < (unsigned)NTOK ? tk : (unsigned)(NTOK - 1)) * lda + (unsigned)C * 2u; } } } }
;             PG8_WAIT_V(8); PG8_WAIT_L(0); PG8_BAR; PG8_MMA(0, 0, At, B0); PG8_MMA(0, 1, At, B1); PG8_BAR; PG8_SCHED;
;             PG8_LDA(At, 0, 1); PG8_STAGE(PG8_SB(0, 0), b2, voffB); PG8_STAGE(PG8_SB(0, 1), b2 + hstepB, voffB); PG8_STAGEA(PG8_SA(0, 0), k2, 0, last);
;             PG8_WAIT_V(8); PG8_WAIT_L(0); PG8_BAR; PG8_MMA(1, 0, At, B0); PG8_MMA(1, 1, At, B1); PG8_BAR; PG8_SCHED;
;             PG8_LDB(B0, 1, 0); PG8_LDB(B1, 1, 1); PG8_SCHED; PG8_LDA(At, 1, 0); PG8_STAGEA(PG8_SA(0, 1), k2, 1, last);
;             PG8_WAIT_V(8); PG8_WAIT_L(0); PG8_BAR; PG8_MMA(0, 0, At, B0); PG8_MMA(0, 1, At, B1); PG8_BAR; PG8_SCHED;
;             PG8_LDA(At, 1, 1); PG8_STAGE(PG8_SB(1, 0), b3, voffB); PG8_STAGE(PG8_SB(1, 1), b3 + hstepB, voffB); PG8_STAGEA(PG8_SA(1, 0), k3, 0, last);
;             PG8_WAIT_V(8); PG8_WAIT_L(0); PG8_BAR; PG8_MMA(1, 0, At, B0); PG8_MMA(1, 1, At, B1); PG8_BAR; PG8_SCHED;
;         }
.LBB0_405:
	ds_read_b128 v[130:133], v186
	ds_read_b128 v[134:137], v186 offset:1024
	ds_read_b128 v[138:141], v186 offset:2048
	ds_read_b128 v[142:145], v186 offset:3072
	ds_read_b128 v[146:149], v186 offset:16384
	ds_read_b128 v[150:153], v186 offset:17408
	ds_read_b128 v[160:163], v186 offset:18432
	ds_read_b128 v[164:167], v186 offset:19456
	s_add_i32 s41, s5, 0xfffe0080
	s_cmp_eq_u32 s7, 4
	s_cselect_b32 s40, s38, s4
	s_cselect_b32 s41, s37, s41
	s_add_i32 s52, s40, 0x80
	s_add_u32 s54, s10, s5
	s_addc_u32 s55, s11, 0
	s_mov_b32 m0, s29
	v_lshl_add_u64 v[206:207], s[54:55], 0, v[154:155]
	ds_read_b128 v[168:171], v185
	ds_read_b128 v[172:175], v185 offset:1024
	ds_read_b128 v[176:179], v185 offset:2048
	ds_read_b128 v[180:183], v185 offset:3072
	ds_read_b128 v[190:193], v185 offset:4096
	ds_read_b128 v[194:197], v185 offset:5120
	ds_read_b128 v[198:201], v185 offset:6144
	ds_read_b128 v[202:205], v185 offset:7168
	global_load_lds_dwordx4 v[206:207], off
	v_lshl_add_u64 v[206:207], s[54:55], 0, v[156:157]
	s_mov_b32 m0, s82
	s_nop 0
	global_load_lds_dwordx4 v[206:207], off
	s_waitcnt vmcnt(8)
	s_waitcnt lgkmcnt(0)
	s_barrier
	s_setprio 1
	v_mfma_f32_16x16x128_f8f6f4 v[126:129], v[130:137], v[168:175], v[126:129]
	v_mfma_f32_16x16x128_f8f6f4 v[122:125], v[138:145], v[168:175], v[122:125]
	v_mfma_f32_16x16x128_f8f6f4 v[110:113], v[130:137], v[176:183], v[110:113]
	v_mfma_f32_16x16x128_f8f6f4 v[106:109], v[138:145], v[176:183], v[106:109]
	v_mfma_f32_16x16x128_f8f6f4 v[206:209], v[130:137], v[190:197], v[94:97]
	v_mfma_f32_16x16x128_f8f6f4 v[210:213], v[138:145], v[190:197], v[90:93]
	v_mfma_f32_16x16x128_f8f6f4 v[214:217], v[130:137], v[198:205], v[78:81]
	v_mfma_f32_16x16x128_f8f6f4 v[218:221], v[138:145], v[198:205], v[74:77]
	s_setprio 0
	s_setprio 1
	v_mfma_f32_16x16x128_f8f6f4 v[118:121], v[146:153], v[168:175], v[118:121]
	v_mfma_f32_16x16x128_f8f6f4 v[114:117], v[160:167], v[168:175], v[114:117]
	v_mfma_f32_16x16x128_f8f6f4 v[102:105], v[146:153], v[176:183], v[102:105]
	v_mfma_f32_16x16x128_f8f6f4 v[98:101], v[160:167], v[176:183], v[98:101]
	v_mfma_f32_16x16x128_f8f6f4 v[168:171], v[146:153], v[190:197], v[86:89]
	v_mfma_f32_16x16x128_f8f6f4 v[172:175], v[160:167], v[190:197], v[82:85]
	v_mfma_f32_16x16x128_f8f6f4 v[176:179], v[146:153], v[198:205], v[70:73]
	v_mfma_f32_16x16x128_f8f6f4 v[180:183], v[160:167], v[198:205], v[66:69]
	s_setprio 0
	s_barrier
	s_add_u32 s54, s10, s40
	s_addc_u32 s55, s11, 0
	s_mov_b32 m0, s58
	v_lshl_add_u64 v[190:191], s[54:55], 0, v[154:155]
	s_add_i32 s53, s40, 0x20000
	ds_read_b128 v[66:69], v185 offset:16384
	ds_read_b128 v[70:73], v185 offset:17408
	ds_read_b128 v[74:77], v185 offset:18432
	ds_read_b128 v[78:81], v185 offset:19456
	ds_read_b128 v[82:85], v185 offset:20480
	ds_read_b128 v[86:89], v185 offset:21504
	ds_read_b128 v[90:93], v185 offset:22528
	ds_read_b128 v[94:97], v185 offset:23552
	global_load_lds_dwordx4 v[190:191], off
	v_lshl_add_u64 v[190:191], s[54:55], 0, v[156:157]
	s_add_u32 s54, s10, s53
	s_mov_b32 m0, s59
	s_addc_u32 s55, s11, 0
	global_load_lds_dwordx4 v[190:191], off
	v_lshl_add_u64 v[190:191], s[54:55], 0, v[154:155]
	s_mov_b32 m0, s60
	s_nop 0
	global_load_lds_dwordx4 v[190:191], off
	v_lshl_add_u64 v[190:191], s[54:55], 0, v[156:157]
	s_add_u32 s54, s10, s41
	s_mov_b32 m0, s61
	s_addc_u32 s55, s11, 0
	global_load_lds_dwordx4 v[190:191], off
	v_lshl_add_u64 v[190:191], s[54:55], 0, v[154:155]
	s_mov_b32 m0, s57
	s_nop 0
	global_load_lds_dwordx4 v[190:191], off
	v_lshl_add_u64 v[190:191], s[54:55], 0, v[156:157]
	s_mov_b32 m0, s62
	s_nop 0
	global_load_lds_dwordx4 v[190:191], off
	s_waitcnt vmcnt(8)
	s_waitcnt lgkmcnt(0)
	s_barrier
	s_setprio 1
	v_mfma_f32_16x16x128_f8f6f4 v[62:65], v[130:137], v[66:73], v[62:65]
	v_mfma_f32_16x16x128_f8f6f4 v[58:61], v[138:145], v[66:73], v[58:61]
	v_mfma_f32_16x16x128_f8f6f4 v[190:193], v[130:137], v[74:81], v[46:49]
	v_mfma_f32_16x16x128_f8f6f4 v[194:197], v[138:145], v[74:81], v[42:45]
	v_mfma_f32_16x16x128_f8f6f4 v[198:201], v[130:137], v[82:89], v[30:33]
	v_mfma_f32_16x16x128_f8f6f4 v[202:205], v[138:145], v[82:89], v[26:29]
	v_mfma_f32_16x16x128_f8f6f4 v[222:225], v[130:137], v[90:97], v[14:17]
	v_mfma_f32_16x16x128_f8f6f4 v[226:229], v[138:145], v[90:97], v[10:13]
	s_setprio 0
	s_setprio 1
	v_mfma_f32_16x16x128_f8f6f4 v[54:57], v[146:153], v[66:73], v[54:57]
	v_mfma_f32_16x16x128_f8f6f4 v[50:53], v[160:167], v[66:73], v[50:53]
	v_mfma_f32_16x16x128_f8f6f4 v[230:233], v[146:153], v[74:81], v[38:41]
	v_mfma_f32_16x16x128_f8f6f4 v[234:237], v[160:167], v[74:81], v[34:37]
	v_mfma_f32_16x16x128_f8f6f4 v[238:241], v[146:153], v[82:89], v[22:25]
	v_mfma_f32_16x16x128_f8f6f4 v[242:245], v[160:167], v[82:89], v[18:21]
	v_mfma_f32_16x16x128_f8f6f4 v[246:249], v[146:153], v[90:97], v[6:9]
	v_mfma_f32_16x16x128_f8f6f4 v[250:253], v[160:167], v[90:97], v[2:5]
	s_setprio 0
	s_barrier
; #define PG8_STAGE(bufoff, gbase, voff) do { _Pragma("unroll") for (int _i = 0; _i < 2; ++_i) \
;         __builtin_amdgcn_global_load_lds((const unsigned*)(wsb + (size_t)(gbase) + (voff)[_i]), (LAS unsigned*)(lds + (bufoff) + ldsw + _i * 8192), 16, 0, 0); } while (0)
; #define PG8_WAIT_V(n) asm volatile("s_waitcnt vmcnt(" #n ")" ::: "memory")
; #define PG8_WAIT_L(n) asm volatile("s_waitcnt lgkmcnt(" #n ")" ::: "memory")
; template <class Epi, class Sched, bool PERM, bool FP8 = false, bool GATHER = false>
; DI void gemm_phase(LAS unsigned char* lds, const unsigned char* wsb, const unsigned lda, const unsigned ldb, const int nt, const Sched& S, const Epi& E) {
;     ...
;         for (int t = 0; t < nt; t += 2) {
;             const bool last = (t == nt - 2);
;             const unsigned b2 = last ? nB : cB + (unsigned)(t + 2) * kstep, b3 = b2 + kstep;
;             const int k2 = last ? 0 : t + 2, k3 = k2 + 1;
;             PG8_LDB(B0, 0, 0); PG8_LDB(B1, 0, 1); PG8_SCHED; PG8_LDA(At, 0, 0); PG8_STAGEA(PG8_SA(1, 1), t + 1, 1, false);
;             if constexpr (GATHER) { if (last) {
;                 int tz = tid; asm volatile("" : "+v"(tz));
; #pragma unroll
;                 for (int i = 0; i < 2; ++i) { int R, C; stage_rc(tz * 16 + i * 8192, R, C);
; #pragma unroll
;                     for (int h = 0; h < 2; ++h) { const unsigned tk = (unsigned)tokt[h * HALF + R]; offC[h][i] = (tk < (unsigned)NTOK ? tk : (unsigned)(NTOK - 1)) * lda + (unsigned)C * 2u; } } } }
;             PG8_WAIT_V(8); PG8_WAIT_L(0); PG8_BAR; PG8_MMA(0, 0, At, B0); PG8_MMA(0, 1, At, B1); PG8_BAR; PG8_SCHED;
;             PG8_LDA(At, 0, 1); PG8_STAGE(PG8_SB(0, 0), b2, voffB); PG8_STAGE(PG8_SB(0, 1), b2 + hstepB, voffB); PG8_STAGEA(PG8_SA(0, 0), k2, 0, last);
;             PG8_WAIT_V(8); PG8_WAIT_L(0); PG8_BAR; PG8_MMA(1, 0, At, B0); PG8_MMA(1, 1, At, B1); PG8_BAR; PG8_SCHED;
;             PG8_LDB(B0, 1, 0); PG8_LDB(B1, 1, 1); PG8_SCHED; PG8_LDA(At, 1, 0); PG8_STAGEA(PG8_SA(0, 1), k2, 1, last);
;             PG8_WAIT_V(8); PG8_WAIT_L(0); PG8_BAR; PG8_MMA(0, 0, At, B0); PG8_MMA(0, 1, At, B1); PG8_BAR; PG8_SCHED;
;             PG8_LDA(At, 1, 1); PG8_STAGE(PG8_SB(1, 0), b3, voffB); PG8_STAGE(PG8_SB(1, 1), b3 + hstepB, voffB); PG8_STAGEA(PG8_SA(1, 0), k3, 0, last);
;             PG8_WAIT_V(8); PG8_WAIT_L(0); PG8_BAR; PG8_MMA(1, 0, At, B0); PG8_MMA(1, 1, At, B1); PG8_BAR; PG8_SCHED;
;         }
	s_nop 4
	ds_read_b128 v[2:5], v186 offset:32768
	ds_read_b128 v[6:9], v186 offset:33792
	ds_read_b128 v[18:21], v186 offset:34816
	ds_read_b128 v[22:25], v186 offset:35840
	ds_read_b128 v[130:133], v186 offset:49152
	ds_read_b128 v[134:137], v186 offset:50176
	ds_read_b128 v[138:141], v186 offset:51200
	ds_read_b128 v[142:145], v186 offset:52224
	s_add_i32 s53, s41, 0x20000
	s_add_u32 s54, s10, s53
	s_addc_u32 s55, s11, 0
	s_mov_b32 m0, s63
	v_lshl_add_u64 v[66:67], s[54:55], 0, v[154:155]
	ds_read_b128 v[10:13], v185 offset:32768
	ds_read_b128 v[14:17], v185 offset:33792
	ds_read_b128 v[26:29], v185 offset:34816
	ds_read_b128 v[30:33], v185 offset:35840
	ds_read_b128 v[34:37], v185 offset:36864
	ds_read_b128 v[38:41], v185 offset:37888
	ds_read_b128 v[42:45], v185 offset:38912
	ds_read_b128 v[46:49], v185 offset:39936
	global_load_lds_dwordx4 v[66:67], off
	v_lshl_add_u64 v[66:67], s[54:55], 0, v[156:157]
	s_mov_b32 m0, s64
	s_nop 0
	global_load_lds_dwordx4 v[66:67], off
	s_waitcnt vmcnt(8)
	s_waitcnt lgkmcnt(0)
	s_barrier
	s_setprio 1
	v_mfma_f32_16x16x128_f8f6f4 v[126:129], v[2:9], v[10:17], v[126:129]
	v_mfma_f32_16x16x128_f8f6f4 v[122:125], v[18:25], v[10:17], v[122:125]
	v_mfma_f32_16x16x128_f8f6f4 v[110:113], v[2:9], v[26:33], v[110:113]
	v_mfma_f32_16x16x128_f8f6f4 v[106:109], v[18:25], v[26:33], v[106:109]
	v_mfma_f32_16x16x128_f8f6f4 v[94:97], v[2:9], v[34:41], v[206:209]
	v_mfma_f32_16x16x128_f8f6f4 v[90:93], v[18:25], v[34:41], v[210:213]
	v_mfma_f32_16x16x128_f8f6f4 v[78:81], v[2:9], v[42:49], v[214:217]
	v_mfma_f32_16x16x128_f8f6f4 v[74:77], v[18:25], v[42:49], v[218:221]
	s_setprio 0
	s_setprio 1
	v_mfma_f32_16x16x128_f8f6f4 v[118:121], v[130:137], v[10:17], v[118:121]
	v_mfma_f32_16x16x128_f8f6f4 v[114:117], v[138:145], v[10:17], v[114:117]
	v_mfma_f32_16x16x128_f8f6f4 v[102:105], v[130:137], v[26:33], v[102:105]
	v_mfma_f32_16x16x128_f8f6f4 v[98:101], v[138:145], v[26:33], v[98:101]
	v_mfma_f32_16x16x128_f8f6f4 v[86:89], v[130:137], v[34:41], v[168:171]
	v_mfma_f32_16x16x128_f8f6f4 v[82:85], v[138:145], v[34:41], v[172:175]
	v_mfma_f32_16x16x128_f8f6f4 v[70:73], v[130:137], v[42:49], v[176:179]
	v_mfma_f32_16x16x128_f8f6f4 v[66:69], v[138:145], v[42:49], v[180:183]
	s_setprio 0
	s_barrier
	s_add_u32 s52, s10, s52
	s_addc_u32 s53, s11, 0
	s_mov_b32 m0, s74
	v_lshl_add_u64 v[10:11], s[52:53], 0, v[154:155]
	s_add_i32 s40, s40, 0x20080
	ds_read_b128 v[34:37], v185 offset:49152
	ds_read_b128 v[38:41], v185 offset:50176
	ds_read_b128 v[146:149], v185 offset:51200
	ds_read_b128 v[150:153], v185 offset:52224
	ds_read_b128 v[160:163], v185 offset:53248
	ds_read_b128 v[164:167], v185 offset:54272
	ds_read_b128 v[168:171], v185 offset:55296
	ds_read_b128 v[172:175], v185 offset:56320
	global_load_lds_dwordx4 v[10:11], off
	v_lshl_add_u64 v[10:11], s[52:53], 0, v[156:157]
	s_add_u32 s52, s10, s40
	s_mov_b32 m0, s75
	s_addc_u32 s53, s11, 0
	s_addk_i32 s41, 0x80
	global_load_lds_dwordx4 v[10:11], off
	v_lshl_add_u64 v[10:11], s[52:53], 0, v[154:155]
	s_mov_b32 m0, s78
	s_add_u32 s40, s10, s41
	global_load_lds_dwordx4 v[10:11], off
	v_lshl_add_u64 v[10:11], s[52:53], 0, v[156:157]
	s_mov_b32 m0, s79
	s_addc_u32 s41, s11, 0
	global_load_lds_dwordx4 v[10:11], off
	v_lshl_add_u64 v[10:11], s[40:41], 0, v[154:155]
	s_mov_b32 m0, s76
	s_nop 0
	global_load_lds_dwordx4 v[10:11], off
	v_lshl_add_u64 v[10:11], s[40:41], 0, v[156:157]
	s_mov_b32 m0, s77
	s_nop 0
	global_load_lds_dwordx4 v[10:11], off
	s_waitcnt vmcnt(8)
	s_waitcnt lgkmcnt(0)
	s_barrier
	s_setprio 1
	v_mfma_f32_16x16x128_f8f6f4 v[62:65], v[2:9], v[34:41], v[62:65]
	v_mfma_f32_16x16x128_f8f6f4 v[58:61], v[18:25], v[34:41], v[58:61]
	v_mfma_f32_16x16x128_f8f6f4 v[46:49], v[2:9], v[146:153], v[190:193]
	v_mfma_f32_16x16x128_f8f6f4 v[42:45], v[18:25], v[146:153], v[194:197]
	v_mfma_f32_16x16x128_f8f6f4 v[30:33], v[2:9], v[160:167], v[198:201]
	v_mfma_f32_16x16x128_f8f6f4 v[26:29], v[18:25], v[160:167], v[202:205]
	v_mfma_f32_16x16x128_f8f6f4 v[14:17], v[2:9], v[168:175], v[222:225]
	v_mfma_f32_16x16x128_f8f6f4 v[10:13], v[18:25], v[168:175], v[226:229]
	s_setprio 0
	s_setprio 1
	v_mfma_f32_16x16x128_f8f6f4 v[54:57], v[130:137], v[34:41], v[54:57]
	v_mfma_f32_16x16x128_f8f6f4 v[50:53], v[138:145], v[34:41], v[50:53]
	v_mfma_f32_16x16x128_f8f6f4 v[38:41], v[130:137], v[146:153], v[230:233]
	v_mfma_f32_16x16x128_f8f6f4 v[34:37], v[138:145], v[146:153], v[234:237]
	v_mfma_f32_16x16x128_f8f6f4 v[22:25], v[130:137], v[160:167], v[238:241]
	v_mfma_f32_16x16x128_f8f6f4 v[18:21], v[138:145], v[160:167], v[242:245]
	v_mfma_f32_16x16x128_f8f6f4 v[6:9], v[130:137], v[168:175], v[246:249]
	v_mfma_f32_16x16x128_f8f6f4 v[2:5], v[138:145], v[168:175], v[250:253]
	s_setprio 0
	s_barrier
	s_add_i32 s7, s7, 2
	s_addk_i32 s5, 0x100
	s_addk_i32 s4, 0x100
	s_cmp_gt_u32 s7, 5
	s_cbranch_scc0 .LBB0_405
	s_and_b64 vcc, exec, s[14:15]
	s_cbranch_vccz .LBB0_408
	s_barrier

; #define PG8_STAGE(bufoff, gbase, voff) do { _Pragma("unroll") for (int _i = 0; _i < 2; ++_i) \
;         __builtin_amdgcn_global_load_lds((const unsigned*)(wsb + (size_t)(gbase) + (voff)[_i]), (LAS unsigned*)(lds + (bufoff) + ldsw + _i * 8192), 16, 0, 0); } while (0)
; #define PG8_WAIT_V(n) asm volatile("s_waitcnt vmcnt(" #n ")" ::: "memory")
; #define PG8_WAIT_L(n) asm volatile("s_waitcnt lgkmcnt(" #n ")" ::: "memory")
; template <class Epi, class Sched, bool PERM, bool FP8 = false, bool GATHER = false>
; DI void gemm_phase(LAS unsigned char* lds, const unsigned char* wsb, const unsigned lda, const unsigned ldb, const int nt, const Sched& S, const Epi& E) {
;     ...
;         for (int t = 0; t < nt; t += 2) {
;             const bool last = (t == nt - 2);
;             const unsigned b2 = last ? nB : cB + (unsigned)(t + 2) * kstep, b3 = b2 + kstep;
;             const int k2 = last ? 0 : t + 2, k3 = k2 + 1;
;             PG8_LDB(B0, 0, 0); PG8_LDB(B1, 0, 1); PG8_SCHED; PG8_LDA(At, 0, 0); PG8_STAGEA(PG8_SA(1, 1), t + 1, 1, false);
;             if constexpr (GATHER) { if (last) {
;                 int tz = tid; asm volatile("" : "+v"(tz));
; #pragma unroll
;                 for (int i = 0; i < 2; ++i) { int R, C; stage_rc(tz * 16 + i * 8192, R, C);
; #pragma unroll
;                     for (int h = 0; h < 2; ++h) { const unsigned tk = (unsigned)tokt[h * HALF + R]; offC[h][i] = (tk < (unsigned)NTOK ? tk : (unsigned)(NTOK - 1)) * lda + (unsigned)C * 2u; } } } }
;             PG8_WAIT_V(8); PG8_WAIT_L(0); PG8_BAR; PG8_MMA(0, 0, At, B0); PG8_MMA(0, 1, At, B1); PG8_BAR; PG8_SCHED;
;             PG8_LDA(At, 0, 1); PG8_STAGE(PG8_SB(0, 0), b2, voffB); PG8_STAGE(PG8_SB(0, 1), b2 + hstepB, voffB); PG8_STAGEA(PG8_SA(0, 0), k2, 0, last);
;             PG8_WAIT_V(8); PG8_WAIT_L(0); PG8_BAR; PG8_MMA(1, 0, At, B0); PG8_MMA(1, 1, At, B1); PG8_BAR; PG8_SCHED;
;             PG8_LDB(B0, 1, 0); PG8_LDB(B1, 1, 1); PG8_SCHED; PG8_LDA(At, 1, 0); PG8_STAGEA(PG8_SA(0, 1), k2, 1, last);
;             PG8_WAIT_V(8); PG8_WAIT_L(0); PG8_BAR; PG8_MMA(0, 0, At, B0); PG8_MMA(0, 1, At, B1); PG8_BAR; PG8_SCHED;
;             PG8_LDA(At, 1, 1); PG8_STAGE(PG8_SB(1, 0), b3, voffB); PG8_STAGE(PG8_SB(1, 1), b3 + hstepB, voffB); PG8_STAGEA(PG8_SA(1, 0), k3, 0, last);
;             PG8_WAIT_V(8); PG8_WAIT_L(0); PG8_BAR; PG8_MMA(1, 0, At, B0); PG8_MMA(1, 1, At, B1); PG8_BAR; PG8_SCHED;
.LBB0_573:
	ds_read_b128 v[144:147], v142
	ds_read_b128 v[148:151], v142 offset:1024
	ds_read_b128 v[152:155], v142 offset:2048
	ds_read_b128 v[156:159], v142 offset:3072
	ds_read_b128 v[160:163], v142 offset:16384
	ds_read_b128 v[164:167], v142 offset:17408
	ds_read_b128 v[168:171], v142 offset:18432
	ds_read_b128 v[172:175], v142 offset:19456
	s_add_i32 s23, s19, 0xfffe0080
	s_cmp_eq_u32 s20, 4
	s_cselect_b32 s22, s66, s18
	s_cselect_b32 s23, s65, s23
	s_add_i32 s24, s22, 0x80
	s_add_u32 s26, s4, s19
	s_addc_u32 s27, s5, 0
	s_mov_b32 m0, s59
	v_lshl_add_u64 v[130:131], s[26:27], 0, v[136:137]
	ds_read_b128 v[176:179], v141
	ds_read_b128 v[180:183], v141 offset:1024
	ds_read_b128 v[184:187], v141 offset:2048
	ds_read_b128 v[188:191], v141 offset:3072
	ds_read_b128 v[192:195], v141 offset:4096
	ds_read_b128 v[196:199], v141 offset:5120
	ds_read_b128 v[200:203], v141 offset:6144
	ds_read_b128 v[204:207], v141 offset:7168
	global_load_lds_dwordx4 v[130:131], off
	v_lshl_add_u64 v[130:131], s[26:27], 0, v[138:139]
	s_mov_b32 m0, s60
	s_nop 0
	global_load_lds_dwordx4 v[130:131], off
	s_waitcnt vmcnt(8)
	s_waitcnt lgkmcnt(0)
	s_barrier
	s_setprio 1
	v_mfma_f32_16x16x128_f8f6f4 v[126:129], v[144:151], v[176:183], v[126:129]
	v_mfma_f32_16x16x128_f8f6f4 v[122:125], v[152:159], v[176:183], v[122:125]
	v_mfma_f32_16x16x128_f8f6f4 v[114:117], v[144:151], v[184:191], v[114:117]
	v_mfma_f32_16x16x128_f8f6f4 v[106:109], v[152:159], v[184:191], v[106:109]
	v_mfma_f32_16x16x128_f8f6f4 v[98:101], v[144:151], v[192:199], v[98:101]
	v_mfma_f32_16x16x128_f8f6f4 v[208:211], v[152:159], v[192:199], v[90:93]
	v_mfma_f32_16x16x128_f8f6f4 v[212:215], v[144:151], v[200:207], v[82:85]
	v_mfma_f32_16x16x128_f8f6f4 v[216:219], v[152:159], v[200:207], v[74:77]
	s_setprio 0
	s_setprio 1
	v_mfma_f32_16x16x128_f8f6f4 v[118:121], v[160:167], v[176:183], v[118:121]
	v_mfma_f32_16x16x128_f8f6f4 v[110:113], v[168:175], v[176:183], v[110:113]
	v_mfma_f32_16x16x128_f8f6f4 v[102:105], v[160:167], v[184:191], v[102:105]
	v_mfma_f32_16x16x128_f8f6f4 v[176:179], v[168:175], v[184:191], v[94:97]
	v_mfma_f32_16x16x128_f8f6f4 v[180:183], v[160:167], v[192:199], v[86:89]
	v_mfma_f32_16x16x128_f8f6f4 v[184:187], v[168:175], v[192:199], v[78:81]
	v_mfma_f32_16x16x128_f8f6f4 v[188:191], v[160:167], v[200:207], v[70:73]
	v_mfma_f32_16x16x128_f8f6f4 v[192:195], v[168:175], v[200:207], v[66:69]
	s_setprio 0
	s_barrier
	s_add_u32 s26, s4, s22
	s_addc_u32 s27, s5, 0
	s_mov_b32 m0, s38
	v_lshl_add_u64 v[130:131], s[26:27], 0, v[134:135]
	s_add_i32 s25, s22, 0x20000
	ds_read_b128 v[66:69], v141 offset:16384
	ds_read_b128 v[70:73], v141 offset:17408
	ds_read_b128 v[74:77], v141 offset:18432
	ds_read_b128 v[78:81], v141 offset:19456
	ds_read_b128 v[82:85], v141 offset:20480
	ds_read_b128 v[86:89], v141 offset:21504
	ds_read_b128 v[90:93], v141 offset:22528
	ds_read_b128 v[94:97], v141 offset:23552
	global_load_lds_dwordx4 v[130:131], off
	v_lshl_add_u64 v[130:131], s[26:27], 0, v[252:253]
	s_add_u32 s26, s4, s25
	s_mov_b32 m0, s39
	s_addc_u32 s27, s5, 0
	global_load_lds_dwordx4 v[130:131], off
	v_lshl_add_u64 v[130:131], s[26:27], 0, v[134:135]
	s_mov_b32 m0, s40
	s_nop 0
	global_load_lds_dwordx4 v[130:131], off
	v_lshl_add_u64 v[130:131], s[26:27], 0, v[252:253]
	s_add_u32 s26, s4, s23
	s_mov_b32 m0, s41
	s_addc_u32 s27, s5, 0
	global_load_lds_dwordx4 v[130:131], off
	v_lshl_add_u64 v[130:131], s[26:27], 0, v[136:137]
	s_mov_b32 m0, s29
	s_nop 0
	global_load_lds_dwordx4 v[130:131], off
	v_lshl_add_u64 v[130:131], s[26:27], 0, v[138:139]
	s_mov_b32 m0, s42
	s_nop 0
	global_load_lds_dwordx4 v[130:131], off
	s_waitcnt vmcnt(8)
	s_waitcnt lgkmcnt(0)
	s_barrier
	s_setprio 1
	v_mfma_f32_16x16x128_f8f6f4 v[62:65], v[144:151], v[66:73], v[62:65]
	v_mfma_f32_16x16x128_f8f6f4 v[58:61], v[152:159], v[66:73], v[58:61]
	v_mfma_f32_16x16x128_f8f6f4 v[50:53], v[144:151], v[74:81], v[50:53]
	v_mfma_f32_16x16x128_f8f6f4 v[196:199], v[152:159], v[74:81], v[42:45]
	v_mfma_f32_16x16x128_f8f6f4 v[200:203], v[144:151], v[82:89], v[34:37]
	v_mfma_f32_16x16x128_f8f6f4 v[204:207], v[152:159], v[82:89], v[26:29]
	v_mfma_f32_16x16x128_f8f6f4 v[220:223], v[144:151], v[90:97], v[18:21]
	v_mfma_f32_16x16x128_f8f6f4 v[224:227], v[152:159], v[90:97], v[10:13]
	s_setprio 0
	s_setprio 1
	v_mfma_f32_16x16x128_f8f6f4 v[54:57], v[160:167], v[66:73], v[54:57]
	v_mfma_f32_16x16x128_f8f6f4 v[228:231], v[168:175], v[66:73], v[46:49]
	v_mfma_f32_16x16x128_f8f6f4 v[232:235], v[160:167], v[74:81], v[38:41]
	v_mfma_f32_16x16x128_f8f6f4 v[236:239], v[168:175], v[74:81], v[30:33]
	v_mfma_f32_16x16x128_f8f6f4 v[240:243], v[160:167], v[82:89], v[22:25]
	v_mfma_f32_16x16x128_f8f6f4 v[244:247], v[168:175], v[82:89], v[14:17]
	v_mfma_f32_16x16x128_f8f6f4 v[248:251], v[160:167], v[90:97], v[6:9]
	v_mfma_f32_16x16x128_f8f6f4 v[130:133], v[168:175], v[90:97], v[2:5]
	s_setprio 0
	s_barrier
; #define PG8_STAGE(bufoff, gbase, voff) do { _Pragma("unroll") for (int _i = 0; _i < 2; ++_i) \
;         __builtin_amdgcn_global_load_lds((const unsigned*)(wsb + (size_t)(gbase) + (voff)[_i]), (LAS unsigned*)(lds + (bufoff) + ldsw + _i * 8192), 16, 0, 0); } while (0)
; #define PG8_WAIT_V(n) asm volatile("s_waitcnt vmcnt(" #n ")" ::: "memory")
; #define PG8_BAR __builtin_amdgcn_s_barrier()
; template <class Epi, class Sched, bool PERM, bool FP8 = false, bool GATHER = false>
; DI void gemm_phase(LAS unsigned char* lds, const unsigned char* wsb, const unsigned lda, const unsigned ldb, const int nt, const Sched& S, const Epi& E) {
;     ...
;         for (int t = 0; t < nt; t += 2) {
;             const bool last = (t == nt - 2);
;             const unsigned b2 = last ? nB : cB + (unsigned)(t + 2) * kstep, b3 = b2 + kstep;
;             const int k2 = last ? 0 : t + 2, k3 = k2 + 1;
;             PG8_LDB(B0, 0, 0); PG8_LDB(B1, 0, 1); PG8_SCHED; PG8_LDA(At, 0, 0); PG8_STAGEA(PG8_SA(1, 1), t + 1, 1, false);
;             if constexpr (GATHER) { if (last) {
;                 int tz = tid; asm volatile("" : "+v"(tz));
; #pragma unroll
;                 for (int i = 0; i < 2; ++i) { int R, C; stage_rc(tz * 16 + i * 8192, R, C);
; #pragma unroll
;                     for (int h = 0; h < 2; ++h) { const unsigned tk = (unsigned)tokt[h * HALF + R]; offC[h][i] = (tk < (unsigned)NTOK ? tk : (unsigned)(NTOK - 1)) * lda + (unsigned)C * 2u; } } } }
;             PG8_WAIT_V(8); PG8_WAIT_L(0); PG8_BAR; PG8_MMA(0, 0, At, B0); PG8_MMA(0, 1, At, B1); PG8_BAR; PG8_SCHED;
;             PG8_LDA(At, 0, 1); PG8_STAGE(PG8_SB(0, 0), b2, voffB); PG8_STAGE(PG8_SB(0, 1), b2 + hstepB, voffB); PG8_STAGEA(PG8_SA(0, 0), k2, 0, last);
;             PG8_WAIT_V(8); PG8_WAIT_L(0); PG8_BAR; PG8_MMA(1, 0, At, B0); PG8_MMA(1, 1, At, B1); PG8_BAR; PG8_SCHED;
;             PG8_LDB(B0, 1, 0); PG8_LDB(B1, 1, 1); PG8_SCHED; PG8_LDA(At, 1, 0); PG8_STAGEA(PG8_SA(0, 1), k2, 1, last);
;             PG8_WAIT_V(8); PG8_WAIT_L(0); PG8_BAR; PG8_MMA(0, 0, At, B0); PG8_MMA(0, 1, At, B1); PG8_BAR; PG8_SCHED;
;             PG8_LDA(At, 1, 1); PG8_STAGE(PG8_SB(1, 0), b3, voffB); PG8_STAGE(PG8_SB(1, 1), b3 + hstepB, voffB); PG8_STAGEA(PG8_SA(1, 0), k3, 0, last);
;             PG8_WAIT_V(8); PG8_WAIT_L(0); PG8_BAR; PG8_MMA(1, 0, At, B0); PG8_MMA(1, 1, At, B1); PG8_BAR; PG8_SCHED;
;         }
;         if (wr == 0) PG8_BAR;
	s_nop 4
	ds_read_b128 v[2:5], v142 offset:32768
	ds_read_b128 v[6:9], v142 offset:33792
	ds_read_b128 v[10:13], v142 offset:34816
	ds_read_b128 v[14:17], v142 offset:35840
	ds_read_b128 v[144:147], v142 offset:49152
	ds_read_b128 v[148:151], v142 offset:50176
	ds_read_b128 v[152:155], v142 offset:51200
	ds_read_b128 v[156:159], v142 offset:52224
	s_add_i32 s25, s23, 0x20000
	s_add_u32 s26, s4, s25
	s_addc_u32 s27, s5, 0
	s_mov_b32 m0, s43
	v_lshl_add_u64 v[66:67], s[26:27], 0, v[136:137]
	ds_read_b128 v[18:21], v141 offset:32768
	ds_read_b128 v[22:25], v141 offset:33792
	ds_read_b128 v[26:29], v141 offset:34816
	ds_read_b128 v[30:33], v141 offset:35840
	ds_read_b128 v[34:37], v141 offset:36864
	ds_read_b128 v[38:41], v141 offset:37888
	ds_read_b128 v[42:45], v141 offset:38912
	ds_read_b128 v[46:49], v141 offset:39936
	global_load_lds_dwordx4 v[66:67], off
	v_lshl_add_u64 v[66:67], s[26:27], 0, v[138:139]
	s_mov_b32 m0, s44
	s_nop 0
	global_load_lds_dwordx4 v[66:67], off
	s_waitcnt vmcnt(8)
	s_waitcnt lgkmcnt(0)
	s_barrier
	s_setprio 1
	v_mfma_f32_16x16x128_f8f6f4 v[126:129], v[2:9], v[18:25], v[126:129]
	v_mfma_f32_16x16x128_f8f6f4 v[122:125], v[10:17], v[18:25], v[122:125]
	v_mfma_f32_16x16x128_f8f6f4 v[114:117], v[2:9], v[26:33], v[114:117]
	v_mfma_f32_16x16x128_f8f6f4 v[106:109], v[10:17], v[26:33], v[106:109]
	v_mfma_f32_16x16x128_f8f6f4 v[98:101], v[2:9], v[34:41], v[98:101]
	v_mfma_f32_16x16x128_f8f6f4 v[90:93], v[10:17], v[34:41], v[208:211]
	v_mfma_f32_16x16x128_f8f6f4 v[82:85], v[2:9], v[42:49], v[212:215]
	v_mfma_f32_16x16x128_f8f6f4 v[74:77], v[10:17], v[42:49], v[216:219]
	s_setprio 0
	s_setprio 1
	v_mfma_f32_16x16x128_f8f6f4 v[118:121], v[144:151], v[18:25], v[118:121]
	v_mfma_f32_16x16x128_f8f6f4 v[110:113], v[152:159], v[18:25], v[110:113]
	v_mfma_f32_16x16x128_f8f6f4 v[102:105], v[144:151], v[26:33], v[102:105]
	v_mfma_f32_16x16x128_f8f6f4 v[94:97], v[152:159], v[26:33], v[176:179]
	v_mfma_f32_16x16x128_f8f6f4 v[86:89], v[144:151], v[34:41], v[180:183]
	v_mfma_f32_16x16x128_f8f6f4 v[78:81], v[152:159], v[34:41], v[184:187]
	v_mfma_f32_16x16x128_f8f6f4 v[70:73], v[144:151], v[42:49], v[188:191]
	v_mfma_f32_16x16x128_f8f6f4 v[66:69], v[152:159], v[42:49], v[192:195]
	s_setprio 0
	s_barrier
	s_add_u32 s24, s4, s24
	s_addc_u32 s25, s5, 0
	s_mov_b32 m0, s46
	v_lshl_add_u64 v[18:19], s[24:25], 0, v[134:135]
	s_add_i32 s22, s22, 0x20080
	ds_read_b128 v[160:163], v141 offset:49152
	ds_read_b128 v[164:167], v141 offset:50176
	ds_read_b128 v[168:171], v141 offset:51200
	ds_read_b128 v[172:175], v141 offset:52224
	ds_read_b128 v[176:179], v141 offset:53248
	ds_read_b128 v[180:183], v141 offset:54272
	ds_read_b128 v[184:187], v141 offset:55296
	ds_read_b128 v[188:191], v141 offset:56320
	global_load_lds_dwordx4 v[18:19], off
	v_lshl_add_u64 v[18:19], s[24:25], 0, v[252:253]
	s_add_u32 s24, s4, s22
	s_mov_b32 m0, s47
	s_addc_u32 s25, s5, 0
	s_addk_i32 s23, 0x80
	global_load_lds_dwordx4 v[18:19], off
	v_lshl_add_u64 v[18:19], s[24:25], 0, v[134:135]
	s_mov_b32 m0, s50
	s_add_u32 s22, s4, s23
	global_load_lds_dwordx4 v[18:19], off
	v_lshl_add_u64 v[18:19], s[24:25], 0, v[252:253]
	s_mov_b32 m0, s51
	s_addc_u32 s23, s5, 0
	global_load_lds_dwordx4 v[18:19], off
	v_lshl_add_u64 v[18:19], s[22:23], 0, v[136:137]
	s_mov_b32 m0, s48
	s_nop 0
	global_load_lds_dwordx4 v[18:19], off
	v_lshl_add_u64 v[18:19], s[22:23], 0, v[138:139]
	s_mov_b32 m0, s49
	s_nop 0
	global_load_lds_dwordx4 v[18:19], off
	s_waitcnt vmcnt(8)
	s_waitcnt lgkmcnt(0)
	s_barrier
	s_setprio 1
	v_mfma_f32_16x16x128_f8f6f4 v[62:65], v[2:9], v[160:167], v[62:65]
	v_mfma_f32_16x16x128_f8f6f4 v[58:61], v[10:17], v[160:167], v[58:61]
	v_mfma_f32_16x16x128_f8f6f4 v[50:53], v[2:9], v[168:175], v[50:53]
	v_mfma_f32_16x16x128_f8f6f4 v[42:45], v[10:17], v[168:175], v[196:199]
	v_mfma_f32_16x16x128_f8f6f4 v[34:37], v[2:9], v[176:183], v[200:203]
	v_mfma_f32_16x16x128_f8f6f4 v[26:29], v[10:17], v[176:183], v[204:207]
	v_mfma_f32_16x16x128_f8f6f4 v[18:21], v[2:9], v[184:191], v[220:223]
	v_mfma_f32_16x16x128_f8f6f4 v[10:13], v[10:17], v[184:191], v[224:227]
	s_setprio 0
	s_setprio 1
	v_mfma_f32_16x16x128_f8f6f4 v[54:57], v[144:151], v[160:167], v[54:57]
	v_mfma_f32_16x16x128_f8f6f4 v[46:49], v[152:159], v[160:167], v[228:231]
	v_mfma_f32_16x16x128_f8f6f4 v[38:41], v[144:151], v[168:175], v[232:235]
	v_mfma_f32_16x16x128_f8f6f4 v[30:33], v[152:159], v[168:175], v[236:239]
	v_mfma_f32_16x16x128_f8f6f4 v[22:25], v[144:151], v[176:183], v[240:243]
	v_mfma_f32_16x16x128_f8f6f4 v[14:17], v[152:159], v[176:183], v[244:247]
	v_mfma_f32_16x16x128_f8f6f4 v[6:9], v[144:151], v[184:191], v[248:251]
	v_mfma_f32_16x16x128_f8f6f4 v[2:5], v[152:159], v[184:191], v[130:133]
	s_setprio 0
	s_barrier
	s_add_i32 s20, s20, 2
	s_addk_i32 s19, 0x100
	s_addk_i32 s18, 0x100
	s_cmp_gt_u32 s20, 5
	s_cbranch_scc0 .LBB0_573
	s_and_b64 vcc, exec, s[12:13]
	s_cbranch_vccz .LBB0_576
	s_barrier

; #define PG8_STAGE(bufoff, gbase, voff) do { _Pragma("unroll") for (int _i = 0; _i < 2; ++_i) \
;         __builtin_amdgcn_global_load_lds((const unsigned*)(wsb + (size_t)(gbase) + (voff)[_i]), (LAS unsigned*)(lds + (bufoff) + ldsw + _i * 8192), 16, 0, 0); } while (0)
; #define PG8_WAIT_V(n) asm volatile("s_waitcnt vmcnt(" #n ")" ::: "memory")
; #define PG8_WAIT_L(n) asm volatile("s_waitcnt lgkmcnt(" #n ")" ::: "memory")
; template <class Epi, class Sched, bool PERM, bool FP8 = false, bool GATHER = false>
; DI void gemm_phase(LAS unsigned char* lds, const unsigned char* wsb, const unsigned lda, const unsigned ldb, const int nt, const Sched& S, const Epi& E) {
;     ...
;         for (int t = 0; t < nt; t += 2) {
;             const bool last = (t == nt - 2);
;             const unsigned b2 = last ? nB : cB + (unsigned)(t + 2) * kstep, b3 = b2 + kstep;
;             const int k2 = last ? 0 : t + 2, k3 = k2 + 1;
;             PG8_LDB(B0, 0, 0); PG8_LDB(B1, 0, 1); PG8_SCHED; PG8_LDA(At, 0, 0); PG8_STAGEA(PG8_SA(1, 1), t + 1, 1, false);
;             if constexpr (GATHER) { if (last) {
;                 int tz = tid; asm volatile("" : "+v"(tz));
; #pragma unroll
;                 for (int i = 0; i < 2; ++i) { int R, C; stage_rc(tz * 16 + i * 8192, R, C);
; #pragma unroll
;                     for (int h = 0; h < 2; ++h) { const unsigned tk = (unsigned)tokt[h * HALF + R]; offC[h][i] = (tk < (unsigned)NTOK ? tk : (unsigned)(NTOK - 1)) * lda + (unsigned)C * 2u; } } } }
;             PG8_WAIT_V(8); PG8_WAIT_L(0); PG8_BAR; PG8_MMA(0, 0, At, B0); PG8_MMA(0, 1, At, B1); PG8_BAR; PG8_SCHED;
;             PG8_LDA(At, 0, 1); PG8_STAGE(PG8_SB(0, 0), b2, voffB); PG8_STAGE(PG8_SB(0, 1), b2 + hstepB, voffB); PG8_STAGEA(PG8_SA(0, 0), k2, 0, last);
;             PG8_WAIT_V(8); PG8_WAIT_L(0); PG8_BAR; PG8_MMA(1, 0, At, B0); PG8_MMA(1, 1, At, B1); PG8_BAR; PG8_SCHED;
;             PG8_LDB(B0, 1, 0); PG8_LDB(B1, 1, 1); PG8_SCHED; PG8_LDA(At, 1, 0); PG8_STAGEA(PG8_SA(0, 1), k2, 1, last);
;             PG8_WAIT_V(8); PG8_WAIT_L(0); PG8_BAR; PG8_MMA(0, 0, At, B0); PG8_MMA(0, 1, At, B1); PG8_BAR; PG8_SCHED;
;             PG8_LDA(At, 1, 1); PG8_STAGE(PG8_SB(1, 0), b3, voffB); PG8_STAGE(PG8_SB(1, 1), b3 + hstepB, voffB); PG8_STAGEA(PG8_SA(1, 0), k3, 0, last);
;             PG8_WAIT_V(8); PG8_WAIT_L(0); PG8_BAR; PG8_MMA(1, 0, At, B0); PG8_MMA(1, 1, At, B1); PG8_BAR; PG8_SCHED;
.LBB0_725:
	ds_read_b128 v[150:153], v147
	ds_read_b128 v[154:157], v147 offset:1024
	ds_read_b128 v[158:161], v147 offset:2048
	ds_read_b128 v[162:165], v147 offset:3072
	ds_read_b128 v[166:169], v147 offset:16384
	ds_read_b128 v[170:173], v147 offset:17408
	ds_read_b128 v[174:177], v147 offset:18432
	ds_read_b128 v[178:181], v147 offset:19456
	s_add_i32 s85, s83, s42
	s_add_u32 s54, s42, 0x100
	s_addc_u32 s55, s43, 0
	s_cmp_eq_u32 s84, 4
	s_cselect_b32 s85, s82, s85
	s_mov_b32 m0, s68
	v_lshl_add_u64 v[142:143], v[140:141], 0, s[42:43]
	ds_read_b128 v[182:185], v146
	ds_read_b128 v[186:189], v146 offset:1024
	ds_read_b128 v[190:193], v146 offset:2048
	ds_read_b128 v[194:197], v146 offset:3072
	ds_read_b128 v[198:201], v146 offset:4096
	ds_read_b128 v[202:205], v146 offset:5120
	ds_read_b128 v[212:215], v146 offset:6144
	ds_read_b128 v[216:219], v146 offset:7168
	global_load_lds_dwordx4 v[142:143], off
	v_lshl_add_u64 v[142:143], v[138:139], 0, s[42:43]
	s_mov_b32 m0, s69
	s_cselect_b32 s43, 0, s54
	global_load_lds_dwordx4 v[142:143], off
	s_waitcnt vmcnt(8)
	s_waitcnt lgkmcnt(0)
	s_add_i32 s42, s85, 0x80
	s_barrier
	s_setprio 1
	v_mfma_f32_16x16x32_bf16 v[126:129], v[150:153], v[182:185], v[126:129]
	v_mfma_f32_16x16x32_bf16 v[122:125], v[158:161], v[182:185], v[122:125]
	v_mfma_f32_16x16x32_bf16 v[110:113], v[150:153], v[190:193], v[110:113]
	v_mfma_f32_16x16x32_bf16 v[106:109], v[158:161], v[190:193], v[106:109]
	v_mfma_f32_16x16x32_bf16 v[94:97], v[150:153], v[198:201], v[94:97]
	v_mfma_f32_16x16x32_bf16 v[90:93], v[158:161], v[198:201], v[90:93]
	v_mfma_f32_16x16x32_bf16 v[78:81], v[150:153], v[212:215], v[78:81]
	v_mfma_f32_16x16x32_bf16 v[74:77], v[158:161], v[212:215], v[74:77]
	v_mfma_f32_16x16x32_bf16 v[126:129], v[154:157], v[186:189], v[126:129]
	v_mfma_f32_16x16x32_bf16 v[122:125], v[162:165], v[186:189], v[122:125]
	v_mfma_f32_16x16x32_bf16 v[110:113], v[154:157], v[194:197], v[110:113]
	v_mfma_f32_16x16x32_bf16 v[106:109], v[162:165], v[194:197], v[106:109]
	v_mfma_f32_16x16x32_bf16 v[94:97], v[154:157], v[202:205], v[94:97]
	v_mfma_f32_16x16x32_bf16 v[90:93], v[162:165], v[202:205], v[90:93]
	v_mfma_f32_16x16x32_bf16 v[78:81], v[154:157], v[216:219], v[78:81]
	v_mfma_f32_16x16x32_bf16 v[74:77], v[162:165], v[216:219], v[74:77]
	s_setprio 0
	s_setprio 1
	v_mfma_f32_16x16x32_bf16 v[118:121], v[166:169], v[182:185], v[118:121]
	v_mfma_f32_16x16x32_bf16 v[114:117], v[174:177], v[182:185], v[114:117]
	v_mfma_f32_16x16x32_bf16 v[102:105], v[166:169], v[190:193], v[102:105]
	v_mfma_f32_16x16x32_bf16 v[98:101], v[174:177], v[190:193], v[98:101]
	v_mfma_f32_16x16x32_bf16 v[86:89], v[166:169], v[198:201], v[86:89]
	v_mfma_f32_16x16x32_bf16 v[82:85], v[174:177], v[198:201], v[82:85]
	v_mfma_f32_16x16x32_bf16 v[70:73], v[166:169], v[212:215], v[70:73]
	v_mfma_f32_16x16x32_bf16 v[66:69], v[174:177], v[212:215], v[66:69]
	v_mfma_f32_16x16x32_bf16 v[118:121], v[170:173], v[186:189], v[118:121]
	v_mfma_f32_16x16x32_bf16 v[114:117], v[178:181], v[186:189], v[114:117]
	v_mfma_f32_16x16x32_bf16 v[102:105], v[170:173], v[194:197], v[102:105]
	v_mfma_f32_16x16x32_bf16 v[98:101], v[178:181], v[194:197], v[98:101]
	v_mfma_f32_16x16x32_bf16 v[86:89], v[170:173], v[202:205], v[86:89]
	v_mfma_f32_16x16x32_bf16 v[82:85], v[178:181], v[202:205], v[82:85]
	v_mfma_f32_16x16x32_bf16 v[70:73], v[170:173], v[216:219], v[70:73]
	v_mfma_f32_16x16x32_bf16 v[66:69], v[178:181], v[216:219], v[66:69]
	s_setprio 0
	s_barrier
	s_add_u32 s86, s6, s85
	s_addc_u32 s87, s7, 0
	s_mov_b32 m0, s47
	v_lshl_add_u64 v[142:143], s[86:87], 0, v[134:135]
	ds_read_b128 v[182:185], v146 offset:16384
	ds_read_b128 v[186:189], v146 offset:17408
	ds_read_b128 v[190:193], v146 offset:18432
	ds_read_b128 v[194:197], v146 offset:19456
	ds_read_b128 v[198:201], v146 offset:20480
	ds_read_b128 v[202:205], v146 offset:21504
	ds_read_b128 v[212:215], v146 offset:22528
	ds_read_b128 v[216:219], v146 offset:23552
	global_load_lds_dwordx4 v[142:143], off
	v_lshl_add_u64 v[142:143], s[86:87], 0, v[130:131]
	s_add_i32 s86, s85, 0x20000
	s_add_u32 s86, s6, s86
	s_addc_u32 s87, s7, 0
	s_mov_b32 m0, s48
	s_add_u32 s88, s6, s43
	global_load_lds_dwordx4 v[142:143], off
	v_lshl_add_u64 v[142:143], s[86:87], 0, v[134:135]
	s_mov_b32 m0, s49
	s_addc_u32 s89, s7, 0
	global_load_lds_dwordx4 v[142:143], off
	v_lshl_add_u64 v[142:143], s[86:87], 0, v[130:131]
	s_add_u32 s86, s88, 0x1d094000
	s_mov_b32 m0, s56
	s_addc_u32 s87, s89, 0
	global_load_lds_dwordx4 v[142:143], off
	v_lshl_add_u64 v[142:143], s[86:87], 0, v[136:137]
	s_mov_b32 m0, s46
	s_nop 0
	global_load_lds_dwordx4 v[142:143], off
	v_lshl_add_u64 v[142:143], s[86:87], 0, v[132:133]
	s_mov_b32 m0, s57
	s_nop 0
	global_load_lds_dwordx4 v[142:143], off
	s_waitcnt vmcnt(8)
	s_waitcnt lgkmcnt(0)
	s_barrier
; #define PG8_STAGE(bufoff, gbase, voff) do { _Pragma("unroll") for (int _i = 0; _i < 2; ++_i) \
;         __builtin_amdgcn_global_load_lds((const unsigned*)(wsb + (size_t)(gbase) + (voff)[_i]), (LAS unsigned*)(lds + (bufoff) + ldsw + _i * 8192), 16, 0, 0); } while (0)
; #define PG8_WAIT_V(n) asm volatile("s_waitcnt vmcnt(" #n ")" ::: "memory")
; #define PG8_WAIT_L(n) asm volatile("s_waitcnt lgkmcnt(" #n ")" ::: "memory")
; template <class Epi, class Sched, bool PERM, bool FP8 = false, bool GATHER = false>
; DI void gemm_phase(LAS unsigned char* lds, const unsigned char* wsb, const unsigned lda, const unsigned ldb, const int nt, const Sched& S, const Epi& E) {
;     ...
;         for (int t = 0; t < nt; t += 2) {
;             const bool last = (t == nt - 2);
;             const unsigned b2 = last ? nB : cB + (unsigned)(t + 2) * kstep, b3 = b2 + kstep;
;             const int k2 = last ? 0 : t + 2, k3 = k2 + 1;
;             PG8_LDB(B0, 0, 0); PG8_LDB(B1, 0, 1); PG8_SCHED; PG8_LDA(At, 0, 0); PG8_STAGEA(PG8_SA(1, 1), t + 1, 1, false);
;             if constexpr (GATHER) { if (last) {
;                 int tz = tid; asm volatile("" : "+v"(tz));
; #pragma unroll
;                 for (int i = 0; i < 2; ++i) { int R, C; stage_rc(tz * 16 + i * 8192, R, C);
; #pragma unroll
;                     for (int h = 0; h < 2; ++h) { const unsigned tk = (unsigned)tokt[h * HALF + R]; offC[h][i] = (tk < (unsigned)NTOK ? tk : (unsigned)(NTOK - 1)) * lda + (unsigned)C * 2u; } } } }
;             PG8_WAIT_V(8); PG8_WAIT_L(0); PG8_BAR; PG8_MMA(0, 0, At, B0); PG8_MMA(0, 1, At, B1); PG8_BAR; PG8_SCHED;
;             PG8_LDA(At, 0, 1); PG8_STAGE(PG8_SB(0, 0), b2, voffB); PG8_STAGE(PG8_SB(0, 1), b2 + hstepB, voffB); PG8_STAGEA(PG8_SA(0, 0), k2, 0, last);
;             PG8_WAIT_V(8); PG8_WAIT_L(0); PG8_BAR; PG8_MMA(1, 0, At, B0); PG8_MMA(1, 1, At, B1); PG8_BAR; PG8_SCHED;
;             PG8_LDB(B0, 1, 0); PG8_LDB(B1, 1, 1); PG8_SCHED; PG8_LDA(At, 1, 0); PG8_STAGEA(PG8_SA(0, 1), k2, 1, last);
;             PG8_WAIT_V(8); PG8_WAIT_L(0); PG8_BAR; PG8_MMA(0, 0, At, B0); PG8_MMA(0, 1, At, B1); PG8_BAR; PG8_SCHED;
;             PG8_LDA(At, 1, 1); PG8_STAGE(PG8_SB(1, 0), b3, voffB); PG8_STAGE(PG8_SB(1, 1), b3 + hstepB, voffB); PG8_STAGEA(PG8_SA(1, 0), k3, 0, last);
;             PG8_WAIT_V(8); PG8_WAIT_L(0); PG8_BAR; PG8_MMA(1, 0, At, B0); PG8_MMA(1, 1, At, B1); PG8_BAR; PG8_SCHED;
	s_setprio 1
	v_mfma_f32_16x16x32_bf16 v[62:65], v[150:153], v[182:185], v[62:65]
	v_mfma_f32_16x16x32_bf16 v[58:61], v[158:161], v[182:185], v[58:61]
	v_mfma_f32_16x16x32_bf16 v[46:49], v[150:153], v[190:193], v[46:49]
	v_mfma_f32_16x16x32_bf16 v[42:45], v[158:161], v[190:193], v[42:45]
	v_mfma_f32_16x16x32_bf16 v[30:33], v[150:153], v[198:201], v[30:33]
	v_mfma_f32_16x16x32_bf16 v[26:29], v[158:161], v[198:201], v[26:29]
	v_mfma_f32_16x16x32_bf16 v[14:17], v[150:153], v[212:215], v[14:17]
	v_mfma_f32_16x16x32_bf16 v[10:13], v[158:161], v[212:215], v[10:13]
	v_mfma_f32_16x16x32_bf16 v[62:65], v[154:157], v[186:189], v[62:65]
	v_mfma_f32_16x16x32_bf16 v[58:61], v[162:165], v[186:189], v[58:61]
	v_mfma_f32_16x16x32_bf16 v[46:49], v[154:157], v[194:197], v[46:49]
	v_mfma_f32_16x16x32_bf16 v[42:45], v[162:165], v[194:197], v[42:45]
	v_mfma_f32_16x16x32_bf16 v[30:33], v[154:157], v[202:205], v[30:33]
	v_mfma_f32_16x16x32_bf16 v[26:29], v[162:165], v[202:205], v[26:29]
	v_mfma_f32_16x16x32_bf16 v[14:17], v[154:157], v[216:219], v[14:17]
	v_mfma_f32_16x16x32_bf16 v[10:13], v[162:165], v[216:219], v[10:13]
	s_setprio 0
	s_setprio 1
	v_mfma_f32_16x16x32_bf16 v[54:57], v[166:169], v[182:185], v[54:57]
	v_mfma_f32_16x16x32_bf16 v[50:53], v[174:177], v[182:185], v[50:53]
	v_mfma_f32_16x16x32_bf16 v[38:41], v[166:169], v[190:193], v[38:41]
	v_mfma_f32_16x16x32_bf16 v[34:37], v[174:177], v[190:193], v[34:37]
	v_mfma_f32_16x16x32_bf16 v[22:25], v[166:169], v[198:201], v[22:25]
	v_mfma_f32_16x16x32_bf16 v[18:21], v[174:177], v[198:201], v[18:21]
	v_mfma_f32_16x16x32_bf16 v[6:9], v[166:169], v[212:215], v[6:9]
	v_mfma_f32_16x16x32_bf16 v[2:5], v[174:177], v[212:215], v[2:5]
	v_mfma_f32_16x16x32_bf16 v[54:57], v[170:173], v[186:189], v[54:57]
	v_mfma_f32_16x16x32_bf16 v[50:53], v[178:181], v[186:189], v[50:53]
	v_mfma_f32_16x16x32_bf16 v[38:41], v[170:173], v[194:197], v[38:41]
	v_mfma_f32_16x16x32_bf16 v[34:37], v[178:181], v[194:197], v[34:37]
	v_mfma_f32_16x16x32_bf16 v[22:25], v[170:173], v[202:205], v[22:25]
	v_mfma_f32_16x16x32_bf16 v[18:21], v[178:181], v[202:205], v[18:21]
	v_mfma_f32_16x16x32_bf16 v[6:9], v[170:173], v[216:219], v[6:9]
	v_mfma_f32_16x16x32_bf16 v[2:5], v[178:181], v[216:219], v[2:5]
	s_setprio 0
	s_barrier
	ds_read_b128 v[150:153], v147 offset:32768
	ds_read_b128 v[154:157], v147 offset:33792
	ds_read_b128 v[158:161], v147 offset:34816
	ds_read_b128 v[162:165], v147 offset:35840
	ds_read_b128 v[166:169], v147 offset:49152
	ds_read_b128 v[170:173], v147 offset:50176
	ds_read_b128 v[174:177], v147 offset:51200
	ds_read_b128 v[178:181], v147 offset:52224
	s_add_u32 s86, s88, 0x1d0b4000
	s_addc_u32 s87, s89, 0
	s_mov_b32 m0, s58
	v_lshl_add_u64 v[142:143], s[86:87], 0, v[136:137]
	ds_read_b128 v[182:185], v146 offset:32768
	ds_read_b128 v[186:189], v146 offset:33792
	ds_read_b128 v[190:193], v146 offset:34816
	ds_read_b128 v[194:197], v146 offset:35840
	ds_read_b128 v[198:201], v146 offset:36864
	ds_read_b128 v[202:205], v146 offset:37888
	ds_read_b128 v[212:215], v146 offset:38912
	ds_read_b128 v[216:219], v146 offset:39936
	global_load_lds_dwordx4 v[142:143], off
	v_lshl_add_u64 v[142:143], s[86:87], 0, v[132:133]
	s_mov_b32 m0, s59
	s_nop 0
	global_load_lds_dwordx4 v[142:143], off
	s_waitcnt vmcnt(8)
	s_waitcnt lgkmcnt(0)
	s_barrier
	s_setprio 1
	v_mfma_f32_16x16x32_bf16 v[126:129], v[150:153], v[182:185], v[126:129]
	v_mfma_f32_16x16x32_bf16 v[122:125], v[158:161], v[182:185], v[122:125]
	v_mfma_f32_16x16x32_bf16 v[110:113], v[150:153], v[190:193], v[110:113]
	v_mfma_f32_16x16x32_bf16 v[106:109], v[158:161], v[190:193], v[106:109]
	v_mfma_f32_16x16x32_bf16 v[94:97], v[150:153], v[198:201], v[94:97]
	v_mfma_f32_16x16x32_bf16 v[90:93], v[158:161], v[198:201], v[90:93]
	v_mfma_f32_16x16x32_bf16 v[78:81], v[150:153], v[212:215], v[78:81]
	v_mfma_f32_16x16x32_bf16 v[74:77], v[158:161], v[212:215], v[74:77]
	v_mfma_f32_16x16x32_bf16 v[126:129], v[154:157], v[186:189], v[126:129]
	v_mfma_f32_16x16x32_bf16 v[122:125], v[162:165], v[186:189], v[122:125]
	v_mfma_f32_16x16x32_bf16 v[110:113], v[154:157], v[194:197], v[110:113]
	v_mfma_f32_16x16x32_bf16 v[106:109], v[162:165], v[194:197], v[106:109]
	v_mfma_f32_16x16x32_bf16 v[94:97], v[154:157], v[202:205], v[94:97]
	v_mfma_f32_16x16x32_bf16 v[90:93], v[162:165], v[202:205], v[90:93]
	v_mfma_f32_16x16x32_bf16 v[78:81], v[154:157], v[216:219], v[78:81]
	v_mfma_f32_16x16x32_bf16 v[74:77], v[162:165], v[216:219], v[74:77]
	s_setprio 0
	s_setprio 1
	v_mfma_f32_16x16x32_bf16 v[118:121], v[166:169], v[182:185], v[118:121]
	v_mfma_f32_16x16x32_bf16 v[114:117], v[174:177], v[182:185], v[114:117]
	v_mfma_f32_16x16x32_bf16 v[102:105], v[166:169], v[190:193], v[102:105]
	v_mfma_f32_16x16x32_bf16 v[98:101], v[174:177], v[190:193], v[98:101]
	v_mfma_f32_16x16x32_bf16 v[86:89], v[166:169], v[198:201], v[86:89]
	v_mfma_f32_16x16x32_bf16 v[82:85], v[174:177], v[198:201], v[82:85]
	v_mfma_f32_16x16x32_bf16 v[70:73], v[166:169], v[212:215], v[70:73]
	v_mfma_f32_16x16x32_bf16 v[66:69], v[174:177], v[212:215], v[66:69]
	v_mfma_f32_16x16x32_bf16 v[118:121], v[170:173], v[186:189], v[118:121]
	v_mfma_f32_16x16x32_bf16 v[114:117], v[178:181], v[186:189], v[114:117]
	v_mfma_f32_16x16x32_bf16 v[102:105], v[170:173], v[194:197], v[102:105]
	v_mfma_f32_16x16x32_bf16 v[98:101], v[178:181], v[194:197], v[98:101]
	v_mfma_f32_16x16x32_bf16 v[86:89], v[170:173], v[202:205], v[86:89]
	v_mfma_f32_16x16x32_bf16 v[82:85], v[178:181], v[202:205], v[82:85]
	v_mfma_f32_16x16x32_bf16 v[70:73], v[170:173], v[216:219], v[70:73]
	v_mfma_f32_16x16x32_bf16 v[66:69], v[178:181], v[216:219], v[66:69]
	s_setprio 0
	s_barrier
; #define PG8_STAGE(bufoff, gbase, voff) do { _Pragma("unroll") for (int _i = 0; _i < 2; ++_i) \
;         __builtin_amdgcn_global_load_lds((const unsigned*)(wsb + (size_t)(gbase) + (voff)[_i]), (LAS unsigned*)(lds + (bufoff) + ldsw + _i * 8192), 16, 0, 0); } while (0)
; #define PG8_WAIT_V(n) asm volatile("s_waitcnt vmcnt(" #n ")" ::: "memory")
; #define PG8_BAR __builtin_amdgcn_s_barrier()
; template <class Epi, class Sched, bool PERM, bool FP8 = false, bool GATHER = false>
; DI void gemm_phase(LAS unsigned char* lds, const unsigned char* wsb, const unsigned lda, const unsigned ldb, const int nt, const Sched& S, const Epi& E) {
;     ...
;         for (int t = 0; t < nt; t += 2) {
;             const bool last = (t == nt - 2);
;             const unsigned b2 = last ? nB : cB + (unsigned)(t + 2) * kstep, b3 = b2 + kstep;
;             const int k2 = last ? 0 : t + 2, k3 = k2 + 1;
;             PG8_LDB(B0, 0, 0); PG8_LDB(B1, 0, 1); PG8_SCHED; PG8_LDA(At, 0, 0); PG8_STAGEA(PG8_SA(1, 1), t + 1, 1, false);
;             if constexpr (GATHER) { if (last) {
;                 int tz = tid; asm volatile("" : "+v"(tz));
; #pragma unroll
;                 for (int i = 0; i < 2; ++i) { int R, C; stage_rc(tz * 16 + i * 8192, R, C);
; #pragma unroll
;                     for (int h = 0; h < 2; ++h) { const unsigned tk = (unsigned)tokt[h * HALF + R]; offC[h][i] = (tk < (unsigned)NTOK ? tk : (unsigned)(NTOK - 1)) * lda + (unsigned)C * 2u; } } } }
;             PG8_WAIT_V(8); PG8_WAIT_L(0); PG8_BAR; PG8_MMA(0, 0, At, B0); PG8_MMA(0, 1, At, B1); PG8_BAR; PG8_SCHED;
;             PG8_LDA(At, 0, 1); PG8_STAGE(PG8_SB(0, 0), b2, voffB); PG8_STAGE(PG8_SB(0, 1), b2 + hstepB, voffB); PG8_STAGEA(PG8_SA(0, 0), k2, 0, last);
;             PG8_WAIT_V(8); PG8_WAIT_L(0); PG8_BAR; PG8_MMA(1, 0, At, B0); PG8_MMA(1, 1, At, B1); PG8_BAR; PG8_SCHED;
;             PG8_LDB(B0, 1, 0); PG8_LDB(B1, 1, 1); PG8_SCHED; PG8_LDA(At, 1, 0); PG8_STAGEA(PG8_SA(0, 1), k2, 1, last);
;             PG8_WAIT_V(8); PG8_WAIT_L(0); PG8_BAR; PG8_MMA(0, 0, At, B0); PG8_MMA(0, 1, At, B1); PG8_BAR; PG8_SCHED;
;             PG8_LDA(At, 1, 1); PG8_STAGE(PG8_SB(1, 0), b3, voffB); PG8_STAGE(PG8_SB(1, 1), b3 + hstepB, voffB); PG8_STAGEA(PG8_SA(1, 0), k3, 0, last);
;             PG8_WAIT_V(8); PG8_WAIT_L(0); PG8_BAR; PG8_MMA(1, 0, At, B0); PG8_MMA(1, 1, At, B1); PG8_BAR; PG8_SCHED;
;         }
;         if (wr == 0) PG8_BAR;
	s_add_u32 s42, s6, s42
	s_addc_u32 s43, s7, 0
	s_mov_b32 m0, s60
	v_lshl_add_u64 v[142:143], s[42:43], 0, v[134:135]
	s_add_i32 s85, s85, 0x20080
	ds_read_b128 v[182:185], v146 offset:49152
	ds_read_b128 v[186:189], v146 offset:50176
	ds_read_b128 v[190:193], v146 offset:51200
	ds_read_b128 v[194:197], v146 offset:52224
	ds_read_b128 v[198:201], v146 offset:53248
	ds_read_b128 v[202:205], v146 offset:54272
	ds_read_b128 v[212:215], v146 offset:55296
	ds_read_b128 v[216:219], v146 offset:56320
	global_load_lds_dwordx4 v[142:143], off
	v_lshl_add_u64 v[142:143], s[42:43], 0, v[130:131]
	s_add_u32 s42, s6, s85
	s_mov_b32 m0, s61
	s_addc_u32 s43, s7, 0
	global_load_lds_dwordx4 v[142:143], off
	v_lshl_add_u64 v[142:143], s[42:43], 0, v[134:135]
	s_mov_b32 m0, s65
	s_nop 0
	global_load_lds_dwordx4 v[142:143], off
	v_lshl_add_u64 v[142:143], s[42:43], 0, v[130:131]
	s_add_u32 s42, s88, 0x1d094080
	s_mov_b32 m0, s66
	s_addc_u32 s43, s89, 0
	global_load_lds_dwordx4 v[142:143], off
	v_lshl_add_u64 v[142:143], s[42:43], 0, v[136:137]
	s_mov_b32 m0, s62
	s_nop 0
	global_load_lds_dwordx4 v[142:143], off
	v_lshl_add_u64 v[142:143], s[42:43], 0, v[132:133]
	s_mov_b32 m0, s63
	s_nop 0
	global_load_lds_dwordx4 v[142:143], off
	s_waitcnt vmcnt(8)
	s_waitcnt lgkmcnt(0)
	s_barrier
	s_setprio 1
	v_mfma_f32_16x16x32_bf16 v[62:65], v[150:153], v[182:185], v[62:65]
	v_mfma_f32_16x16x32_bf16 v[58:61], v[158:161], v[182:185], v[58:61]
	v_mfma_f32_16x16x32_bf16 v[46:49], v[150:153], v[190:193], v[46:49]
	v_mfma_f32_16x16x32_bf16 v[42:45], v[158:161], v[190:193], v[42:45]
	v_mfma_f32_16x16x32_bf16 v[30:33], v[150:153], v[198:201], v[30:33]
	v_mfma_f32_16x16x32_bf16 v[26:29], v[158:161], v[198:201], v[26:29]
	v_mfma_f32_16x16x32_bf16 v[14:17], v[150:153], v[212:215], v[14:17]
	v_mfma_f32_16x16x32_bf16 v[10:13], v[158:161], v[212:215], v[10:13]
	v_mfma_f32_16x16x32_bf16 v[62:65], v[154:157], v[186:189], v[62:65]
	v_mfma_f32_16x16x32_bf16 v[58:61], v[162:165], v[186:189], v[58:61]
	v_mfma_f32_16x16x32_bf16 v[46:49], v[154:157], v[194:197], v[46:49]
	v_mfma_f32_16x16x32_bf16 v[42:45], v[162:165], v[194:197], v[42:45]
	v_mfma_f32_16x16x32_bf16 v[30:33], v[154:157], v[202:205], v[30:33]
	v_mfma_f32_16x16x32_bf16 v[26:29], v[162:165], v[202:205], v[26:29]
	v_mfma_f32_16x16x32_bf16 v[14:17], v[154:157], v[216:219], v[14:17]
	v_mfma_f32_16x16x32_bf16 v[10:13], v[162:165], v[216:219], v[10:13]
	s_setprio 0
	s_setprio 1
	v_mfma_f32_16x16x32_bf16 v[54:57], v[166:169], v[182:185], v[54:57]
	v_mfma_f32_16x16x32_bf16 v[50:53], v[174:177], v[182:185], v[50:53]
	v_mfma_f32_16x16x32_bf16 v[38:41], v[166:169], v[190:193], v[38:41]
	v_mfma_f32_16x16x32_bf16 v[34:37], v[174:177], v[190:193], v[34:37]
	v_mfma_f32_16x16x32_bf16 v[22:25], v[166:169], v[198:201], v[22:25]
	v_mfma_f32_16x16x32_bf16 v[18:21], v[174:177], v[198:201], v[18:21]
	v_mfma_f32_16x16x32_bf16 v[6:9], v[166:169], v[212:215], v[6:9]
	v_mfma_f32_16x16x32_bf16 v[2:5], v[174:177], v[212:215], v[2:5]
	v_mfma_f32_16x16x32_bf16 v[54:57], v[170:173], v[186:189], v[54:57]
	v_mfma_f32_16x16x32_bf16 v[50:53], v[178:181], v[186:189], v[50:53]
	v_mfma_f32_16x16x32_bf16 v[38:41], v[170:173], v[194:197], v[38:41]
	v_mfma_f32_16x16x32_bf16 v[34:37], v[178:181], v[194:197], v[34:37]
	v_mfma_f32_16x16x32_bf16 v[22:25], v[170:173], v[202:205], v[22:25]
	v_mfma_f32_16x16x32_bf16 v[18:21], v[178:181], v[202:205], v[18:21]
	v_mfma_f32_16x16x32_bf16 v[6:9], v[170:173], v[216:219], v[6:9]
	v_mfma_f32_16x16x32_bf16 v[2:5], v[178:181], v[216:219], v[2:5]
	s_setprio 0
	s_barrier
	s_add_i32 s84, s84, 2
	s_cmp_gt_u32 s84, 5
	s_mov_b64 s[42:43], s[54:55]
	s_cbranch_scc0 .LBB0_725
	s_and_b64 vcc, exec, s[10:11]
	s_cbranch_vccz .LBB0_728
	s_barrier

; #define PG8_STAGE(bufoff, gbase, voff) do { _Pragma("unroll") for (int _i = 0; _i < 2; ++_i) \
;         __builtin_amdgcn_global_load_lds((const unsigned*)(wsb + (size_t)(gbase) + (voff)[_i]), (LAS unsigned*)(lds + (bufoff) + ldsw + _i * 8192), 16, 0, 0); } while (0)
; #define PG8_WAIT_V(n) asm volatile("s_waitcnt vmcnt(" #n ")" ::: "memory")
; #define PG8_WAIT_L(n) asm volatile("s_waitcnt lgkmcnt(" #n ")" ::: "memory")
; template <class Epi, class Sched, bool PERM, bool FP8 = false, bool GATHER = false>
; DI void gemm_phase(LAS unsigned char* lds, const unsigned char* wsb, const unsigned lda, const unsigned ldb, const int nt, const Sched& S, const Epi& E) {
;     ...
;         for (int t = 0; t < nt; t += 2) {
;             const bool last = (t == nt - 2);
;             const unsigned b2 = last ? nB : cB + (unsigned)(t + 2) * kstep, b3 = b2 + kstep;
;             const int k2 = last ? 0 : t + 2, k3 = k2 + 1;
;             PG8_LDB(B0, 0, 0); PG8_LDB(B1, 0, 1); PG8_SCHED; PG8_LDA(At, 0, 0); PG8_STAGEA(PG8_SA(1, 1), t + 1, 1, false);
;             if constexpr (GATHER) { if (last) {
;                 int tz = tid; asm volatile("" : "+v"(tz));
; #pragma unroll
;                 for (int i = 0; i < 2; ++i) { int R, C; stage_rc(tz * 16 + i * 8192, R, C);
; #pragma unroll
;                     for (int h = 0; h < 2; ++h) { const unsigned tk = (unsigned)tokt[h * HALF + R]; offC[h][i] = (tk < (unsigned)NTOK ? tk : (unsigned)(NTOK - 1)) * lda + (unsigned)C * 2u; } } } }
;             PG8_WAIT_V(8); PG8_WAIT_L(0); PG8_BAR; PG8_MMA(0, 0, At, B0); PG8_MMA(0, 1, At, B1); PG8_BAR; PG8_SCHED;
;             PG8_LDA(At, 0, 1); PG8_STAGE(PG8_SB(0, 0), b2, voffB); PG8_STAGE(PG8_SB(0, 1), b2 + hstepB, voffB); PG8_STAGEA(PG8_SA(0, 0), k2, 0, last);
;             PG8_WAIT_V(8); PG8_WAIT_L(0); PG8_BAR; PG8_MMA(1, 0, At, B0); PG8_MMA(1, 1, At, B1); PG8_BAR; PG8_SCHED;
;             PG8_LDB(B0, 1, 0); PG8_LDB(B1, 1, 1); PG8_SCHED; PG8_LDA(At, 1, 0); PG8_STAGEA(PG8_SA(0, 1), k2, 1, last);
;             PG8_WAIT_V(8); PG8_WAIT_L(0); PG8_BAR; PG8_MMA(0, 0, At, B0); PG8_MMA(0, 1, At, B1); PG8_BAR; PG8_SCHED;
;             PG8_LDA(At, 1, 1); PG8_STAGE(PG8_SB(1, 0), b3, voffB); PG8_STAGE(PG8_SB(1, 1), b3 + hstepB, voffB); PG8_STAGEA(PG8_SA(1, 0), k3, 0, last);
;             PG8_WAIT_V(8); PG8_WAIT_L(0); PG8_BAR; PG8_MMA(1, 0, At, B0); PG8_MMA(1, 1, At, B1); PG8_BAR; PG8_SCHED;
.LBB0_910:
	ds_read_b128 v[130:133], v162
	ds_read_b128 v[134:137], v162 offset:1024
	ds_read_b128 v[138:141], v162 offset:2048
	ds_read_b128 v[142:145], v162 offset:3072
	ds_read_b128 v[150:153], v162 offset:16384
	ds_read_b128 v[154:157], v162 offset:17408
	ds_read_b128 v[164:167], v162 offset:18432
	ds_read_b128 v[168:171], v162 offset:19456
	s_add_i32 s25, s21, 0xfffe0080
	s_cmp_eq_u32 s23, 4
	s_cselect_b32 s24, s59, s22
	s_cselect_b32 s25, s58, s25
	s_add_i32 s61, s24, 0x80
	s_add_u32 s62, s6, s21
	s_addc_u32 s63, s7, 0
	s_mov_b32 m0, s54
	v_lshl_add_u64 v[158:159], s[62:63], 0, v[148:149]
	ds_read_b128 v[172:175], v161
	ds_read_b128 v[176:179], v161 offset:1024
	ds_read_b128 v[180:183], v161 offset:2048
	ds_read_b128 v[184:187], v161 offset:3072
	ds_read_b128 v[188:191], v161 offset:4096
	ds_read_b128 v[192:195], v161 offset:5120
	ds_read_b128 v[196:199], v161 offset:6144
	ds_read_b128 v[200:203], v161 offset:7168
	global_load_lds_dwordx4 v[158:159], off
	v_lshl_add_u64 v[158:159], s[62:63], 0, v[146:147]
	s_mov_b32 m0, s55
	s_nop 0
	global_load_lds_dwordx4 v[158:159], off
	s_waitcnt vmcnt(8)
	s_waitcnt lgkmcnt(0)
	s_barrier
	s_setprio 1
	v_mfma_f32_16x16x128_f8f6f4 v[126:129], v[130:137], v[172:179], v[126:129]
	v_mfma_f32_16x16x128_f8f6f4 v[122:125], v[138:145], v[172:179], v[122:125]
	v_mfma_f32_16x16x128_f8f6f4 v[118:121], v[130:137], v[180:187], v[118:121]
	v_mfma_f32_16x16x128_f8f6f4 v[114:117], v[138:145], v[180:187], v[114:117]
	v_mfma_f32_16x16x128_f8f6f4 v[102:105], v[130:137], v[188:195], v[102:105]
	v_mfma_f32_16x16x128_f8f6f4 v[98:101], v[138:145], v[188:195], v[98:101]
	v_mfma_f32_16x16x128_f8f6f4 v[204:207], v[130:137], v[196:203], v[86:89]
	v_mfma_f32_16x16x128_f8f6f4 v[208:211], v[138:145], v[196:203], v[78:81]
	s_setprio 0
	s_setprio 1
	v_mfma_f32_16x16x128_f8f6f4 v[110:113], v[150:157], v[172:179], v[110:113]
	v_mfma_f32_16x16x128_f8f6f4 v[106:109], v[164:171], v[172:179], v[106:109]
	v_mfma_f32_16x16x128_f8f6f4 v[172:175], v[150:157], v[180:187], v[94:97]
	v_mfma_f32_16x16x128_f8f6f4 v[176:179], v[164:171], v[180:187], v[90:93]
	v_mfma_f32_16x16x128_f8f6f4 v[180:183], v[150:157], v[188:195], v[82:85]
	v_mfma_f32_16x16x128_f8f6f4 v[184:187], v[164:171], v[188:195], v[74:77]
	v_mfma_f32_16x16x128_f8f6f4 v[188:191], v[150:157], v[196:203], v[70:73]
	v_mfma_f32_16x16x128_f8f6f4 v[192:195], v[164:171], v[196:203], v[66:69]
	s_setprio 0
	s_barrier
	s_add_u32 s62, s6, s24
	s_addc_u32 s63, s7, 0
	s_mov_b32 m0, s36
	v_lshl_add_u64 v[158:159], s[62:63], 0, v[148:149]
	s_nop 0
	ds_read_b128 v[66:69], v161 offset:16384
	ds_read_b128 v[70:73], v161 offset:17408
	ds_read_b128 v[74:77], v161 offset:18432
	ds_read_b128 v[78:81], v161 offset:19456
	ds_read_b128 v[82:85], v161 offset:20480
	ds_read_b128 v[86:89], v161 offset:21504
	ds_read_b128 v[90:93], v161 offset:22528
	ds_read_b128 v[94:97], v161 offset:23552
	global_load_lds_dwordx4 v[158:159], off
	v_lshl_add_u64 v[158:159], s[62:63], 0, v[146:147]
	s_add_i32 s62, s24, 0x20000
	s_add_u32 s62, s6, s62
	s_mov_b32 m0, s37
	s_addc_u32 s63, s7, 0
	global_load_lds_dwordx4 v[158:159], off
	v_lshl_add_u64 v[158:159], s[62:63], 0, v[148:149]
	s_mov_b32 m0, s38
	s_nop 0
	global_load_lds_dwordx4 v[158:159], off
	v_lshl_add_u64 v[158:159], s[62:63], 0, v[146:147]
	s_add_u32 s62, s6, s25
	s_mov_b32 m0, s39
	s_addc_u32 s63, s7, 0
	global_load_lds_dwordx4 v[158:159], off
	v_lshl_add_u64 v[158:159], s[62:63], 0, v[148:149]
	s_mov_b32 m0, s29
	s_nop 0
	global_load_lds_dwordx4 v[158:159], off
	v_lshl_add_u64 v[158:159], s[62:63], 0, v[146:147]
	s_mov_b32 m0, s40
	s_nop 0
	global_load_lds_dwordx4 v[158:159], off
	s_waitcnt vmcnt(8)
	s_waitcnt lgkmcnt(0)
	s_barrier
	s_setprio 1
	v_mfma_f32_16x16x128_f8f6f4 v[62:65], v[130:137], v[66:73], v[62:65]
	v_mfma_f32_16x16x128_f8f6f4 v[58:61], v[138:145], v[66:73], v[58:61]
	v_mfma_f32_16x16x128_f8f6f4 v[50:53], v[130:137], v[74:81], v[50:53]
	v_mfma_f32_16x16x128_f8f6f4 v[196:199], v[138:145], v[74:81], v[42:45]
	v_mfma_f32_16x16x128_f8f6f4 v[200:203], v[130:137], v[82:89], v[38:41]
	v_mfma_f32_16x16x128_f8f6f4 v[212:215], v[138:145], v[82:89], v[30:33]
	v_mfma_f32_16x16x128_f8f6f4 v[216:219], v[130:137], v[90:97], v[22:25]
	v_mfma_f32_16x16x128_f8f6f4 v[220:223], v[138:145], v[90:97], v[14:17]
	s_setprio 0
	s_setprio 1
	v_mfma_f32_16x16x128_f8f6f4 v[54:57], v[150:157], v[66:73], v[54:57]
	v_mfma_f32_16x16x128_f8f6f4 v[224:227], v[164:171], v[66:73], v[46:49]
	v_mfma_f32_16x16x128_f8f6f4 v[228:231], v[150:157], v[74:81], v[34:37]
	v_mfma_f32_16x16x128_f8f6f4 v[232:235], v[164:171], v[74:81], v[26:29]
	v_mfma_f32_16x16x128_f8f6f4 v[236:239], v[150:157], v[82:89], v[18:21]
	v_mfma_f32_16x16x128_f8f6f4 v[240:243], v[164:171], v[82:89], v[10:13]
	v_mfma_f32_16x16x128_f8f6f4 v[244:247], v[150:157], v[90:97], v[6:9]
	v_mfma_f32_16x16x128_f8f6f4 v[248:251], v[164:171], v[90:97], v[2:5]
	s_setprio 0
	s_barrier
; #define PG8_STAGE(bufoff, gbase, voff) do { _Pragma("unroll") for (int _i = 0; _i < 2; ++_i) \
;         __builtin_amdgcn_global_load_lds((const unsigned*)(wsb + (size_t)(gbase) + (voff)[_i]), (LAS unsigned*)(lds + (bufoff) + ldsw + _i * 8192), 16, 0, 0); } while (0)
; #define PG8_WAIT_V(n) asm volatile("s_waitcnt vmcnt(" #n ")" ::: "memory")
; #define PG8_BAR __builtin_amdgcn_s_barrier()
; template <class Epi, class Sched, bool PERM, bool FP8 = false, bool GATHER = false>
; DI void gemm_phase(LAS unsigned char* lds, const unsigned char* wsb, const unsigned lda, const unsigned ldb, const int nt, const Sched& S, const Epi& E) {
;     ...
;         for (int t = 0; t < nt; t += 2) {
;             const bool last = (t == nt - 2);
;             const unsigned b2 = last ? nB : cB + (unsigned)(t + 2) * kstep, b3 = b2 + kstep;
;             const int k2 = last ? 0 : t + 2, k3 = k2 + 1;
;             PG8_LDB(B0, 0, 0); PG8_LDB(B1, 0, 1); PG8_SCHED; PG8_LDA(At, 0, 0); PG8_STAGEA(PG8_SA(1, 1), t + 1, 1, false);
;             if constexpr (GATHER) { if (last) {
;                 int tz = tid; asm volatile("" : "+v"(tz));
; #pragma unroll
;                 for (int i = 0; i < 2; ++i) { int R, C; stage_rc(tz * 16 + i * 8192, R, C);
; #pragma unroll
;                     for (int h = 0; h < 2; ++h) { const unsigned tk = (unsigned)tokt[h * HALF + R]; offC[h][i] = (tk < (unsigned)NTOK ? tk : (unsigned)(NTOK - 1)) * lda + (unsigned)C * 2u; } } } }
;             PG8_WAIT_V(8); PG8_WAIT_L(0); PG8_BAR; PG8_MMA(0, 0, At, B0); PG8_MMA(0, 1, At, B1); PG8_BAR; PG8_SCHED;
;             PG8_LDA(At, 0, 1); PG8_STAGE(PG8_SB(0, 0), b2, voffB); PG8_STAGE(PG8_SB(0, 1), b2 + hstepB, voffB); PG8_STAGEA(PG8_SA(0, 0), k2, 0, last);
;             PG8_WAIT_V(8); PG8_WAIT_L(0); PG8_BAR; PG8_MMA(1, 0, At, B0); PG8_MMA(1, 1, At, B1); PG8_BAR; PG8_SCHED;
;             PG8_LDB(B0, 1, 0); PG8_LDB(B1, 1, 1); PG8_SCHED; PG8_LDA(At, 1, 0); PG8_STAGEA(PG8_SA(0, 1), k2, 1, last);
;             PG8_WAIT_V(8); PG8_WAIT_L(0); PG8_BAR; PG8_MMA(0, 0, At, B0); PG8_MMA(0, 1, At, B1); PG8_BAR; PG8_SCHED;
;             PG8_LDA(At, 1, 1); PG8_STAGE(PG8_SB(1, 0), b3, voffB); PG8_STAGE(PG8_SB(1, 1), b3 + hstepB, voffB); PG8_STAGEA(PG8_SA(1, 0), k3, 0, last);
;             PG8_WAIT_V(8); PG8_WAIT_L(0); PG8_BAR; PG8_MMA(1, 0, At, B0); PG8_MMA(1, 1, At, B1); PG8_BAR; PG8_SCHED;
;         }
;         if (wr == 0) PG8_BAR;
	s_nop 4
	ds_read_b128 v[2:5], v162 offset:32768
	ds_read_b128 v[6:9], v162 offset:33792
	ds_read_b128 v[10:13], v162 offset:34816
	ds_read_b128 v[14:17], v162 offset:35840
	ds_read_b128 v[130:133], v162 offset:49152
	ds_read_b128 v[134:137], v162 offset:50176
	ds_read_b128 v[138:141], v162 offset:51200
	ds_read_b128 v[142:145], v162 offset:52224
	s_add_i32 s62, s25, 0x20000
	s_add_u32 s62, s6, s62
	s_addc_u32 s63, s7, 0
	s_mov_b32 m0, s41
	v_lshl_add_u64 v[66:67], s[62:63], 0, v[148:149]
	ds_read_b128 v[18:21], v161 offset:32768
	ds_read_b128 v[22:25], v161 offset:33792
	ds_read_b128 v[26:29], v161 offset:34816
	ds_read_b128 v[30:33], v161 offset:35840
	ds_read_b128 v[34:37], v161 offset:36864
	ds_read_b128 v[38:41], v161 offset:37888
	ds_read_b128 v[42:45], v161 offset:38912
	ds_read_b128 v[46:49], v161 offset:39936
	global_load_lds_dwordx4 v[66:67], off
	v_lshl_add_u64 v[66:67], s[62:63], 0, v[146:147]
	s_mov_b32 m0, s42
	s_nop 0
	global_load_lds_dwordx4 v[66:67], off
	s_waitcnt vmcnt(8)
	s_waitcnt lgkmcnt(0)
	s_barrier
	s_setprio 1
	v_mfma_f32_16x16x128_f8f6f4 v[126:129], v[2:9], v[18:25], v[126:129]
	v_mfma_f32_16x16x128_f8f6f4 v[122:125], v[10:17], v[18:25], v[122:125]
	v_mfma_f32_16x16x128_f8f6f4 v[118:121], v[2:9], v[26:33], v[118:121]
	v_mfma_f32_16x16x128_f8f6f4 v[114:117], v[10:17], v[26:33], v[114:117]
	v_mfma_f32_16x16x128_f8f6f4 v[102:105], v[2:9], v[34:41], v[102:105]
	v_mfma_f32_16x16x128_f8f6f4 v[98:101], v[10:17], v[34:41], v[98:101]
	v_mfma_f32_16x16x128_f8f6f4 v[86:89], v[2:9], v[42:49], v[204:207]
	v_mfma_f32_16x16x128_f8f6f4 v[78:81], v[10:17], v[42:49], v[208:211]
	s_setprio 0
	s_setprio 1
	v_mfma_f32_16x16x128_f8f6f4 v[110:113], v[130:137], v[18:25], v[110:113]
	v_mfma_f32_16x16x128_f8f6f4 v[106:109], v[138:145], v[18:25], v[106:109]
	v_mfma_f32_16x16x128_f8f6f4 v[94:97], v[130:137], v[26:33], v[172:175]
	v_mfma_f32_16x16x128_f8f6f4 v[90:93], v[138:145], v[26:33], v[176:179]
	v_mfma_f32_16x16x128_f8f6f4 v[82:85], v[130:137], v[34:41], v[180:183]
	v_mfma_f32_16x16x128_f8f6f4 v[74:77], v[138:145], v[34:41], v[184:187]
	v_mfma_f32_16x16x128_f8f6f4 v[70:73], v[130:137], v[42:49], v[188:191]
	v_mfma_f32_16x16x128_f8f6f4 v[66:69], v[138:145], v[42:49], v[192:195]
	s_setprio 0
	s_barrier
	s_add_u32 s62, s6, s61
	s_addc_u32 s63, s7, 0
	s_mov_b32 m0, s46
	v_lshl_add_u64 v[18:19], s[62:63], 0, v[148:149]
	s_add_i32 s24, s24, 0x20080
	ds_read_b128 v[150:153], v161 offset:49152
	ds_read_b128 v[154:157], v161 offset:50176
	ds_read_b128 v[164:167], v161 offset:51200
	ds_read_b128 v[168:171], v161 offset:52224
	ds_read_b128 v[172:175], v161 offset:53248
	ds_read_b128 v[176:179], v161 offset:54272
	ds_read_b128 v[180:183], v161 offset:55296
	ds_read_b128 v[184:187], v161 offset:56320
	global_load_lds_dwordx4 v[18:19], off
	v_lshl_add_u64 v[18:19], s[62:63], 0, v[146:147]
	s_add_u32 s62, s6, s24
	s_mov_b32 m0, s47
	s_addc_u32 s63, s7, 0
	s_addk_i32 s25, 0x80
	global_load_lds_dwordx4 v[18:19], off
	v_lshl_add_u64 v[18:19], s[62:63], 0, v[148:149]
	s_mov_b32 m0, s50
	s_add_u32 s24, s6, s25
	global_load_lds_dwordx4 v[18:19], off
	v_lshl_add_u64 v[18:19], s[62:63], 0, v[146:147]
	s_mov_b32 m0, s51
	s_addc_u32 s25, s7, 0
	global_load_lds_dwordx4 v[18:19], off
	v_lshl_add_u64 v[18:19], s[24:25], 0, v[148:149]
	s_mov_b32 m0, s48
	s_nop 0
	global_load_lds_dwordx4 v[18:19], off
	v_lshl_add_u64 v[18:19], s[24:25], 0, v[146:147]
	s_mov_b32 m0, s49
	s_nop 0
	global_load_lds_dwordx4 v[18:19], off
	s_waitcnt vmcnt(8)
	s_waitcnt lgkmcnt(0)
	s_barrier
	s_setprio 1
	v_mfma_f32_16x16x128_f8f6f4 v[62:65], v[2:9], v[150:157], v[62:65]
	v_mfma_f32_16x16x128_f8f6f4 v[58:61], v[10:17], v[150:157], v[58:61]
	v_mfma_f32_16x16x128_f8f6f4 v[50:53], v[2:9], v[164:171], v[50:53]
	v_mfma_f32_16x16x128_f8f6f4 v[42:45], v[10:17], v[164:171], v[196:199]
	v_mfma_f32_16x16x128_f8f6f4 v[38:41], v[2:9], v[172:179], v[200:203]
	v_mfma_f32_16x16x128_f8f6f4 v[30:33], v[10:17], v[172:179], v[212:215]
	v_mfma_f32_16x16x128_f8f6f4 v[22:25], v[2:9], v[180:187], v[216:219]
	v_mfma_f32_16x16x128_f8f6f4 v[14:17], v[10:17], v[180:187], v[220:223]
	s_setprio 0
	s_setprio 1
	v_mfma_f32_16x16x128_f8f6f4 v[54:57], v[130:137], v[150:157], v[54:57]
	v_mfma_f32_16x16x128_f8f6f4 v[46:49], v[138:145], v[150:157], v[224:227]
	v_mfma_f32_16x16x128_f8f6f4 v[34:37], v[130:137], v[164:171], v[228:231]
	v_mfma_f32_16x16x128_f8f6f4 v[26:29], v[138:145], v[164:171], v[232:235]
	v_mfma_f32_16x16x128_f8f6f4 v[18:21], v[130:137], v[172:179], v[236:239]
	v_mfma_f32_16x16x128_f8f6f4 v[10:13], v[138:145], v[172:179], v[240:243]
	v_mfma_f32_16x16x128_f8f6f4 v[6:9], v[130:137], v[180:187], v[244:247]
	v_mfma_f32_16x16x128_f8f6f4 v[2:5], v[138:145], v[180:187], v[248:251]
	s_setprio 0
	s_barrier
	s_add_i32 s23, s23, 2
	s_addk_i32 s21, 0x100
	s_addk_i32 s22, 0x100
	s_cmp_gt_u32 s23, 5
	s_cbranch_scc0 .LBB0_910
	s_and_b64 vcc, exec, s[10:11]
	s_cbranch_vccz .LBB0_913
	s_barrier

; #define PG8_STAGE(bufoff, gbase, voff) do { _Pragma("unroll") for (int _i = 0; _i < 2; ++_i) \
;         __builtin_amdgcn_global_load_lds((const unsigned*)(wsb + (size_t)(gbase) + (voff)[_i]), (LAS unsigned*)(lds + (bufoff) + ldsw + _i * 8192), 16, 0, 0); } while (0)
; #define PG8_WAIT_V(n) asm volatile("s_waitcnt vmcnt(" #n ")" ::: "memory")
; #define PG8_WAIT_L(n) asm volatile("s_waitcnt lgkmcnt(" #n ")" ::: "memory")
; template <class Epi, class Sched, bool PERM, bool FP8 = false, bool GATHER = false>
; DI void gemm_phase(LAS unsigned char* lds, const unsigned char* wsb, const unsigned lda, const unsigned ldb, const int nt, const Sched& S, const Epi& E) {
;     ...
;         for (int t = 0; t < nt; t += 2) {
;             const bool last = (t == nt - 2);
;             const unsigned b2 = last ? nB : cB + (unsigned)(t + 2) * kstep, b3 = b2 + kstep;
;             const int k2 = last ? 0 : t + 2, k3 = k2 + 1;
;             PG8_LDB(B0, 0, 0); PG8_LDB(B1, 0, 1); PG8_SCHED; PG8_LDA(At, 0, 0); PG8_STAGEA(PG8_SA(1, 1), t + 1, 1, false);
;             if constexpr (GATHER) { if (last) {
;                 int tz = tid; asm volatile("" : "+v"(tz));
; #pragma unroll
;                 for (int i = 0; i < 2; ++i) { int R, C; stage_rc(tz * 16 + i * 8192, R, C);
; #pragma unroll
;                     for (int h = 0; h < 2; ++h) { const unsigned tk = (unsigned)tokt[h * HALF + R]; offC[h][i] = (tk < (unsigned)NTOK ? tk : (unsigned)(NTOK - 1)) * lda + (unsigned)C * 2u; } } } }
;             PG8_WAIT_V(8); PG8_WAIT_L(0); PG8_BAR; PG8_MMA(0, 0, At, B0); PG8_MMA(0, 1, At, B1); PG8_BAR; PG8_SCHED;
;             PG8_LDA(At, 0, 1); PG8_STAGE(PG8_SB(0, 0), b2, voffB); PG8_STAGE(PG8_SB(0, 1), b2 + hstepB, voffB); PG8_STAGEA(PG8_SA(0, 0), k2, 0, last);
;             PG8_WAIT_V(8); PG8_WAIT_L(0); PG8_BAR; PG8_MMA(1, 0, At, B0); PG8_MMA(1, 1, At, B1); PG8_BAR; PG8_SCHED;
;             PG8_LDB(B0, 1, 0); PG8_LDB(B1, 1, 1); PG8_SCHED; PG8_LDA(At, 1, 0); PG8_STAGEA(PG8_SA(0, 1), k2, 1, last);
;             PG8_WAIT_V(8); PG8_WAIT_L(0); PG8_BAR; PG8_MMA(0, 0, At, B0); PG8_MMA(0, 1, At, B1); PG8_BAR; PG8_SCHED;
;             PG8_LDA(At, 1, 1); PG8_STAGE(PG8_SB(1, 0), b3, voffB); PG8_STAGE(PG8_SB(1, 1), b3 + hstepB, voffB); PG8_STAGEA(PG8_SA(1, 0), k3, 0, last);
;             PG8_WAIT_V(8); PG8_WAIT_L(0); PG8_BAR; PG8_MMA(1, 0, At, B0); PG8_MMA(1, 1, At, B1); PG8_BAR; PG8_SCHED;
.LBB0_1342:
	s_waitcnt vmcnt(8)
	s_add_i32 s85, s83, s50
	s_waitcnt lgkmcnt(0)
	s_and_b64 s[86:87], s[52:53], exec
	s_cselect_b32 s85, s14, s85
	v_mov_b32_e32 v205, v197
	s_add_i32 s86, s85, 0x80
	s_barrier
	s_setprio 1
	v_mfma_f32_16x16x128_f8f6f4 v[190:193], v[18:25], v[58:65], v[190:193]
	v_mfma_f32_16x16x128_f8f6f4 v[186:189], v[26:33], v[58:65], v[186:189]
	v_mfma_f32_16x16x128_f8f6f4 v[174:177], v[18:25], v[50:57], v[174:177]
	v_mfma_f32_16x16x128_f8f6f4 v[166:169], v[26:33], v[50:57], v[166:169]
	v_mfma_f32_16x16x128_f8f6f4 v[158:161], v[18:25], v[42:49], v[158:161]
	v_mfma_f32_16x16x128_f8f6f4 v[150:153], v[26:33], v[42:49], v[150:153]
	v_mfma_f32_16x16x128_f8f6f4 v[142:145], v[18:25], v[34:41], v[142:145]
	v_mfma_f32_16x16x128_f8f6f4 v[134:137], v[26:33], v[34:41], v[134:137]
	s_setprio 0
	s_setprio 1
	v_mfma_f32_16x16x128_f8f6f4 v[182:185], v[2:9], v[58:65], v[182:185]
	v_mfma_f32_16x16x128_f8f6f4 v[178:181], v[10:17], v[58:65], v[178:181]
	v_mfma_f32_16x16x128_f8f6f4 v[170:173], v[2:9], v[50:57], v[170:173]
	v_mfma_f32_16x16x128_f8f6f4 v[162:165], v[10:17], v[50:57], v[162:165]
	v_mfma_f32_16x16x128_f8f6f4 v[154:157], v[2:9], v[42:49], v[154:157]
	v_mfma_f32_16x16x128_f8f6f4 v[146:149], v[10:17], v[42:49], v[146:149]
	v_mfma_f32_16x16x128_f8f6f4 v[138:141], v[2:9], v[34:41], v[138:141]
	v_mfma_f32_16x16x128_f8f6f4 v[130:133], v[10:17], v[34:41], v[130:133]
	s_setprio 0
	s_barrier
	s_add_u32 s88, s10, s85
	s_addc_u32 s89, s11, 0
	s_mov_b32 m0, s41
	v_lshl_add_u64 v[214:215], s[88:89], 0, v[198:199]
	s_add_i32 s87, s85, 0x20000
	ds_read_b128 v[34:37], v209 offset:16384
	ds_read_b128 v[38:41], v209 offset:17408
	ds_read_b128 v[42:45], v209 offset:18432
	ds_read_b128 v[46:49], v209 offset:19456
	ds_read_b128 v[50:53], v209 offset:20480
	ds_read_b128 v[54:57], v209 offset:21504
	ds_read_b128 v[58:61], v209 offset:22528
	ds_read_b128 v[62:65], v209 offset:23552
	global_load_lds_dwordx4 v[214:215], off
	v_lshl_add_u64 v[214:215], s[88:89], 0, v[200:201]
	s_add_u32 s88, s10, s87
	s_addc_u32 s89, s11, 0
	s_add_u32 s50, s50, 0x100
	s_addc_u32 s51, s51, 0
	s_mov_b32 m0, s46
	s_and_b64 s[52:53], s[52:53], exec
	global_load_lds_dwordx4 v[214:215], off
	v_lshl_add_u64 v[214:215], s[88:89], 0, v[198:199]
	s_mov_b32 m0, s47
	s_cselect_b32 s87, 0, s50
	global_load_lds_dwordx4 v[214:215], off
	v_lshl_add_u64 v[214:215], s[88:89], 0, v[200:201]
	s_mov_b32 m0, s54
	s_add_u32 s52, s12, s87
	global_load_lds_dwordx4 v[214:215], off
	s_addc_u32 s53, s13, 0
	s_mov_b32 m0, s39
	s_nop 0
	global_load_lds_dwordx4 v212, s[52:53]
	s_mov_b32 m0, s55
	s_nop 0
	global_load_lds_dwordx4 v202, s[52:53]
	s_waitcnt vmcnt(8)
	s_waitcnt lgkmcnt(0)
	s_barrier
	s_setprio 1
	v_mfma_f32_16x16x128_f8f6f4 v[126:129], v[18:25], v[34:41], v[126:129]
	v_mfma_f32_16x16x128_f8f6f4 v[118:121], v[26:33], v[34:41], v[118:121]
	v_mfma_f32_16x16x128_f8f6f4 v[110:113], v[18:25], v[42:49], v[110:113]
	v_mfma_f32_16x16x128_f8f6f4 v[102:105], v[26:33], v[42:49], v[102:105]
	v_mfma_f32_16x16x128_f8f6f4 v[94:97], v[18:25], v[50:57], v[94:97]
	v_mfma_f32_16x16x128_f8f6f4 v[86:89], v[26:33], v[50:57], v[86:89]
	v_mfma_f32_16x16x128_f8f6f4 v[78:81], v[18:25], v[58:65], v[78:81]
	v_mfma_f32_16x16x128_f8f6f4 v[70:73], v[26:33], v[58:65], v[70:73]
	s_setprio 0
	s_setprio 1
	v_mfma_f32_16x16x128_f8f6f4 v[122:125], v[2:9], v[34:41], v[122:125]
	v_mfma_f32_16x16x128_f8f6f4 v[114:117], v[10:17], v[34:41], v[114:117]
	v_mfma_f32_16x16x128_f8f6f4 v[106:109], v[2:9], v[42:49], v[106:109]
	v_mfma_f32_16x16x128_f8f6f4 v[98:101], v[10:17], v[42:49], v[98:101]
	v_mfma_f32_16x16x128_f8f6f4 v[90:93], v[2:9], v[50:57], v[90:93]
	v_mfma_f32_16x16x128_f8f6f4 v[82:85], v[10:17], v[50:57], v[82:85]
	v_mfma_f32_16x16x128_f8f6f4 v[74:77], v[2:9], v[58:65], v[74:77]
	v_mfma_f32_16x16x128_f8f6f4 v[66:69], v[10:17], v[58:65], v[66:69]
	s_setprio 0
	s_barrier
; #define PG8_STAGE(bufoff, gbase, voff) do { _Pragma("unroll") for (int _i = 0; _i < 2; ++_i) \
;         __builtin_amdgcn_global_load_lds((const unsigned*)(wsb + (size_t)(gbase) + (voff)[_i]), (LAS unsigned*)(lds + (bufoff) + ldsw + _i * 8192), 16, 0, 0); } while (0)
; #define PG8_WAIT_V(n) asm volatile("s_waitcnt vmcnt(" #n ")" ::: "memory")
; #define PG8_BAR __builtin_amdgcn_s_barrier()
; template <class Epi, class Sched, bool PERM, bool FP8 = false, bool GATHER = false>
; DI void gemm_phase(LAS unsigned char* lds, const unsigned char* wsb, const unsigned lda, const unsigned ldb, const int nt, const Sched& S, const Epi& E) {
;     ...
;         for (int t = 0; t < nt; t += 2) {
;             const bool last = (t == nt - 2);
;             const unsigned b2 = last ? nB : cB + (unsigned)(t + 2) * kstep, b3 = b2 + kstep;
;             const int k2 = last ? 0 : t + 2, k3 = k2 + 1;
;             PG8_LDB(B0, 0, 0); PG8_LDB(B1, 0, 1); PG8_SCHED; PG8_LDA(At, 0, 0); PG8_STAGEA(PG8_SA(1, 1), t + 1, 1, false);
;             if constexpr (GATHER) { if (last) {
;                 int tz = tid; asm volatile("" : "+v"(tz));
; #pragma unroll
;                 for (int i = 0; i < 2; ++i) { int R, C; stage_rc(tz * 16 + i * 8192, R, C);
; #pragma unroll
;                     for (int h = 0; h < 2; ++h) { const unsigned tk = (unsigned)tokt[h * HALF + R]; offC[h][i] = (tk < (unsigned)NTOK ? tk : (unsigned)(NTOK - 1)) * lda + (unsigned)C * 2u; } } } }
;             PG8_WAIT_V(8); PG8_WAIT_L(0); PG8_BAR; PG8_MMA(0, 0, At, B0); PG8_MMA(0, 1, At, B1); PG8_BAR; PG8_SCHED;
;             PG8_LDA(At, 0, 1); PG8_STAGE(PG8_SB(0, 0), b2, voffB); PG8_STAGE(PG8_SB(0, 1), b2 + hstepB, voffB); PG8_STAGEA(PG8_SA(0, 0), k2, 0, last);
;             PG8_WAIT_V(8); PG8_WAIT_L(0); PG8_BAR; PG8_MMA(1, 0, At, B0); PG8_MMA(1, 1, At, B1); PG8_BAR; PG8_SCHED;
;             PG8_LDB(B0, 1, 0); PG8_LDB(B1, 1, 1); PG8_SCHED; PG8_LDA(At, 1, 0); PG8_STAGEA(PG8_SA(0, 1), k2, 1, last);
;             PG8_WAIT_V(8); PG8_WAIT_L(0); PG8_BAR; PG8_MMA(0, 0, At, B0); PG8_MMA(0, 1, At, B1); PG8_BAR; PG8_SCHED;
;             PG8_LDA(At, 1, 1); PG8_STAGE(PG8_SB(1, 0), b3, voffB); PG8_STAGE(PG8_SB(1, 1), b3 + hstepB, voffB); PG8_STAGEA(PG8_SA(1, 0), k3, 0, last);
;             PG8_WAIT_V(8); PG8_WAIT_L(0); PG8_BAR; PG8_MMA(1, 0, At, B0); PG8_MMA(1, 1, At, B1); PG8_BAR; PG8_SCHED;
;         }
;         if (wr == 0) PG8_BAR;
	ds_read_b128 v[2:5], v210 offset:32768
	ds_read_b128 v[6:9], v210 offset:33792
	ds_read_b128 v[10:13], v210 offset:34816
	ds_read_b128 v[14:17], v210 offset:35840
	ds_read_b128 v[18:21], v210 offset:49152
	ds_read_b128 v[22:25], v210 offset:50176
	ds_read_b128 v[26:29], v210 offset:51200
	ds_read_b128 v[30:33], v210 offset:52224
	s_mov_b32 m0, s56
	v_lshl_add_u64 v[214:215], s[52:53], 0, v[196:197]
	ds_read_b128 v[34:37], v209 offset:32768
	ds_read_b128 v[38:41], v209 offset:33792
	ds_read_b128 v[42:45], v209 offset:34816
	ds_read_b128 v[46:49], v209 offset:35840
	ds_read_b128 v[50:53], v209 offset:36864
	ds_read_b128 v[54:57], v209 offset:37888
	ds_read_b128 v[58:61], v209 offset:38912
	ds_read_b128 v[62:65], v209 offset:39936
	global_load_lds_dwordx4 v[214:215], off
	v_lshl_add_u64 v[214:215], s[52:53], 0, v[204:205]
	s_mov_b32 m0, s57
	s_nop 0
	global_load_lds_dwordx4 v[214:215], off
	s_waitcnt vmcnt(8)
	s_waitcnt lgkmcnt(0)
	s_barrier
	s_setprio 1
	v_mfma_f32_16x16x128_f8f6f4 v[190:193], v[2:9], v[34:41], v[190:193]
	v_mfma_f32_16x16x128_f8f6f4 v[186:189], v[10:17], v[34:41], v[186:189]
	v_mfma_f32_16x16x128_f8f6f4 v[174:177], v[2:9], v[42:49], v[174:177]
	v_mfma_f32_16x16x128_f8f6f4 v[166:169], v[10:17], v[42:49], v[166:169]
	v_mfma_f32_16x16x128_f8f6f4 v[158:161], v[2:9], v[50:57], v[158:161]
	v_mfma_f32_16x16x128_f8f6f4 v[150:153], v[10:17], v[50:57], v[150:153]
	v_mfma_f32_16x16x128_f8f6f4 v[142:145], v[2:9], v[58:65], v[142:145]
	v_mfma_f32_16x16x128_f8f6f4 v[134:137], v[10:17], v[58:65], v[134:137]
	s_setprio 0
	s_setprio 1
	v_mfma_f32_16x16x128_f8f6f4 v[182:185], v[18:25], v[34:41], v[182:185]
	v_mfma_f32_16x16x128_f8f6f4 v[178:181], v[26:33], v[34:41], v[178:181]
	v_mfma_f32_16x16x128_f8f6f4 v[170:173], v[18:25], v[42:49], v[170:173]
	v_mfma_f32_16x16x128_f8f6f4 v[162:165], v[26:33], v[42:49], v[162:165]
	v_mfma_f32_16x16x128_f8f6f4 v[154:157], v[18:25], v[50:57], v[154:157]
	v_mfma_f32_16x16x128_f8f6f4 v[146:149], v[26:33], v[50:57], v[146:149]
	v_mfma_f32_16x16x128_f8f6f4 v[138:141], v[18:25], v[58:65], v[138:141]
	v_mfma_f32_16x16x128_f8f6f4 v[130:133], v[26:33], v[58:65], v[130:133]
	s_setprio 0
	s_barrier
	s_add_u32 s52, s10, s86
	s_addc_u32 s53, s11, 0
	s_mov_b32 m0, s61
	v_lshl_add_u64 v[214:215], s[52:53], 0, v[198:199]
	s_add_i32 s85, s85, 0x20080
	ds_read_b128 v[34:37], v209 offset:49152
	ds_read_b128 v[38:41], v209 offset:50176
	ds_read_b128 v[42:45], v209 offset:51200
	ds_read_b128 v[46:49], v209 offset:52224
	ds_read_b128 v[50:53], v209 offset:53248
	ds_read_b128 v[54:57], v209 offset:54272
	ds_read_b128 v[58:61], v209 offset:55296
	ds_read_b128 v[62:65], v209 offset:56320
	global_load_lds_dwordx4 v[214:215], off
	v_lshl_add_u64 v[214:215], s[52:53], 0, v[200:201]
	s_add_u32 s52, s10, s85
	s_mov_b32 m0, s63
	s_addc_u32 s53, s11, 0
	global_load_lds_dwordx4 v[214:215], off
	v_lshl_add_u64 v[214:215], s[52:53], 0, v[198:199]
	s_mov_b32 m0, s66
	s_nop 0
	global_load_lds_dwordx4 v[214:215], off
	v_lshl_add_u64 v[214:215], s[52:53], 0, v[200:201]
	s_add_u32 s52, s10, s87
	s_addc_u32 s53, s11, 0
	s_mov_b32 m0, s67
	s_add_u32 s52, s52, 0x5b9d4080
	global_load_lds_dwordx4 v[214:215], off
	s_addc_u32 s53, s53, 0
	s_mov_b32 m0, s64
	s_nop 0
	global_load_lds_dwordx4 v212, s[52:53]
	s_mov_b32 m0, s65
	s_nop 0
	global_load_lds_dwordx4 v202, s[52:53]
	s_waitcnt vmcnt(8)
	s_waitcnt lgkmcnt(0)
	s_barrier
	s_setprio 1
	v_mfma_f32_16x16x128_f8f6f4 v[126:129], v[2:9], v[34:41], v[126:129]
	v_mfma_f32_16x16x128_f8f6f4 v[118:121], v[10:17], v[34:41], v[118:121]
	v_mfma_f32_16x16x128_f8f6f4 v[110:113], v[2:9], v[42:49], v[110:113]
	v_mfma_f32_16x16x128_f8f6f4 v[102:105], v[10:17], v[42:49], v[102:105]
	v_mfma_f32_16x16x128_f8f6f4 v[94:97], v[2:9], v[50:57], v[94:97]
	v_mfma_f32_16x16x128_f8f6f4 v[86:89], v[10:17], v[50:57], v[86:89]
	v_mfma_f32_16x16x128_f8f6f4 v[78:81], v[2:9], v[58:65], v[78:81]
	v_mfma_f32_16x16x128_f8f6f4 v[70:73], v[10:17], v[58:65], v[70:73]
	s_setprio 0
	s_setprio 1
	v_mfma_f32_16x16x128_f8f6f4 v[122:125], v[18:25], v[34:41], v[122:125]
	v_mfma_f32_16x16x128_f8f6f4 v[114:117], v[26:33], v[34:41], v[114:117]
	v_mfma_f32_16x16x128_f8f6f4 v[106:109], v[18:25], v[42:49], v[106:109]
	v_mfma_f32_16x16x128_f8f6f4 v[98:101], v[26:33], v[42:49], v[98:101]
	v_mfma_f32_16x16x128_f8f6f4 v[90:93], v[18:25], v[50:57], v[90:93]
	v_mfma_f32_16x16x128_f8f6f4 v[82:85], v[26:33], v[50:57], v[82:85]
	v_mfma_f32_16x16x128_f8f6f4 v[74:77], v[18:25], v[58:65], v[74:77]
	v_mfma_f32_16x16x128_f8f6f4 v[66:69], v[26:33], v[58:65], v[66:69]
	s_setprio 0
	s_barrier
	s_add_i32 s84, s84, 2
	s_cmp_gt_u32 s84, 5
	s_cbranch_scc1 .LBB0_1345

; #define PG8_STAGE(bufoff, gbase, voff) do { _Pragma("unroll") for (int _i = 0; _i < 2; ++_i) \
;         __builtin_amdgcn_global_load_lds((const unsigned*)(wsb + (size_t)(gbase) + (voff)[_i]), (LAS unsigned*)(lds + (bufoff) + ldsw + _i * 8192), 16, 0, 0); } while (0)
; #define PG8_WAIT_V(n) asm volatile("s_waitcnt vmcnt(" #n ")" ::: "memory")
; #define PG8_WAIT_L(n) asm volatile("s_waitcnt lgkmcnt(" #n ")" ::: "memory")
; template <class Epi, class Sched, bool PERM, bool FP8 = false, bool GATHER = false>
; DI void gemm_phase(LAS unsigned char* lds, const unsigned char* wsb, const unsigned lda, const unsigned ldb, const int nt, const Sched& S, const Epi& E) {
;     ...
;         for (int t = 0; t < nt; t += 2) {
;             const bool last = (t == nt - 2);
;             const unsigned b2 = last ? nB : cB + (unsigned)(t + 2) * kstep, b3 = b2 + kstep;
;             const int k2 = last ? 0 : t + 2, k3 = k2 + 1;
;             PG8_LDB(B0, 0, 0); PG8_LDB(B1, 0, 1); PG8_SCHED; PG8_LDA(At, 0, 0); PG8_STAGEA(PG8_SA(1, 1), t + 1, 1, false);
;             if constexpr (GATHER) { if (last) {
;                 int tz = tid; asm volatile("" : "+v"(tz));
; #pragma unroll
;                 for (int i = 0; i < 2; ++i) { int R, C; stage_rc(tz * 16 + i * 8192, R, C);
; #pragma unroll
;                     for (int h = 0; h < 2; ++h) { const unsigned tk = (unsigned)tokt[h * HALF + R]; offC[h][i] = (tk < (unsigned)NTOK ? tk : (unsigned)(NTOK - 1)) * lda + (unsigned)C * 2u; } } } }
;             PG8_WAIT_V(8); PG8_WAIT_L(0); PG8_BAR; PG8_MMA(0, 0, At, B0); PG8_MMA(0, 1, At, B1); PG8_BAR; PG8_SCHED;
;             PG8_LDA(At, 0, 1); PG8_STAGE(PG8_SB(0, 0), b2, voffB); PG8_STAGE(PG8_SB(0, 1), b2 + hstepB, voffB); PG8_STAGEA(PG8_SA(0, 0), k2, 0, last);
;             PG8_WAIT_V(8); PG8_WAIT_L(0); PG8_BAR; PG8_MMA(1, 0, At, B0); PG8_MMA(1, 1, At, B1); PG8_BAR; PG8_SCHED;
;             PG8_LDB(B0, 1, 0); PG8_LDB(B1, 1, 1); PG8_SCHED; PG8_LDA(At, 1, 0); PG8_STAGEA(PG8_SA(0, 1), k2, 1, last);
;             PG8_WAIT_V(8); PG8_WAIT_L(0); PG8_BAR; PG8_MMA(0, 0, At, B0); PG8_MMA(0, 1, At, B1); PG8_BAR; PG8_SCHED;
;             PG8_LDA(At, 1, 1); PG8_STAGE(PG8_SB(1, 0), b3, voffB); PG8_STAGE(PG8_SB(1, 1), b3 + hstepB, voffB); PG8_STAGEA(PG8_SA(1, 0), k3, 0, last);
;             PG8_WAIT_V(8); PG8_WAIT_L(0); PG8_BAR; PG8_MMA(1, 0, At, B0); PG8_MMA(1, 1, At, B1); PG8_BAR; PG8_SCHED;
.LBB0_1450:
	ds_read_b128 v[130:133], v154
	ds_read_b128 v[134:137], v154 offset:1024
	ds_read_b128 v[138:141], v154 offset:2048
	ds_read_b128 v[142:145], v154 offset:3072
	ds_read_b128 v[158:161], v154 offset:16384
	ds_read_b128 v[162:165], v154 offset:17408
	ds_read_b128 v[166:169], v154 offset:18432
	ds_read_b128 v[170:173], v154 offset:19456
	s_add_i32 s74, s71, 0xfffe0080
	s_add_i32 s75, s74, s68
	s_cmp_eq_u32 s70, 4
	s_cselect_b64 s[24:25], -1, 0
	s_and_b64 s[72:73], s[24:25], exec
	s_cselect_b32 s72, s69, s75
	s_cselect_b32 s76, 0, s74
	s_add_i32 s73, s72, 0x80
	s_add_i32 s74, s67, s71
	s_add_u32 s74, s10, s74
	s_addc_u32 s75, s11, 0
	v_lshl_add_u64 v[150:151], s[74:75], 0, v[146:147]
	s_add_i32 m0, s5, 0xc000
	ds_read_b128 v[174:177], v153
	ds_read_b128 v[178:181], v153 offset:1024
	ds_read_b128 v[182:185], v153 offset:2048
	ds_read_b128 v[186:189], v153 offset:3072
	ds_read_b128 v[190:193], v153 offset:4096
	ds_read_b128 v[194:197], v153 offset:5120
	ds_read_b128 v[198:201], v153 offset:6144
	ds_read_b128 v[202:205], v153 offset:7168
	global_load_lds_dwordx4 v[150:151], off
	v_lshl_add_u64 v[150:151], s[74:75], 0, v[148:149]
	s_add_i32 m0, s5, 0xe000
	s_nop 0
	global_load_lds_dwordx4 v[150:151], off
	s_waitcnt vmcnt(8)
	s_waitcnt lgkmcnt(0)
	s_barrier
	s_setprio 1
	v_mfma_f32_16x16x128_f8f6f4 v[126:129], v[130:137], v[174:181], v[126:129]
	v_mfma_f32_16x16x128_f8f6f4 v[122:125], v[138:145], v[174:181], v[122:125]
	v_mfma_f32_16x16x128_f8f6f4 v[118:121], v[130:137], v[182:189], v[118:121]
	v_mfma_f32_16x16x128_f8f6f4 v[114:117], v[138:145], v[182:189], v[114:117]
	v_mfma_f32_16x16x128_f8f6f4 v[206:209], v[130:137], v[190:197], v[94:97]
	v_mfma_f32_16x16x128_f8f6f4 v[210:213], v[138:145], v[190:197], v[90:93]
	v_mfma_f32_16x16x128_f8f6f4 v[214:217], v[130:137], v[198:205], v[82:85]
	v_mfma_f32_16x16x128_f8f6f4 v[218:221], v[138:145], v[198:205], v[74:77]
	s_setprio 0
	s_setprio 1
	v_mfma_f32_16x16x128_f8f6f4 v[110:113], v[158:165], v[174:181], v[110:113]
	v_mfma_f32_16x16x128_f8f6f4 v[106:109], v[166:173], v[174:181], v[106:109]
	v_mfma_f32_16x16x128_f8f6f4 v[102:105], v[158:165], v[182:189], v[102:105]
	v_mfma_f32_16x16x128_f8f6f4 v[98:101], v[166:173], v[182:189], v[98:101]
	v_mfma_f32_16x16x128_f8f6f4 v[174:177], v[158:165], v[190:197], v[86:89]
	v_mfma_f32_16x16x128_f8f6f4 v[178:181], v[166:173], v[190:197], v[78:81]
	v_mfma_f32_16x16x128_f8f6f4 v[182:185], v[158:165], v[198:205], v[70:73]
	v_mfma_f32_16x16x128_f8f6f4 v[186:189], v[166:173], v[198:205], v[66:69]
	s_setprio 0
	s_barrier
	s_add_u32 s74, s10, s72
	s_addc_u32 s75, s11, 0
	s_mov_b32 m0, s19
	v_lshl_add_u64 v[150:151], s[74:75], 0, v[146:147]
	s_nop 0
	ds_read_b128 v[66:69], v153 offset:16384
	ds_read_b128 v[70:73], v153 offset:17408
	ds_read_b128 v[74:77], v153 offset:18432
	ds_read_b128 v[78:81], v153 offset:19456
	ds_read_b128 v[82:85], v153 offset:20480
	ds_read_b128 v[86:89], v153 offset:21504
	ds_read_b128 v[90:93], v153 offset:22528
	ds_read_b128 v[94:97], v153 offset:23552
	global_load_lds_dwordx4 v[150:151], off
	v_lshl_add_u64 v[150:151], s[74:75], 0, v[148:149]
	s_add_i32 s74, s72, 0x20000
	s_add_u32 s74, s10, s74
	s_addc_u32 s75, s11, 0
	s_and_b64 s[24:25], s[20:21], s[24:25]
	s_and_b64 s[24:25], s[24:25], exec
	s_mov_b32 m0, s28
	s_cselect_b32 s24, s60, s67
	global_load_lds_dwordx4 v[150:151], off
	v_lshl_add_u64 v[150:151], s[74:75], 0, v[146:147]
	s_mov_b32 m0, s29
	s_add_i32 s24, s76, s24
	global_load_lds_dwordx4 v[150:151], off
	v_lshl_add_u64 v[150:151], s[74:75], 0, v[148:149]
	s_add_u32 s74, s10, s24
	s_mov_b32 m0, s36
	s_addc_u32 s75, s11, 0
	global_load_lds_dwordx4 v[150:151], off
	v_lshl_add_u64 v[150:151], s[74:75], 0, v[146:147]
	s_mov_b32 m0, s5
	s_nop 0
	global_load_lds_dwordx4 v[150:151], off
	v_lshl_add_u64 v[150:151], s[74:75], 0, v[148:149]
	s_mov_b32 m0, s37
	s_nop 0
	global_load_lds_dwordx4 v[150:151], off
	s_waitcnt vmcnt(8)
	s_waitcnt lgkmcnt(0)
	s_barrier
	s_setprio 1
	v_mfma_f32_16x16x128_f8f6f4 v[62:65], v[130:137], v[66:73], v[62:65]
	v_mfma_f32_16x16x128_f8f6f4 v[58:61], v[138:145], v[66:73], v[58:61]
	v_mfma_f32_16x16x128_f8f6f4 v[50:53], v[130:137], v[74:81], v[50:53]
	v_mfma_f32_16x16x128_f8f6f4 v[190:193], v[138:145], v[74:81], v[42:45]
	v_mfma_f32_16x16x128_f8f6f4 v[194:197], v[130:137], v[82:89], v[34:37]
	v_mfma_f32_16x16x128_f8f6f4 v[198:201], v[138:145], v[82:89], v[26:29]
	v_mfma_f32_16x16x128_f8f6f4 v[202:205], v[130:137], v[90:97], v[18:21]
	v_mfma_f32_16x16x128_f8f6f4 v[222:225], v[138:145], v[90:97], v[10:13]
	s_setprio 0
	s_setprio 1
	v_mfma_f32_16x16x128_f8f6f4 v[54:57], v[158:165], v[66:73], v[54:57]
	v_mfma_f32_16x16x128_f8f6f4 v[226:229], v[166:173], v[66:73], v[46:49]
	v_mfma_f32_16x16x128_f8f6f4 v[230:233], v[158:165], v[74:81], v[38:41]
	v_mfma_f32_16x16x128_f8f6f4 v[234:237], v[166:173], v[74:81], v[30:33]
	v_mfma_f32_16x16x128_f8f6f4 v[238:241], v[158:165], v[82:89], v[22:25]
	v_mfma_f32_16x16x128_f8f6f4 v[242:245], v[166:173], v[82:89], v[14:17]
	v_mfma_f32_16x16x128_f8f6f4 v[246:249], v[158:165], v[90:97], v[6:9]
	v_mfma_f32_16x16x128_f8f6f4 v[250:253], v[166:173], v[90:97], v[2:5]
	s_setprio 0
	s_barrier
; #define PG8_STAGE(bufoff, gbase, voff) do { _Pragma("unroll") for (int _i = 0; _i < 2; ++_i) \
;         __builtin_amdgcn_global_load_lds((const unsigned*)(wsb + (size_t)(gbase) + (voff)[_i]), (LAS unsigned*)(lds + (bufoff) + ldsw + _i * 8192), 16, 0, 0); } while (0)
; #define PG8_WAIT_V(n) asm volatile("s_waitcnt vmcnt(" #n ")" ::: "memory")
; #define PG8_BAR __builtin_amdgcn_s_barrier()
; template <class Epi, class Sched, bool PERM, bool FP8 = false, bool GATHER = false>
; DI void gemm_phase(LAS unsigned char* lds, const unsigned char* wsb, const unsigned lda, const unsigned ldb, const int nt, const Sched& S, const Epi& E) {
;     ...
;         for (int t = 0; t < nt; t += 2) {
;             const bool last = (t == nt - 2);
;             const unsigned b2 = last ? nB : cB + (unsigned)(t + 2) * kstep, b3 = b2 + kstep;
;             const int k2 = last ? 0 : t + 2, k3 = k2 + 1;
;             PG8_LDB(B0, 0, 0); PG8_LDB(B1, 0, 1); PG8_SCHED; PG8_LDA(At, 0, 0); PG8_STAGEA(PG8_SA(1, 1), t + 1, 1, false);
;             if constexpr (GATHER) { if (last) {
;                 int tz = tid; asm volatile("" : "+v"(tz));
; #pragma unroll
;                 for (int i = 0; i < 2; ++i) { int R, C; stage_rc(tz * 16 + i * 8192, R, C);
; #pragma unroll
;                     for (int h = 0; h < 2; ++h) { const unsigned tk = (unsigned)tokt[h * HALF + R]; offC[h][i] = (tk < (unsigned)NTOK ? tk : (unsigned)(NTOK - 1)) * lda + (unsigned)C * 2u; } } } }
;             PG8_WAIT_V(8); PG8_WAIT_L(0); PG8_BAR; PG8_MMA(0, 0, At, B0); PG8_MMA(0, 1, At, B1); PG8_BAR; PG8_SCHED;
;             PG8_LDA(At, 0, 1); PG8_STAGE(PG8_SB(0, 0), b2, voffB); PG8_STAGE(PG8_SB(0, 1), b2 + hstepB, voffB); PG8_STAGEA(PG8_SA(0, 0), k2, 0, last);
;             PG8_WAIT_V(8); PG8_WAIT_L(0); PG8_BAR; PG8_MMA(1, 0, At, B0); PG8_MMA(1, 1, At, B1); PG8_BAR; PG8_SCHED;
;             PG8_LDB(B0, 1, 0); PG8_LDB(B1, 1, 1); PG8_SCHED; PG8_LDA(At, 1, 0); PG8_STAGEA(PG8_SA(0, 1), k2, 1, last);
;             PG8_WAIT_V(8); PG8_WAIT_L(0); PG8_BAR; PG8_MMA(0, 0, At, B0); PG8_MMA(0, 1, At, B1); PG8_BAR; PG8_SCHED;
;             PG8_LDA(At, 1, 1); PG8_STAGE(PG8_SB(1, 0), b3, voffB); PG8_STAGE(PG8_SB(1, 1), b3 + hstepB, voffB); PG8_STAGEA(PG8_SA(1, 0), k3, 0, last);
;             PG8_WAIT_V(8); PG8_WAIT_L(0); PG8_BAR; PG8_MMA(1, 0, At, B0); PG8_MMA(1, 1, At, B1); PG8_BAR; PG8_SCHED;
;         }
;         if (wr == 0) PG8_BAR;
	s_nop 4
	ds_read_b128 v[2:5], v154 offset:32768
	ds_read_b128 v[6:9], v154 offset:33792
	ds_read_b128 v[10:13], v154 offset:34816
	ds_read_b128 v[14:17], v154 offset:35840
	ds_read_b128 v[130:133], v154 offset:49152
	ds_read_b128 v[134:137], v154 offset:50176
	ds_read_b128 v[138:141], v154 offset:51200
	ds_read_b128 v[142:145], v154 offset:52224
	s_add_i32 s25, s24, 0x20000
	s_add_u32 s74, s10, s25
	s_addc_u32 s75, s11, 0
	s_mov_b32 m0, s38
	v_lshl_add_u64 v[66:67], s[74:75], 0, v[146:147]
	ds_read_b128 v[18:21], v153 offset:32768
	ds_read_b128 v[22:25], v153 offset:33792
	ds_read_b128 v[26:29], v153 offset:34816
	ds_read_b128 v[30:33], v153 offset:35840
	ds_read_b128 v[34:37], v153 offset:36864
	ds_read_b128 v[38:41], v153 offset:37888
	ds_read_b128 v[42:45], v153 offset:38912
	ds_read_b128 v[46:49], v153 offset:39936
	global_load_lds_dwordx4 v[66:67], off
	v_lshl_add_u64 v[66:67], s[74:75], 0, v[148:149]
	s_mov_b32 m0, s39
	s_nop 0
	global_load_lds_dwordx4 v[66:67], off
	s_waitcnt vmcnt(8)
	s_waitcnt lgkmcnt(0)
	s_barrier
	s_setprio 1
	v_mfma_f32_16x16x128_f8f6f4 v[126:129], v[2:9], v[18:25], v[126:129]
	v_mfma_f32_16x16x128_f8f6f4 v[122:125], v[10:17], v[18:25], v[122:125]
	v_mfma_f32_16x16x128_f8f6f4 v[118:121], v[2:9], v[26:33], v[118:121]
	v_mfma_f32_16x16x128_f8f6f4 v[114:117], v[10:17], v[26:33], v[114:117]
	v_mfma_f32_16x16x128_f8f6f4 v[94:97], v[2:9], v[34:41], v[206:209]
	v_mfma_f32_16x16x128_f8f6f4 v[90:93], v[10:17], v[34:41], v[210:213]
	v_mfma_f32_16x16x128_f8f6f4 v[82:85], v[2:9], v[42:49], v[214:217]
	v_mfma_f32_16x16x128_f8f6f4 v[74:77], v[10:17], v[42:49], v[218:221]
	s_setprio 0
	s_setprio 1
	v_mfma_f32_16x16x128_f8f6f4 v[110:113], v[130:137], v[18:25], v[110:113]
	v_mfma_f32_16x16x128_f8f6f4 v[106:109], v[138:145], v[18:25], v[106:109]
	v_mfma_f32_16x16x128_f8f6f4 v[102:105], v[130:137], v[26:33], v[102:105]
	v_mfma_f32_16x16x128_f8f6f4 v[98:101], v[138:145], v[26:33], v[98:101]
	v_mfma_f32_16x16x128_f8f6f4 v[86:89], v[130:137], v[34:41], v[174:177]
	v_mfma_f32_16x16x128_f8f6f4 v[78:81], v[138:145], v[34:41], v[178:181]
	v_mfma_f32_16x16x128_f8f6f4 v[70:73], v[130:137], v[42:49], v[182:185]
	v_mfma_f32_16x16x128_f8f6f4 v[66:69], v[138:145], v[42:49], v[186:189]
	s_setprio 0
	s_barrier
	s_add_u32 s74, s10, s73
	s_addc_u32 s75, s11, 0
	s_add_i32 s72, s72, 0x20080
	s_mov_b32 m0, s43
	v_lshl_add_u64 v[18:19], s[74:75], 0, v[146:147]
	s_add_u32 s72, s10, s72
	ds_read_b128 v[158:161], v153 offset:49152
	ds_read_b128 v[162:165], v153 offset:50176
	ds_read_b128 v[166:169], v153 offset:51200
	ds_read_b128 v[170:173], v153 offset:52224
	ds_read_b128 v[174:177], v153 offset:53248
	ds_read_b128 v[178:181], v153 offset:54272
	ds_read_b128 v[182:185], v153 offset:55296
	ds_read_b128 v[186:189], v153 offset:56320
	global_load_lds_dwordx4 v[18:19], off
	v_lshl_add_u64 v[18:19], s[74:75], 0, v[148:149]
	s_mov_b32 m0, s46
	s_addc_u32 s73, s11, 0
	s_addk_i32 s24, 0x80
	global_load_lds_dwordx4 v[18:19], off
	v_lshl_add_u64 v[18:19], s[72:73], 0, v[146:147]
	s_mov_b32 m0, s49
	s_add_u32 s24, s10, s24
	global_load_lds_dwordx4 v[18:19], off
	v_lshl_add_u64 v[18:19], s[72:73], 0, v[148:149]
	s_mov_b32 m0, s50
	s_addc_u32 s25, s11, 0
	global_load_lds_dwordx4 v[18:19], off
	v_lshl_add_u64 v[18:19], s[24:25], 0, v[146:147]
	s_mov_b32 m0, s47
	s_nop 0
	global_load_lds_dwordx4 v[18:19], off
	v_lshl_add_u64 v[18:19], s[24:25], 0, v[148:149]
	s_mov_b32 m0, s48
	s_nop 0
	global_load_lds_dwordx4 v[18:19], off
	s_waitcnt vmcnt(8)
	s_waitcnt lgkmcnt(0)
	s_barrier
	s_setprio 1
	v_mfma_f32_16x16x128_f8f6f4 v[62:65], v[2:9], v[158:165], v[62:65]
	v_mfma_f32_16x16x128_f8f6f4 v[58:61], v[10:17], v[158:165], v[58:61]
	v_mfma_f32_16x16x128_f8f6f4 v[50:53], v[2:9], v[166:173], v[50:53]
	v_mfma_f32_16x16x128_f8f6f4 v[42:45], v[10:17], v[166:173], v[190:193]
	v_mfma_f32_16x16x128_f8f6f4 v[34:37], v[2:9], v[174:181], v[194:197]
	v_mfma_f32_16x16x128_f8f6f4 v[26:29], v[10:17], v[174:181], v[198:201]
	v_mfma_f32_16x16x128_f8f6f4 v[18:21], v[2:9], v[182:189], v[202:205]
	v_mfma_f32_16x16x128_f8f6f4 v[10:13], v[10:17], v[182:189], v[222:225]
	s_setprio 0
	s_setprio 1
	v_mfma_f32_16x16x128_f8f6f4 v[54:57], v[130:137], v[158:165], v[54:57]
	v_mfma_f32_16x16x128_f8f6f4 v[46:49], v[138:145], v[158:165], v[226:229]
	v_mfma_f32_16x16x128_f8f6f4 v[38:41], v[130:137], v[166:173], v[230:233]
	v_mfma_f32_16x16x128_f8f6f4 v[30:33], v[138:145], v[166:173], v[234:237]
	v_mfma_f32_16x16x128_f8f6f4 v[22:25], v[130:137], v[174:181], v[238:241]
	v_mfma_f32_16x16x128_f8f6f4 v[14:17], v[138:145], v[174:181], v[242:245]
	v_mfma_f32_16x16x128_f8f6f4 v[6:9], v[130:137], v[182:189], v[246:249]
	v_mfma_f32_16x16x128_f8f6f4 v[2:5], v[138:145], v[182:189], v[250:253]
	s_setprio 0
	s_barrier
	s_add_i32 s70, s70, 2
	s_addk_i32 s71, 0x100
	s_cmp_gt_u32 s70, 5
	s_cbranch_scc0 .LBB0_1450
	s_and_b64 vcc, exec, s[14:15]
	s_cbranch_vccz .LBB0_1453
	s_barrier

; #define PG8_STAGE(bufoff, gbase, voff) do { _Pragma("unroll") for (int _i = 0; _i < 2; ++_i) \
;         __builtin_amdgcn_global_load_lds((const unsigned*)(wsb + (size_t)(gbase) + (voff)[_i]), (LAS unsigned*)(lds + (bufoff) + ldsw + _i * 8192), 16, 0, 0); } while (0)
; #define PG8_WAIT_V(n) asm volatile("s_waitcnt vmcnt(" #n ")" ::: "memory")
; #define PG8_WAIT_L(n) asm volatile("s_waitcnt lgkmcnt(" #n ")" ::: "memory")
; template <class Epi, class Sched, bool PERM, bool FP8 = false, bool GATHER = false>
; DI void gemm_phase(LAS unsigned char* lds, const unsigned char* wsb, const unsigned lda, const unsigned ldb, const int nt, const Sched& S, const Epi& E) {
;     ...
;         for (int t = 0; t < nt; t += 2) {
;             const bool last = (t == nt - 2);
;             const unsigned b2 = last ? nB : cB + (unsigned)(t + 2) * kstep, b3 = b2 + kstep;
;             const int k2 = last ? 0 : t + 2, k3 = k2 + 1;
;             PG8_LDB(B0, 0, 0); PG8_LDB(B1, 0, 1); PG8_SCHED; PG8_LDA(At, 0, 0); PG8_STAGEA(PG8_SA(1, 1), t + 1, 1, false);
;             if constexpr (GATHER) { if (last) {
;                 int tz = tid; asm volatile("" : "+v"(tz));
; #pragma unroll
;                 for (int i = 0; i < 2; ++i) { int R, C; stage_rc(tz * 16 + i * 8192, R, C);
; #pragma unroll
;                     for (int h = 0; h < 2; ++h) { const unsigned tk = (unsigned)tokt[h * HALF + R]; offC[h][i] = (tk < (unsigned)NTOK ? tk : (unsigned)(NTOK - 1)) * lda + (unsigned)C * 2u; } } } }
;             PG8_WAIT_V(8); PG8_WAIT_L(0); PG8_BAR; PG8_MMA(0, 0, At, B0); PG8_MMA(0, 1, At, B1); PG8_BAR; PG8_SCHED;
;             PG8_LDA(At, 0, 1); PG8_STAGE(PG8_SB(0, 0), b2, voffB); PG8_STAGE(PG8_SB(0, 1), b2 + hstepB, voffB); PG8_STAGEA(PG8_SA(0, 0), k2, 0, last);
;             PG8_WAIT_V(8); PG8_WAIT_L(0); PG8_BAR; PG8_MMA(1, 0, At, B0); PG8_MMA(1, 1, At, B1); PG8_BAR; PG8_SCHED;
;             PG8_LDB(B0, 1, 0); PG8_LDB(B1, 1, 1); PG8_SCHED; PG8_LDA(At, 1, 0); PG8_STAGEA(PG8_SA(0, 1), k2, 1, last);
;             PG8_WAIT_V(8); PG8_WAIT_L(0); PG8_BAR; PG8_MMA(0, 0, At, B0); PG8_MMA(0, 1, At, B1); PG8_BAR; PG8_SCHED;
;             PG8_LDA(At, 1, 1); PG8_STAGE(PG8_SB(1, 0), b3, voffB); PG8_STAGE(PG8_SB(1, 1), b3 + hstepB, voffB); PG8_STAGEA(PG8_SA(1, 0), k3, 0, last);
;             PG8_WAIT_V(8); PG8_WAIT_L(0); PG8_BAR; PG8_MMA(1, 0, At, B0); PG8_MMA(1, 1, At, B1); PG8_BAR; PG8_SCHED;
.LBB0_1626:
	ds_read_b128 v[130:133], v186
	ds_read_b128 v[134:137], v186 offset:1024
	ds_read_b128 v[138:141], v186 offset:2048
	ds_read_b128 v[142:145], v186 offset:3072
	ds_read_b128 v[146:149], v186 offset:16384
	ds_read_b128 v[150:153], v186 offset:17408
	ds_read_b128 v[160:163], v186 offset:18432
	ds_read_b128 v[164:167], v186 offset:19456
	s_add_i32 s53, s7, 0xfffe0080
	s_cmp_eq_u32 s8, 4
	s_cselect_b32 s9, s50, s6
	s_cselect_b32 s53, s49, s53
	s_add_i32 s58, s9, 0x80
	s_add_u32 s60, s12, s7
	s_addc_u32 s61, s13, 0
	v_lshl_add_u64 v[206:207], s[60:61], 0, v[154:155]
	s_add_i32 m0, s69, 0xc000
	ds_read_b128 v[168:171], v185
	ds_read_b128 v[172:175], v185 offset:1024
	ds_read_b128 v[176:179], v185 offset:2048
	ds_read_b128 v[180:183], v185 offset:3072
	ds_read_b128 v[190:193], v185 offset:4096
	ds_read_b128 v[194:197], v185 offset:5120
	ds_read_b128 v[198:201], v185 offset:6144
	ds_read_b128 v[202:205], v185 offset:7168
	global_load_lds_dwordx4 v[206:207], off
	v_lshl_add_u64 v[206:207], s[60:61], 0, v[156:157]
	s_add_i32 m0, s69, 0xe000
	s_nop 0
	global_load_lds_dwordx4 v[206:207], off
	s_waitcnt vmcnt(8)
	s_waitcnt lgkmcnt(0)
	s_barrier
	s_setprio 1
	v_mfma_f32_16x16x128_f8f6f4 v[126:129], v[130:137], v[168:175], v[126:129]
	v_mfma_f32_16x16x128_f8f6f4 v[122:125], v[138:145], v[168:175], v[122:125]
	v_mfma_f32_16x16x128_f8f6f4 v[110:113], v[130:137], v[176:183], v[110:113]
	v_mfma_f32_16x16x128_f8f6f4 v[106:109], v[138:145], v[176:183], v[106:109]
	v_mfma_f32_16x16x128_f8f6f4 v[206:209], v[130:137], v[190:197], v[94:97]
	v_mfma_f32_16x16x128_f8f6f4 v[210:213], v[138:145], v[190:197], v[90:93]
	v_mfma_f32_16x16x128_f8f6f4 v[214:217], v[130:137], v[198:205], v[78:81]
	v_mfma_f32_16x16x128_f8f6f4 v[218:221], v[138:145], v[198:205], v[74:77]
	s_setprio 0
	s_setprio 1
	v_mfma_f32_16x16x128_f8f6f4 v[118:121], v[146:153], v[168:175], v[118:121]
	v_mfma_f32_16x16x128_f8f6f4 v[114:117], v[160:167], v[168:175], v[114:117]
	v_mfma_f32_16x16x128_f8f6f4 v[102:105], v[146:153], v[176:183], v[102:105]
	v_mfma_f32_16x16x128_f8f6f4 v[98:101], v[160:167], v[176:183], v[98:101]
	v_mfma_f32_16x16x128_f8f6f4 v[168:171], v[146:153], v[190:197], v[86:89]
	v_mfma_f32_16x16x128_f8f6f4 v[172:175], v[160:167], v[190:197], v[82:85]
	v_mfma_f32_16x16x128_f8f6f4 v[176:179], v[146:153], v[198:205], v[70:73]
	v_mfma_f32_16x16x128_f8f6f4 v[180:183], v[160:167], v[198:205], v[66:69]
	s_setprio 0
	s_barrier
	s_add_u32 s60, s12, s9
	s_addc_u32 s61, s13, 0
	s_mov_b32 m0, s70
	v_lshl_add_u64 v[190:191], s[60:61], 0, v[154:155]
	s_add_i32 s59, s9, 0x20000
	ds_read_b128 v[66:69], v185 offset:16384
	ds_read_b128 v[70:73], v185 offset:17408
	ds_read_b128 v[74:77], v185 offset:18432
	ds_read_b128 v[78:81], v185 offset:19456
	ds_read_b128 v[82:85], v185 offset:20480
	ds_read_b128 v[86:89], v185 offset:21504
	ds_read_b128 v[90:93], v185 offset:22528
	ds_read_b128 v[94:97], v185 offset:23552
	global_load_lds_dwordx4 v[190:191], off
	v_lshl_add_u64 v[190:191], s[60:61], 0, v[156:157]
	s_add_u32 s60, s12, s59
	s_mov_b32 m0, s71
	s_addc_u32 s61, s13, 0
	global_load_lds_dwordx4 v[190:191], off
	v_lshl_add_u64 v[190:191], s[60:61], 0, v[154:155]
	s_mov_b32 m0, s72
	s_nop 0
	global_load_lds_dwordx4 v[190:191], off
	v_lshl_add_u64 v[190:191], s[60:61], 0, v[156:157]
	s_add_u32 s60, s12, s53
	s_mov_b32 m0, s73
	s_addc_u32 s61, s13, 0
	global_load_lds_dwordx4 v[190:191], off
	v_lshl_add_u64 v[190:191], s[60:61], 0, v[154:155]
	s_mov_b32 m0, s69
	s_nop 0
	global_load_lds_dwordx4 v[190:191], off
	v_lshl_add_u64 v[190:191], s[60:61], 0, v[156:157]
	s_mov_b32 m0, s74
	s_nop 0
	global_load_lds_dwordx4 v[190:191], off
	s_waitcnt vmcnt(8)
	s_waitcnt lgkmcnt(0)
	s_barrier
	s_setprio 1
	v_mfma_f32_16x16x128_f8f6f4 v[62:65], v[130:137], v[66:73], v[62:65]
	v_mfma_f32_16x16x128_f8f6f4 v[58:61], v[138:145], v[66:73], v[58:61]
	v_mfma_f32_16x16x128_f8f6f4 v[190:193], v[130:137], v[74:81], v[46:49]
	v_mfma_f32_16x16x128_f8f6f4 v[194:197], v[138:145], v[74:81], v[42:45]
	v_mfma_f32_16x16x128_f8f6f4 v[198:201], v[130:137], v[82:89], v[30:33]
	v_mfma_f32_16x16x128_f8f6f4 v[202:205], v[138:145], v[82:89], v[26:29]
	v_mfma_f32_16x16x128_f8f6f4 v[222:225], v[130:137], v[90:97], v[14:17]
	v_mfma_f32_16x16x128_f8f6f4 v[226:229], v[138:145], v[90:97], v[10:13]
	s_setprio 0
	s_setprio 1
	v_mfma_f32_16x16x128_f8f6f4 v[54:57], v[146:153], v[66:73], v[54:57]
	v_mfma_f32_16x16x128_f8f6f4 v[50:53], v[160:167], v[66:73], v[50:53]
	v_mfma_f32_16x16x128_f8f6f4 v[230:233], v[146:153], v[74:81], v[38:41]
	v_mfma_f32_16x16x128_f8f6f4 v[234:237], v[160:167], v[74:81], v[34:37]
	v_mfma_f32_16x16x128_f8f6f4 v[238:241], v[146:153], v[82:89], v[22:25]
	v_mfma_f32_16x16x128_f8f6f4 v[242:245], v[160:167], v[82:89], v[18:21]
	v_mfma_f32_16x16x128_f8f6f4 v[246:249], v[146:153], v[90:97], v[6:9]
	v_mfma_f32_16x16x128_f8f6f4 v[250:253], v[160:167], v[90:97], v[2:5]
	s_setprio 0
	s_barrier
; #define PG8_STAGE(bufoff, gbase, voff) do { _Pragma("unroll") for (int _i = 0; _i < 2; ++_i) \
;         __builtin_amdgcn_global_load_lds((const unsigned*)(wsb + (size_t)(gbase) + (voff)[_i]), (LAS unsigned*)(lds + (bufoff) + ldsw + _i * 8192), 16, 0, 0); } while (0)
; #define PG8_WAIT_V(n) asm volatile("s_waitcnt vmcnt(" #n ")" ::: "memory")
; #define PG8_BAR __builtin_amdgcn_s_barrier()
; template <class Epi, class Sched, bool PERM, bool FP8 = false, bool GATHER = false>
; DI void gemm_phase(LAS unsigned char* lds, const unsigned char* wsb, const unsigned lda, const unsigned ldb, const int nt, const Sched& S, const Epi& E) {
;     ...
;         for (int t = 0; t < nt; t += 2) {
;             const bool last = (t == nt - 2);
;             const unsigned b2 = last ? nB : cB + (unsigned)(t + 2) * kstep, b3 = b2 + kstep;
;             const int k2 = last ? 0 : t + 2, k3 = k2 + 1;
;             PG8_LDB(B0, 0, 0); PG8_LDB(B1, 0, 1); PG8_SCHED; PG8_LDA(At, 0, 0); PG8_STAGEA(PG8_SA(1, 1), t + 1, 1, false);
;             if constexpr (GATHER) { if (last) {
;                 int tz = tid; asm volatile("" : "+v"(tz));
; #pragma unroll
;                 for (int i = 0; i < 2; ++i) { int R, C; stage_rc(tz * 16 + i * 8192, R, C);
; #pragma unroll
;                     for (int h = 0; h < 2; ++h) { const unsigned tk = (unsigned)tokt[h * HALF + R]; offC[h][i] = (tk < (unsigned)NTOK ? tk : (unsigned)(NTOK - 1)) * lda + (unsigned)C * 2u; } } } }
;             PG8_WAIT_V(8); PG8_WAIT_L(0); PG8_BAR; PG8_MMA(0, 0, At, B0); PG8_MMA(0, 1, At, B1); PG8_BAR; PG8_SCHED;
;             PG8_LDA(At, 0, 1); PG8_STAGE(PG8_SB(0, 0), b2, voffB); PG8_STAGE(PG8_SB(0, 1), b2 + hstepB, voffB); PG8_STAGEA(PG8_SA(0, 0), k2, 0, last);
;             PG8_WAIT_V(8); PG8_WAIT_L(0); PG8_BAR; PG8_MMA(1, 0, At, B0); PG8_MMA(1, 1, At, B1); PG8_BAR; PG8_SCHED;
;             PG8_LDB(B0, 1, 0); PG8_LDB(B1, 1, 1); PG8_SCHED; PG8_LDA(At, 1, 0); PG8_STAGEA(PG8_SA(0, 1), k2, 1, last);
;             PG8_WAIT_V(8); PG8_WAIT_L(0); PG8_BAR; PG8_MMA(0, 0, At, B0); PG8_MMA(0, 1, At, B1); PG8_BAR; PG8_SCHED;
;             PG8_LDA(At, 1, 1); PG8_STAGE(PG8_SB(1, 0), b3, voffB); PG8_STAGE(PG8_SB(1, 1), b3 + hstepB, voffB); PG8_STAGEA(PG8_SA(1, 0), k3, 0, last);
;             PG8_WAIT_V(8); PG8_WAIT_L(0); PG8_BAR; PG8_MMA(1, 0, At, B0); PG8_MMA(1, 1, At, B1); PG8_BAR; PG8_SCHED;
;         }
;         if (wr == 0) PG8_BAR;
	s_nop 4
	ds_read_b128 v[2:5], v186 offset:32768
	ds_read_b128 v[6:9], v186 offset:33792
	ds_read_b128 v[18:21], v186 offset:34816
	ds_read_b128 v[22:25], v186 offset:35840
	ds_read_b128 v[130:133], v186 offset:49152
	ds_read_b128 v[134:137], v186 offset:50176
	ds_read_b128 v[138:141], v186 offset:51200
	ds_read_b128 v[142:145], v186 offset:52224
	s_add_i32 s59, s53, 0x20000
	s_add_u32 s60, s12, s59
	s_addc_u32 s61, s13, 0
	s_mov_b32 m0, s75
	v_lshl_add_u64 v[66:67], s[60:61], 0, v[154:155]
	ds_read_b128 v[10:13], v185 offset:32768
	ds_read_b128 v[14:17], v185 offset:33792
	ds_read_b128 v[26:29], v185 offset:34816
	ds_read_b128 v[30:33], v185 offset:35840
	ds_read_b128 v[34:37], v185 offset:36864
	ds_read_b128 v[38:41], v185 offset:37888
	ds_read_b128 v[42:45], v185 offset:38912
	ds_read_b128 v[46:49], v185 offset:39936
	global_load_lds_dwordx4 v[66:67], off
	v_lshl_add_u64 v[66:67], s[60:61], 0, v[156:157]
	s_mov_b32 m0, s76
	s_nop 0
	global_load_lds_dwordx4 v[66:67], off
	s_waitcnt vmcnt(8)
	s_waitcnt lgkmcnt(0)
	s_barrier
	s_setprio 1
	v_mfma_f32_16x16x128_f8f6f4 v[126:129], v[2:9], v[10:17], v[126:129]
	v_mfma_f32_16x16x128_f8f6f4 v[122:125], v[18:25], v[10:17], v[122:125]
	v_mfma_f32_16x16x128_f8f6f4 v[110:113], v[2:9], v[26:33], v[110:113]
	v_mfma_f32_16x16x128_f8f6f4 v[106:109], v[18:25], v[26:33], v[106:109]
	v_mfma_f32_16x16x128_f8f6f4 v[94:97], v[2:9], v[34:41], v[206:209]
	v_mfma_f32_16x16x128_f8f6f4 v[90:93], v[18:25], v[34:41], v[210:213]
	v_mfma_f32_16x16x128_f8f6f4 v[78:81], v[2:9], v[42:49], v[214:217]
	v_mfma_f32_16x16x128_f8f6f4 v[74:77], v[18:25], v[42:49], v[218:221]
	s_setprio 0
	s_setprio 1
	v_mfma_f32_16x16x128_f8f6f4 v[118:121], v[130:137], v[10:17], v[118:121]
	v_mfma_f32_16x16x128_f8f6f4 v[114:117], v[138:145], v[10:17], v[114:117]
	v_mfma_f32_16x16x128_f8f6f4 v[102:105], v[130:137], v[26:33], v[102:105]
	v_mfma_f32_16x16x128_f8f6f4 v[98:101], v[138:145], v[26:33], v[98:101]
	v_mfma_f32_16x16x128_f8f6f4 v[86:89], v[130:137], v[34:41], v[168:171]
	v_mfma_f32_16x16x128_f8f6f4 v[82:85], v[138:145], v[34:41], v[172:175]
	v_mfma_f32_16x16x128_f8f6f4 v[70:73], v[130:137], v[42:49], v[176:179]
	v_mfma_f32_16x16x128_f8f6f4 v[66:69], v[138:145], v[42:49], v[180:183]
	s_setprio 0
	s_barrier
	s_add_u32 s58, s12, s58
	s_addc_u32 s59, s13, 0
	s_mov_b32 m0, s85
	v_lshl_add_u64 v[10:11], s[58:59], 0, v[154:155]
	s_add_i32 s9, s9, 0x20080
	ds_read_b128 v[34:37], v185 offset:49152
	ds_read_b128 v[38:41], v185 offset:50176
	ds_read_b128 v[146:149], v185 offset:51200
	ds_read_b128 v[150:153], v185 offset:52224
	ds_read_b128 v[160:163], v185 offset:53248
	ds_read_b128 v[164:167], v185 offset:54272
	ds_read_b128 v[168:171], v185 offset:55296
	ds_read_b128 v[172:175], v185 offset:56320
	global_load_lds_dwordx4 v[10:11], off
	v_lshl_add_u64 v[10:11], s[58:59], 0, v[156:157]
	s_add_u32 s58, s12, s9
	s_mov_b32 m0, s86
	s_addc_u32 s59, s13, 0
	global_load_lds_dwordx4 v[10:11], off
	v_lshl_add_u64 v[10:11], s[58:59], 0, v[154:155]
	s_mov_b32 m0, s89
	s_addk_i32 s53, 0x80
	global_load_lds_dwordx4 v[10:11], off
	v_lshl_add_u64 v[10:11], s[58:59], 0, v[156:157]
	s_add_u32 s58, s12, s53
	s_mov_b32 m0, s90
	s_addc_u32 s59, s13, 0
	global_load_lds_dwordx4 v[10:11], off
	v_lshl_add_u64 v[10:11], s[58:59], 0, v[154:155]
	s_mov_b32 m0, s87
	s_nop 0
	global_load_lds_dwordx4 v[10:11], off
	v_lshl_add_u64 v[10:11], s[58:59], 0, v[156:157]
	s_mov_b32 m0, s88
	s_nop 0
	global_load_lds_dwordx4 v[10:11], off
	s_waitcnt vmcnt(8)
	s_waitcnt lgkmcnt(0)
	s_barrier
	s_setprio 1
	v_mfma_f32_16x16x128_f8f6f4 v[62:65], v[2:9], v[34:41], v[62:65]
	v_mfma_f32_16x16x128_f8f6f4 v[58:61], v[18:25], v[34:41], v[58:61]
	v_mfma_f32_16x16x128_f8f6f4 v[46:49], v[2:9], v[146:153], v[190:193]
	v_mfma_f32_16x16x128_f8f6f4 v[42:45], v[18:25], v[146:153], v[194:197]
	v_mfma_f32_16x16x128_f8f6f4 v[30:33], v[2:9], v[160:167], v[198:201]
	v_mfma_f32_16x16x128_f8f6f4 v[26:29], v[18:25], v[160:167], v[202:205]
	v_mfma_f32_16x16x128_f8f6f4 v[14:17], v[2:9], v[168:175], v[222:225]
	v_mfma_f32_16x16x128_f8f6f4 v[10:13], v[18:25], v[168:175], v[226:229]
	s_setprio 0
	s_setprio 1
	v_mfma_f32_16x16x128_f8f6f4 v[54:57], v[130:137], v[34:41], v[54:57]
	v_mfma_f32_16x16x128_f8f6f4 v[50:53], v[138:145], v[34:41], v[50:53]
	v_mfma_f32_16x16x128_f8f6f4 v[38:41], v[130:137], v[146:153], v[230:233]
	v_mfma_f32_16x16x128_f8f6f4 v[34:37], v[138:145], v[146:153], v[234:237]
	v_mfma_f32_16x16x128_f8f6f4 v[22:25], v[130:137], v[160:167], v[238:241]
	v_mfma_f32_16x16x128_f8f6f4 v[18:21], v[138:145], v[160:167], v[242:245]
	v_mfma_f32_16x16x128_f8f6f4 v[6:9], v[130:137], v[168:175], v[246:249]
	v_mfma_f32_16x16x128_f8f6f4 v[2:5], v[138:145], v[168:175], v[250:253]
	s_setprio 0
	s_barrier
	s_add_i32 s8, s8, 2
	s_addk_i32 s7, 0x100
	s_addk_i32 s6, 0x100
	s_cmp_gt_u32 s8, 5
	s_cbranch_scc0 .LBB0_1626
	s_and_b64 vcc, exec, s[16:17]
	s_cbranch_vccz .LBB0_1629
	s_barrier

; #define PG8_STAGE(bufoff, gbase, voff) do { _Pragma("unroll") for (int _i = 0; _i < 2; ++_i) \
;         __builtin_amdgcn_global_load_lds((const unsigned*)(wsb + (size_t)(gbase) + (voff)[_i]), (LAS unsigned*)(lds + (bufoff) + ldsw + _i * 8192), 16, 0, 0); } while (0)
; #define PG8_WAIT_V(n) asm volatile("s_waitcnt vmcnt(" #n ")" ::: "memory")
; #define PG8_WAIT_L(n) asm volatile("s_waitcnt lgkmcnt(" #n ")" ::: "memory")
; template <class Epi, class Sched, bool PERM, bool FP8 = false, bool GATHER = false>
; DI void gemm_phase(LAS unsigned char* lds, const unsigned char* wsb, const unsigned lda, const unsigned ldb, const int nt, const Sched& S, const Epi& E) {
;     ...
;         for (int t = 0; t < nt; t += 2) {
;             const bool last = (t == nt - 2);
;             const unsigned b2 = last ? nB : cB + (unsigned)(t + 2) * kstep, b3 = b2 + kstep;
;             const int k2 = last ? 0 : t + 2, k3 = k2 + 1;
;             PG8_LDB(B0, 0, 0); PG8_LDB(B1, 0, 1); PG8_SCHED; PG8_LDA(At, 0, 0); PG8_STAGEA(PG8_SA(1, 1), t + 1, 1, false);
;             if constexpr (GATHER) { if (last) {
;                 int tz = tid; asm volatile("" : "+v"(tz));
; #pragma unroll
;                 for (int i = 0; i < 2; ++i) { int R, C; stage_rc(tz * 16 + i * 8192, R, C);
; #pragma unroll
;                     for (int h = 0; h < 2; ++h) { const unsigned tk = (unsigned)tokt[h * HALF + R]; offC[h][i] = (tk < (unsigned)NTOK ? tk : (unsigned)(NTOK - 1)) * lda + (unsigned)C * 2u; } } } }
;             PG8_WAIT_V(8); PG8_WAIT_L(0); PG8_BAR; PG8_MMA(0, 0, At, B0); PG8_MMA(0, 1, At, B1); PG8_BAR; PG8_SCHED;
;             PG8_LDA(At, 0, 1); PG8_STAGE(PG8_SB(0, 0), b2, voffB); PG8_STAGE(PG8_SB(0, 1), b2 + hstepB, voffB); PG8_STAGEA(PG8_SA(0, 0), k2, 0, last);
;             PG8_WAIT_V(8); PG8_WAIT_L(0); PG8_BAR; PG8_MMA(1, 0, At, B0); PG8_MMA(1, 1, At, B1); PG8_BAR; PG8_SCHED;
;             PG8_LDB(B0, 1, 0); PG8_LDB(B1, 1, 1); PG8_SCHED; PG8_LDA(At, 1, 0); PG8_STAGEA(PG8_SA(0, 1), k2, 1, last);
;             PG8_WAIT_V(8); PG8_WAIT_L(0); PG8_BAR; PG8_MMA(0, 0, At, B0); PG8_MMA(0, 1, At, B1); PG8_BAR; PG8_SCHED;
;             PG8_LDA(At, 1, 1); PG8_STAGE(PG8_SB(1, 0), b3, voffB); PG8_STAGE(PG8_SB(1, 1), b3 + hstepB, voffB); PG8_STAGEA(PG8_SA(1, 0), k3, 0, last);
;             PG8_WAIT_V(8); PG8_WAIT_L(0); PG8_BAR; PG8_MMA(1, 0, At, B0); PG8_MMA(1, 1, At, B1); PG8_BAR; PG8_SCHED;
.LBB0_1802:
	ds_read_b128 v[144:147], v142
	ds_read_b128 v[148:151], v142 offset:1024
	ds_read_b128 v[152:155], v142 offset:2048
	ds_read_b128 v[156:159], v142 offset:3072
	ds_read_b128 v[160:163], v142 offset:16384
	ds_read_b128 v[164:167], v142 offset:17408
	ds_read_b128 v[168:171], v142 offset:18432
	ds_read_b128 v[172:175], v142 offset:19456
	s_add_i32 s24, s20, 0xfffe0080
	s_cmp_eq_u32 s21, 4
	s_cselect_b32 s22, s72, s8
	s_cselect_b32 s24, s71, s24
	s_add_i32 s36, s22, 0x80
	s_add_u32 s38, s6, s20
	s_addc_u32 s39, s7, 0
	s_mov_b32 m0, s65
	v_lshl_add_u64 v[130:131], s[38:39], 0, v[138:139]
	ds_read_b128 v[176:179], v141
	ds_read_b128 v[180:183], v141 offset:1024
	ds_read_b128 v[184:187], v141 offset:2048
	ds_read_b128 v[188:191], v141 offset:3072
	ds_read_b128 v[192:195], v141 offset:4096
	ds_read_b128 v[196:199], v141 offset:5120
	ds_read_b128 v[200:203], v141 offset:6144
	ds_read_b128 v[204:207], v141 offset:7168
	global_load_lds_dwordx4 v[130:131], off
	v_lshl_add_u64 v[130:131], s[38:39], 0, v[134:135]
	s_mov_b32 m0, s66
	s_nop 0
	global_load_lds_dwordx4 v[130:131], off
	s_waitcnt vmcnt(8)
	s_waitcnt lgkmcnt(0)
	s_barrier
	s_setprio 1
	v_mfma_f32_16x16x128_f8f6f4 v[126:129], v[144:151], v[176:183], v[126:129]
	v_mfma_f32_16x16x128_f8f6f4 v[122:125], v[152:159], v[176:183], v[122:125]
	v_mfma_f32_16x16x128_f8f6f4 v[114:117], v[144:151], v[184:191], v[114:117]
	v_mfma_f32_16x16x128_f8f6f4 v[106:109], v[152:159], v[184:191], v[106:109]
	v_mfma_f32_16x16x128_f8f6f4 v[98:101], v[144:151], v[192:199], v[98:101]
	v_mfma_f32_16x16x128_f8f6f4 v[208:211], v[152:159], v[192:199], v[90:93]
	v_mfma_f32_16x16x128_f8f6f4 v[212:215], v[144:151], v[200:207], v[82:85]
	v_mfma_f32_16x16x128_f8f6f4 v[216:219], v[152:159], v[200:207], v[74:77]
	s_setprio 0
	s_setprio 1
	v_mfma_f32_16x16x128_f8f6f4 v[118:121], v[160:167], v[176:183], v[118:121]
	v_mfma_f32_16x16x128_f8f6f4 v[110:113], v[168:175], v[176:183], v[110:113]
	v_mfma_f32_16x16x128_f8f6f4 v[102:105], v[160:167], v[184:191], v[102:105]
	v_mfma_f32_16x16x128_f8f6f4 v[176:179], v[168:175], v[184:191], v[94:97]
	v_mfma_f32_16x16x128_f8f6f4 v[180:183], v[160:167], v[192:199], v[86:89]
	v_mfma_f32_16x16x128_f8f6f4 v[184:187], v[168:175], v[192:199], v[78:81]
	v_mfma_f32_16x16x128_f8f6f4 v[188:191], v[160:167], v[200:207], v[70:73]
	v_mfma_f32_16x16x128_f8f6f4 v[192:195], v[168:175], v[200:207], v[66:69]
	s_setprio 0
	s_barrier
	s_add_u32 s38, s6, s22
	s_addc_u32 s39, s7, 0
	s_mov_b32 m0, s28
	v_lshl_add_u64 v[130:131], s[38:39], 0, v[252:253]
	s_add_i32 s37, s22, 0x20000
	ds_read_b128 v[66:69], v141 offset:16384
	ds_read_b128 v[70:73], v141 offset:17408
	ds_read_b128 v[74:77], v141 offset:18432
	ds_read_b128 v[78:81], v141 offset:19456
	ds_read_b128 v[82:85], v141 offset:20480
	ds_read_b128 v[86:89], v141 offset:21504
	ds_read_b128 v[90:93], v141 offset:22528
	ds_read_b128 v[94:97], v141 offset:23552
	global_load_lds_dwordx4 v[130:131], off
	v_lshl_add_u64 v[130:131], s[38:39], 0, v[136:137]
	s_add_u32 s38, s6, s37
	s_mov_b32 m0, s29
	s_addc_u32 s39, s7, 0
	global_load_lds_dwordx4 v[130:131], off
	v_lshl_add_u64 v[130:131], s[38:39], 0, v[252:253]
	s_mov_b32 m0, s42
	s_nop 0
	global_load_lds_dwordx4 v[130:131], off
	v_lshl_add_u64 v[130:131], s[38:39], 0, v[136:137]
	s_add_u32 s38, s6, s24
	s_mov_b32 m0, s43
	s_addc_u32 s39, s7, 0
	global_load_lds_dwordx4 v[130:131], off
	v_lshl_add_u64 v[130:131], s[38:39], 0, v[138:139]
	s_mov_b32 m0, s17
	s_nop 0
	global_load_lds_dwordx4 v[130:131], off
	v_lshl_add_u64 v[130:131], s[38:39], 0, v[134:135]
	s_mov_b32 m0, s46
	s_nop 0
	global_load_lds_dwordx4 v[130:131], off
	s_waitcnt vmcnt(8)
	s_waitcnt lgkmcnt(0)
	s_barrier
	s_setprio 1
	v_mfma_f32_16x16x128_f8f6f4 v[62:65], v[144:151], v[66:73], v[62:65]
	v_mfma_f32_16x16x128_f8f6f4 v[58:61], v[152:159], v[66:73], v[58:61]
	v_mfma_f32_16x16x128_f8f6f4 v[50:53], v[144:151], v[74:81], v[50:53]
	v_mfma_f32_16x16x128_f8f6f4 v[196:199], v[152:159], v[74:81], v[42:45]
	v_mfma_f32_16x16x128_f8f6f4 v[200:203], v[144:151], v[82:89], v[34:37]
	v_mfma_f32_16x16x128_f8f6f4 v[204:207], v[152:159], v[82:89], v[26:29]
	v_mfma_f32_16x16x128_f8f6f4 v[220:223], v[144:151], v[90:97], v[18:21]
	v_mfma_f32_16x16x128_f8f6f4 v[224:227], v[152:159], v[90:97], v[10:13]
	s_setprio 0
	s_setprio 1
	v_mfma_f32_16x16x128_f8f6f4 v[54:57], v[160:167], v[66:73], v[54:57]
	v_mfma_f32_16x16x128_f8f6f4 v[228:231], v[168:175], v[66:73], v[46:49]
	v_mfma_f32_16x16x128_f8f6f4 v[232:235], v[160:167], v[74:81], v[38:41]
	v_mfma_f32_16x16x128_f8f6f4 v[236:239], v[168:175], v[74:81], v[30:33]
	v_mfma_f32_16x16x128_f8f6f4 v[240:243], v[160:167], v[82:89], v[22:25]
	v_mfma_f32_16x16x128_f8f6f4 v[244:247], v[168:175], v[82:89], v[14:17]
	v_mfma_f32_16x16x128_f8f6f4 v[248:251], v[160:167], v[90:97], v[6:9]
	v_mfma_f32_16x16x128_f8f6f4 v[130:133], v[168:175], v[90:97], v[2:5]
	s_setprio 0
	s_barrier
; #define PG8_STAGE(bufoff, gbase, voff) do { _Pragma("unroll") for (int _i = 0; _i < 2; ++_i) \
;         __builtin_amdgcn_global_load_lds((const unsigned*)(wsb + (size_t)(gbase) + (voff)[_i]), (LAS unsigned*)(lds + (bufoff) + ldsw + _i * 8192), 16, 0, 0); } while (0)
; #define PG8_WAIT_V(n) asm volatile("s_waitcnt vmcnt(" #n ")" ::: "memory")
; #define PG8_BAR __builtin_amdgcn_s_barrier()
; template <class Epi, class Sched, bool PERM, bool FP8 = false, bool GATHER = false>
; DI void gemm_phase(LAS unsigned char* lds, const unsigned char* wsb, const unsigned lda, const unsigned ldb, const int nt, const Sched& S, const Epi& E) {
;     ...
;         for (int t = 0; t < nt; t += 2) {
;             const bool last = (t == nt - 2);
;             const unsigned b2 = last ? nB : cB + (unsigned)(t + 2) * kstep, b3 = b2 + kstep;
;             const int k2 = last ? 0 : t + 2, k3 = k2 + 1;
;             PG8_LDB(B0, 0, 0); PG8_LDB(B1, 0, 1); PG8_SCHED; PG8_LDA(At, 0, 0); PG8_STAGEA(PG8_SA(1, 1), t + 1, 1, false);
;             if constexpr (GATHER) { if (last) {
;                 int tz = tid; asm volatile("" : "+v"(tz));
; #pragma unroll
;                 for (int i = 0; i < 2; ++i) { int R, C; stage_rc(tz * 16 + i * 8192, R, C);
; #pragma unroll
;                     for (int h = 0; h < 2; ++h) { const unsigned tk = (unsigned)tokt[h * HALF + R]; offC[h][i] = (tk < (unsigned)NTOK ? tk : (unsigned)(NTOK - 1)) * lda + (unsigned)C * 2u; } } } }
;             PG8_WAIT_V(8); PG8_WAIT_L(0); PG8_BAR; PG8_MMA(0, 0, At, B0); PG8_MMA(0, 1, At, B1); PG8_BAR; PG8_SCHED;
;             PG8_LDA(At, 0, 1); PG8_STAGE(PG8_SB(0, 0), b2, voffB); PG8_STAGE(PG8_SB(0, 1), b2 + hstepB, voffB); PG8_STAGEA(PG8_SA(0, 0), k2, 0, last);
;             PG8_WAIT_V(8); PG8_WAIT_L(0); PG8_BAR; PG8_MMA(1, 0, At, B0); PG8_MMA(1, 1, At, B1); PG8_BAR; PG8_SCHED;
;             PG8_LDB(B0, 1, 0); PG8_LDB(B1, 1, 1); PG8_SCHED; PG8_LDA(At, 1, 0); PG8_STAGEA(PG8_SA(0, 1), k2, 1, last);
;             PG8_WAIT_V(8); PG8_WAIT_L(0); PG8_BAR; PG8_MMA(0, 0, At, B0); PG8_MMA(0, 1, At, B1); PG8_BAR; PG8_SCHED;
;             PG8_LDA(At, 1, 1); PG8_STAGE(PG8_SB(1, 0), b3, voffB); PG8_STAGE(PG8_SB(1, 1), b3 + hstepB, voffB); PG8_STAGEA(PG8_SA(1, 0), k3, 0, last);
;             PG8_WAIT_V(8); PG8_WAIT_L(0); PG8_BAR; PG8_MMA(1, 0, At, B0); PG8_MMA(1, 1, At, B1); PG8_BAR; PG8_SCHED;
;         }
;         if (wr == 0) PG8_BAR;
	s_nop 4
	ds_read_b128 v[2:5], v142 offset:32768
	ds_read_b128 v[6:9], v142 offset:33792
	ds_read_b128 v[10:13], v142 offset:34816
	ds_read_b128 v[14:17], v142 offset:35840
	ds_read_b128 v[144:147], v142 offset:49152
	ds_read_b128 v[148:151], v142 offset:50176
	ds_read_b128 v[152:155], v142 offset:51200
	ds_read_b128 v[156:159], v142 offset:52224
	s_add_i32 s37, s24, 0x20000
	s_add_u32 s38, s6, s37
	s_addc_u32 s39, s7, 0
	s_mov_b32 m0, s47
	v_lshl_add_u64 v[66:67], s[38:39], 0, v[138:139]
	ds_read_b128 v[18:21], v141 offset:32768
	ds_read_b128 v[22:25], v141 offset:33792
	ds_read_b128 v[26:29], v141 offset:34816
	ds_read_b128 v[30:33], v141 offset:35840
	ds_read_b128 v[34:37], v141 offset:36864
	ds_read_b128 v[38:41], v141 offset:37888
	ds_read_b128 v[42:45], v141 offset:38912
	ds_read_b128 v[46:49], v141 offset:39936
	global_load_lds_dwordx4 v[66:67], off
	v_lshl_add_u64 v[66:67], s[38:39], 0, v[134:135]
	s_mov_b32 m0, s48
	s_nop 0
	global_load_lds_dwordx4 v[66:67], off
	s_waitcnt vmcnt(8)
	s_waitcnt lgkmcnt(0)
	s_barrier
	s_setprio 1
	v_mfma_f32_16x16x128_f8f6f4 v[126:129], v[2:9], v[18:25], v[126:129]
	v_mfma_f32_16x16x128_f8f6f4 v[122:125], v[10:17], v[18:25], v[122:125]
	v_mfma_f32_16x16x128_f8f6f4 v[114:117], v[2:9], v[26:33], v[114:117]
	v_mfma_f32_16x16x128_f8f6f4 v[106:109], v[10:17], v[26:33], v[106:109]
	v_mfma_f32_16x16x128_f8f6f4 v[98:101], v[2:9], v[34:41], v[98:101]
	v_mfma_f32_16x16x128_f8f6f4 v[90:93], v[10:17], v[34:41], v[208:211]
	v_mfma_f32_16x16x128_f8f6f4 v[82:85], v[2:9], v[42:49], v[212:215]
	v_mfma_f32_16x16x128_f8f6f4 v[74:77], v[10:17], v[42:49], v[216:219]
	s_setprio 0
	s_setprio 1
	v_mfma_f32_16x16x128_f8f6f4 v[118:121], v[144:151], v[18:25], v[118:121]
	v_mfma_f32_16x16x128_f8f6f4 v[110:113], v[152:159], v[18:25], v[110:113]
	v_mfma_f32_16x16x128_f8f6f4 v[102:105], v[144:151], v[26:33], v[102:105]
	v_mfma_f32_16x16x128_f8f6f4 v[94:97], v[152:159], v[26:33], v[176:179]
	v_mfma_f32_16x16x128_f8f6f4 v[86:89], v[144:151], v[34:41], v[180:183]
	v_mfma_f32_16x16x128_f8f6f4 v[78:81], v[152:159], v[34:41], v[184:187]
	v_mfma_f32_16x16x128_f8f6f4 v[70:73], v[144:151], v[42:49], v[188:191]
	v_mfma_f32_16x16x128_f8f6f4 v[66:69], v[152:159], v[42:49], v[192:195]
	s_setprio 0
	s_barrier
	s_add_u32 s36, s6, s36
	s_addc_u32 s37, s7, 0
	s_mov_b32 m0, s50
	v_lshl_add_u64 v[18:19], s[36:37], 0, v[252:253]
	s_add_i32 s22, s22, 0x20080
	ds_read_b128 v[160:163], v141 offset:49152
	ds_read_b128 v[164:167], v141 offset:50176
	ds_read_b128 v[168:171], v141 offset:51200
	ds_read_b128 v[172:175], v141 offset:52224
	ds_read_b128 v[176:179], v141 offset:53248
	ds_read_b128 v[180:183], v141 offset:54272
	ds_read_b128 v[184:187], v141 offset:55296
	ds_read_b128 v[188:191], v141 offset:56320
	global_load_lds_dwordx4 v[18:19], off
	v_lshl_add_u64 v[18:19], s[36:37], 0, v[136:137]
	s_add_u32 s36, s6, s22
	s_mov_b32 m0, s51
	s_addc_u32 s37, s7, 0
	global_load_lds_dwordx4 v[18:19], off
	v_lshl_add_u64 v[18:19], s[36:37], 0, v[252:253]
	s_mov_b32 m0, s54
	s_addk_i32 s24, 0x80
	global_load_lds_dwordx4 v[18:19], off
	v_lshl_add_u64 v[18:19], s[36:37], 0, v[136:137]
	s_add_u32 s36, s6, s24
	s_mov_b32 m0, s55
	s_addc_u32 s37, s7, 0
	global_load_lds_dwordx4 v[18:19], off
	v_lshl_add_u64 v[18:19], s[36:37], 0, v[138:139]
	s_mov_b32 m0, s52
	s_nop 0
	global_load_lds_dwordx4 v[18:19], off
	v_lshl_add_u64 v[18:19], s[36:37], 0, v[134:135]
	s_mov_b32 m0, s53
	s_nop 0
	global_load_lds_dwordx4 v[18:19], off
	s_waitcnt vmcnt(8)
	s_waitcnt lgkmcnt(0)
	s_barrier
	s_setprio 1
	v_mfma_f32_16x16x128_f8f6f4 v[62:65], v[2:9], v[160:167], v[62:65]
	v_mfma_f32_16x16x128_f8f6f4 v[58:61], v[10:17], v[160:167], v[58:61]
	v_mfma_f32_16x16x128_f8f6f4 v[50:53], v[2:9], v[168:175], v[50:53]
	v_mfma_f32_16x16x128_f8f6f4 v[42:45], v[10:17], v[168:175], v[196:199]
	v_mfma_f32_16x16x128_f8f6f4 v[34:37], v[2:9], v[176:183], v[200:203]
	v_mfma_f32_16x16x128_f8f6f4 v[26:29], v[10:17], v[176:183], v[204:207]
	v_mfma_f32_16x16x128_f8f6f4 v[18:21], v[2:9], v[184:191], v[220:223]
	v_mfma_f32_16x16x128_f8f6f4 v[10:13], v[10:17], v[184:191], v[224:227]
	s_setprio 0
	s_setprio 1
	v_mfma_f32_16x16x128_f8f6f4 v[54:57], v[144:151], v[160:167], v[54:57]
	v_mfma_f32_16x16x128_f8f6f4 v[46:49], v[152:159], v[160:167], v[228:231]
	v_mfma_f32_16x16x128_f8f6f4 v[38:41], v[144:151], v[168:175], v[232:235]
	v_mfma_f32_16x16x128_f8f6f4 v[30:33], v[152:159], v[168:175], v[236:239]
	v_mfma_f32_16x16x128_f8f6f4 v[22:25], v[144:151], v[176:183], v[240:243]
	v_mfma_f32_16x16x128_f8f6f4 v[14:17], v[152:159], v[176:183], v[244:247]
	v_mfma_f32_16x16x128_f8f6f4 v[6:9], v[144:151], v[184:191], v[248:251]
	v_mfma_f32_16x16x128_f8f6f4 v[2:5], v[152:159], v[184:191], v[130:133]
	s_setprio 0
	s_barrier
	s_add_i32 s21, s21, 2
	s_addk_i32 s20, 0x100
	s_addk_i32 s8, 0x100
	s_cmp_gt_u32 s21, 5
	s_cbranch_scc0 .LBB0_1802
	s_and_b64 vcc, exec, s[14:15]
	s_cbranch_vccz .LBB0_1805
	s_barrier

; #define PG8_STAGE(bufoff, gbase, voff) do { _Pragma("unroll") for (int _i = 0; _i < 2; ++_i) \
;         __builtin_amdgcn_global_load_lds((const unsigned*)(wsb + (size_t)(gbase) + (voff)[_i]), (LAS unsigned*)(lds + (bufoff) + ldsw + _i * 8192), 16, 0, 0); } while (0)
; #define PG8_WAIT_V(n) asm volatile("s_waitcnt vmcnt(" #n ")" ::: "memory")
; #define PG8_WAIT_L(n) asm volatile("s_waitcnt lgkmcnt(" #n ")" ::: "memory")
; template <class Epi, class Sched, bool PERM, bool FP8 = false, bool GATHER = false>
; DI void gemm_phase(LAS unsigned char* lds, const unsigned char* wsb, const unsigned lda, const unsigned ldb, const int nt, const Sched& S, const Epi& E) {
;     ...
;         for (int t = 0; t < nt; t += 2) {
;             const bool last = (t == nt - 2);
;             const unsigned b2 = last ? nB : cB + (unsigned)(t + 2) * kstep, b3 = b2 + kstep;
;             const int k2 = last ? 0 : t + 2, k3 = k2 + 1;
;             PG8_LDB(B0, 0, 0); PG8_LDB(B1, 0, 1); PG8_SCHED; PG8_LDA(At, 0, 0); PG8_STAGEA(PG8_SA(1, 1), t + 1, 1, false);
;             if constexpr (GATHER) { if (last) {
;                 int tz = tid; asm volatile("" : "+v"(tz));
; #pragma unroll
;                 for (int i = 0; i < 2; ++i) { int R, C; stage_rc(tz * 16 + i * 8192, R, C);
; #pragma unroll
;                     for (int h = 0; h < 2; ++h) { const unsigned tk = (unsigned)tokt[h * HALF + R]; offC[h][i] = (tk < (unsigned)NTOK ? tk : (unsigned)(NTOK - 1)) * lda + (unsigned)C * 2u; } } } }
;             PG8_WAIT_V(8); PG8_WAIT_L(0); PG8_BAR; PG8_MMA(0, 0, At, B0); PG8_MMA(0, 1, At, B1); PG8_BAR; PG8_SCHED;
;             PG8_LDA(At, 0, 1); PG8_STAGE(PG8_SB(0, 0), b2, voffB); PG8_STAGE(PG8_SB(0, 1), b2 + hstepB, voffB); PG8_STAGEA(PG8_SA(0, 0), k2, 0, last);
;             PG8_WAIT_V(8); PG8_WAIT_L(0); PG8_BAR; PG8_MMA(1, 0, At, B0); PG8_MMA(1, 1, At, B1); PG8_BAR; PG8_SCHED;
;             PG8_LDB(B0, 1, 0); PG8_LDB(B1, 1, 1); PG8_SCHED; PG8_LDA(At, 1, 0); PG8_STAGEA(PG8_SA(0, 1), k2, 1, last);
;             PG8_WAIT_V(8); PG8_WAIT_L(0); PG8_BAR; PG8_MMA(0, 0, At, B0); PG8_MMA(0, 1, At, B1); PG8_BAR; PG8_SCHED;
;             PG8_LDA(At, 1, 1); PG8_STAGE(PG8_SB(1, 0), b3, voffB); PG8_STAGE(PG8_SB(1, 1), b3 + hstepB, voffB); PG8_STAGEA(PG8_SA(1, 0), k3, 0, last);
;             PG8_WAIT_V(8); PG8_WAIT_L(0); PG8_BAR; PG8_MMA(1, 0, At, B0); PG8_MMA(1, 1, At, B1); PG8_BAR; PG8_SCHED;
.LBB0_2116:
	ds_read_b128 v[130:133], v200
	ds_read_b128 v[134:137], v200 offset:1024
	ds_read_b128 v[138:141], v200 offset:2048
	ds_read_b128 v[142:145], v200 offset:3072
	ds_read_b128 v[146:149], v200 offset:16384
	ds_read_b128 v[150:153], v200 offset:17408
	ds_read_b128 v[154:157], v200 offset:18432
	ds_read_b128 v[158:161], v200 offset:19456
	s_add_i32 s75, s71, 0xfffe0080
	s_cmp_eq_u32 s73, 4
	s_cselect_b32 s74, s68, s72
	s_cselect_b32 s75, s67, s75
	s_add_i32 s76, s74, 0x80
	s_add_u32 s78, s8, s71
	s_addc_u32 s79, s9, 0
	s_mov_b32 m0, s60
	v_lshl_add_u64 v[162:163], s[78:79], 0, v[168:169]
	ds_read_b128 v[170:173], v199
	ds_read_b128 v[174:177], v199 offset:1024
	ds_read_b128 v[178:181], v199 offset:2048
	ds_read_b128 v[182:185], v199 offset:3072
	ds_read_b128 v[186:189], v199 offset:4096
	ds_read_b128 v[190:193], v199 offset:5120
	ds_read_b128 v[202:205], v199 offset:6144
	ds_read_b128 v[206:209], v199 offset:7168
	global_load_lds_dwordx4 v[162:163], off
	v_lshl_add_u64 v[162:163], s[78:79], 0, v[166:167]
	s_mov_b32 m0, s61
	s_nop 0
	global_load_lds_dwordx4 v[162:163], off
	s_waitcnt vmcnt(8)
	s_waitcnt lgkmcnt(0)
	s_barrier
	s_setprio 1
	v_mfma_f32_16x16x128_f8f6f4 v[126:129], v[130:137], v[170:177], v[126:129]
	v_mfma_f32_16x16x128_f8f6f4 v[122:125], v[138:145], v[170:177], v[122:125]
	v_mfma_f32_16x16x128_f8f6f4 v[114:117], v[130:137], v[178:185], v[114:117]
	v_mfma_f32_16x16x128_f8f6f4 v[106:109], v[138:145], v[178:185], v[106:109]
	v_mfma_f32_16x16x128_f8f6f4 v[98:101], v[130:137], v[186:193], v[98:101]
	v_mfma_f32_16x16x128_f8f6f4 v[162:165], v[138:145], v[186:193], v[90:93]
	v_mfma_f32_16x16x128_f8f6f4 v[194:197], v[130:137], v[202:209], v[82:85]
	v_mfma_f32_16x16x128_f8f6f4 v[210:213], v[138:145], v[202:209], v[74:77]
	s_setprio 0
	s_setprio 1
	v_mfma_f32_16x16x128_f8f6f4 v[118:121], v[146:153], v[170:177], v[118:121]
	v_mfma_f32_16x16x128_f8f6f4 v[110:113], v[154:161], v[170:177], v[110:113]
	v_mfma_f32_16x16x128_f8f6f4 v[102:105], v[146:153], v[178:185], v[102:105]
	v_mfma_f32_16x16x128_f8f6f4 v[170:173], v[154:161], v[178:185], v[94:97]
	v_mfma_f32_16x16x128_f8f6f4 v[174:177], v[146:153], v[186:193], v[86:89]
	v_mfma_f32_16x16x128_f8f6f4 v[178:181], v[154:161], v[186:193], v[78:81]
	v_mfma_f32_16x16x128_f8f6f4 v[182:185], v[146:153], v[202:209], v[70:73]
	v_mfma_f32_16x16x128_f8f6f4 v[186:189], v[154:161], v[202:209], v[66:69]
	s_setprio 0
	s_barrier
	s_add_u32 s78, s8, s74
	s_addc_u32 s79, s9, 0
	s_mov_b32 m0, s28
	v_lshl_add_u64 v[190:191], s[78:79], 0, v[168:169]
	s_add_i32 s77, s74, 0x20000
	ds_read_b128 v[66:69], v199 offset:16384
	ds_read_b128 v[70:73], v199 offset:17408
	ds_read_b128 v[74:77], v199 offset:18432
	ds_read_b128 v[78:81], v199 offset:19456
	ds_read_b128 v[82:85], v199 offset:20480
	ds_read_b128 v[86:89], v199 offset:21504
	ds_read_b128 v[90:93], v199 offset:22528
	ds_read_b128 v[94:97], v199 offset:23552
	global_load_lds_dwordx4 v[190:191], off
	v_lshl_add_u64 v[190:191], s[78:79], 0, v[166:167]
	s_add_u32 s78, s8, s77
	s_mov_b32 m0, s29
	s_addc_u32 s79, s9, 0
	global_load_lds_dwordx4 v[190:191], off
	v_lshl_add_u64 v[190:191], s[78:79], 0, v[168:169]
	s_mov_b32 m0, s46
	s_nop 0
	global_load_lds_dwordx4 v[190:191], off
	v_lshl_add_u64 v[190:191], s[78:79], 0, v[166:167]
	s_add_u32 s78, s8, s75
	s_mov_b32 m0, s47
	s_addc_u32 s79, s9, 0
	global_load_lds_dwordx4 v[190:191], off
	v_lshl_add_u64 v[190:191], s[78:79], 0, v[168:169]
	s_mov_b32 m0, s21
	s_nop 0
	global_load_lds_dwordx4 v[190:191], off
	v_lshl_add_u64 v[190:191], s[78:79], 0, v[166:167]
	s_mov_b32 m0, s48
	s_nop 0
	global_load_lds_dwordx4 v[190:191], off
	s_waitcnt vmcnt(8)
	s_waitcnt lgkmcnt(0)
	s_barrier
	s_setprio 1
	v_mfma_f32_16x16x128_f8f6f4 v[62:65], v[130:137], v[66:73], v[62:65]
	v_mfma_f32_16x16x128_f8f6f4 v[58:61], v[138:145], v[66:73], v[58:61]
	v_mfma_f32_16x16x128_f8f6f4 v[50:53], v[130:137], v[74:81], v[50:53]
	v_mfma_f32_16x16x128_f8f6f4 v[190:193], v[138:145], v[74:81], v[42:45]
	v_mfma_f32_16x16x128_f8f6f4 v[202:205], v[130:137], v[82:89], v[34:37]
	v_mfma_f32_16x16x128_f8f6f4 v[206:209], v[138:145], v[82:89], v[26:29]
	v_mfma_f32_16x16x128_f8f6f4 v[214:217], v[130:137], v[90:97], v[18:21]
	v_mfma_f32_16x16x128_f8f6f4 v[218:221], v[138:145], v[90:97], v[10:13]
	s_setprio 0
	s_setprio 1
	v_mfma_f32_16x16x128_f8f6f4 v[54:57], v[146:153], v[66:73], v[54:57]
	v_mfma_f32_16x16x128_f8f6f4 v[222:225], v[154:161], v[66:73], v[46:49]
	v_mfma_f32_16x16x128_f8f6f4 v[226:229], v[146:153], v[74:81], v[38:41]
	v_mfma_f32_16x16x128_f8f6f4 v[230:233], v[154:161], v[74:81], v[30:33]
	v_mfma_f32_16x16x128_f8f6f4 v[234:237], v[146:153], v[82:89], v[22:25]
	v_mfma_f32_16x16x128_f8f6f4 v[238:241], v[154:161], v[82:89], v[14:17]
	v_mfma_f32_16x16x128_f8f6f4 v[242:245], v[146:153], v[90:97], v[6:9]
	v_mfma_f32_16x16x128_f8f6f4 v[246:249], v[154:161], v[90:97], v[2:5]
	s_setprio 0
	s_barrier
; #define PG8_STAGE(bufoff, gbase, voff) do { _Pragma("unroll") for (int _i = 0; _i < 2; ++_i) \
;         __builtin_amdgcn_global_load_lds((const unsigned*)(wsb + (size_t)(gbase) + (voff)[_i]), (LAS unsigned*)(lds + (bufoff) + ldsw + _i * 8192), 16, 0, 0); } while (0)
; #define PG8_WAIT_V(n) asm volatile("s_waitcnt vmcnt(" #n ")" ::: "memory")
; #define PG8_BAR __builtin_amdgcn_s_barrier()
; template <class Epi, class Sched, bool PERM, bool FP8 = false, bool GATHER = false>
; DI void gemm_phase(LAS unsigned char* lds, const unsigned char* wsb, const unsigned lda, const unsigned ldb, const int nt, const Sched& S, const Epi& E) {
;     ...
;         for (int t = 0; t < nt; t += 2) {
;             const bool last = (t == nt - 2);
;             const unsigned b2 = last ? nB : cB + (unsigned)(t + 2) * kstep, b3 = b2 + kstep;
;             const int k2 = last ? 0 : t + 2, k3 = k2 + 1;
;             PG8_LDB(B0, 0, 0); PG8_LDB(B1, 0, 1); PG8_SCHED; PG8_LDA(At, 0, 0); PG8_STAGEA(PG8_SA(1, 1), t + 1, 1, false);
;             if constexpr (GATHER) { if (last) {
;                 int tz = tid; asm volatile("" : "+v"(tz));
; #pragma unroll
;                 for (int i = 0; i < 2; ++i) { int R, C; stage_rc(tz * 16 + i * 8192, R, C);
; #pragma unroll
;                     for (int h = 0; h < 2; ++h) { const unsigned tk = (unsigned)tokt[h * HALF + R]; offC[h][i] = (tk < (unsigned)NTOK ? tk : (unsigned)(NTOK - 1)) * lda + (unsigned)C * 2u; } } } }
;             PG8_WAIT_V(8); PG8_WAIT_L(0); PG8_BAR; PG8_MMA(0, 0, At, B0); PG8_MMA(0, 1, At, B1); PG8_BAR; PG8_SCHED;
;             PG8_LDA(At, 0, 1); PG8_STAGE(PG8_SB(0, 0), b2, voffB); PG8_STAGE(PG8_SB(0, 1), b2 + hstepB, voffB); PG8_STAGEA(PG8_SA(0, 0), k2, 0, last);
;             PG8_WAIT_V(8); PG8_WAIT_L(0); PG8_BAR; PG8_MMA(1, 0, At, B0); PG8_MMA(1, 1, At, B1); PG8_BAR; PG8_SCHED;
;             PG8_LDB(B0, 1, 0); PG8_LDB(B1, 1, 1); PG8_SCHED; PG8_LDA(At, 1, 0); PG8_STAGEA(PG8_SA(0, 1), k2, 1, last);
;             PG8_WAIT_V(8); PG8_WAIT_L(0); PG8_BAR; PG8_MMA(0, 0, At, B0); PG8_MMA(0, 1, At, B1); PG8_BAR; PG8_SCHED;
;             PG8_LDA(At, 1, 1); PG8_STAGE(PG8_SB(1, 0), b3, voffB); PG8_STAGE(PG8_SB(1, 1), b3 + hstepB, voffB); PG8_STAGEA(PG8_SA(1, 0), k3, 0, last);
;             PG8_WAIT_V(8); PG8_WAIT_L(0); PG8_BAR; PG8_MMA(1, 0, At, B0); PG8_MMA(1, 1, At, B1); PG8_BAR; PG8_SCHED;
;         }
;         if (wr == 0) PG8_BAR;
	s_nop 4
	ds_read_b128 v[2:5], v200 offset:32768
	ds_read_b128 v[6:9], v200 offset:33792
	ds_read_b128 v[10:13], v200 offset:34816
	ds_read_b128 v[14:17], v200 offset:35840
	ds_read_b128 v[130:133], v200 offset:49152
	ds_read_b128 v[134:137], v200 offset:50176
	ds_read_b128 v[138:141], v200 offset:51200
	ds_read_b128 v[142:145], v200 offset:52224
	s_add_i32 s77, s75, 0x20000
	s_add_u32 s78, s8, s77
	s_addc_u32 s79, s9, 0
	s_mov_b32 m0, s49
	v_lshl_add_u64 v[66:67], s[78:79], 0, v[168:169]
	ds_read_b128 v[18:21], v199 offset:32768
	ds_read_b128 v[22:25], v199 offset:33792
	ds_read_b128 v[26:29], v199 offset:34816
	ds_read_b128 v[30:33], v199 offset:35840
	ds_read_b128 v[34:37], v199 offset:36864
	ds_read_b128 v[38:41], v199 offset:37888
	ds_read_b128 v[42:45], v199 offset:38912
	ds_read_b128 v[46:49], v199 offset:39936
	global_load_lds_dwordx4 v[66:67], off
	v_lshl_add_u64 v[66:67], s[78:79], 0, v[166:167]
	s_mov_b32 m0, s50
	s_nop 0
	global_load_lds_dwordx4 v[66:67], off
	s_waitcnt vmcnt(8)
	s_waitcnt lgkmcnt(0)
	s_barrier
	s_setprio 1
	v_mfma_f32_16x16x128_f8f6f4 v[126:129], v[2:9], v[18:25], v[126:129]
	v_mfma_f32_16x16x128_f8f6f4 v[122:125], v[10:17], v[18:25], v[122:125]
	v_mfma_f32_16x16x128_f8f6f4 v[114:117], v[2:9], v[26:33], v[114:117]
	v_mfma_f32_16x16x128_f8f6f4 v[106:109], v[10:17], v[26:33], v[106:109]
	v_mfma_f32_16x16x128_f8f6f4 v[98:101], v[2:9], v[34:41], v[98:101]
	v_mfma_f32_16x16x128_f8f6f4 v[90:93], v[10:17], v[34:41], v[162:165]
	v_mfma_f32_16x16x128_f8f6f4 v[82:85], v[2:9], v[42:49], v[194:197]
	v_mfma_f32_16x16x128_f8f6f4 v[74:77], v[10:17], v[42:49], v[210:213]
	s_setprio 0
	s_setprio 1
	v_mfma_f32_16x16x128_f8f6f4 v[118:121], v[130:137], v[18:25], v[118:121]
	v_mfma_f32_16x16x128_f8f6f4 v[110:113], v[138:145], v[18:25], v[110:113]
	v_mfma_f32_16x16x128_f8f6f4 v[102:105], v[130:137], v[26:33], v[102:105]
	v_mfma_f32_16x16x128_f8f6f4 v[94:97], v[138:145], v[26:33], v[170:173]
	v_mfma_f32_16x16x128_f8f6f4 v[86:89], v[130:137], v[34:41], v[174:177]
	v_mfma_f32_16x16x128_f8f6f4 v[78:81], v[138:145], v[34:41], v[178:181]
	v_mfma_f32_16x16x128_f8f6f4 v[70:73], v[130:137], v[42:49], v[182:185]
	v_mfma_f32_16x16x128_f8f6f4 v[66:69], v[138:145], v[42:49], v[186:189]
	s_setprio 0
	s_barrier
	s_add_u32 s76, s8, s76
	s_addc_u32 s77, s9, 0
	s_mov_b32 m0, s52
	v_lshl_add_u64 v[18:19], s[76:77], 0, v[168:169]
	s_add_i32 s74, s74, 0x20080
	ds_read_b128 v[146:149], v199 offset:49152
	ds_read_b128 v[150:153], v199 offset:50176
	ds_read_b128 v[154:157], v199 offset:51200
	ds_read_b128 v[158:161], v199 offset:52224
	ds_read_b128 v[170:173], v199 offset:53248
	ds_read_b128 v[174:177], v199 offset:54272
	ds_read_b128 v[178:181], v199 offset:55296
	ds_read_b128 v[182:185], v199 offset:56320
	global_load_lds_dwordx4 v[18:19], off
	v_lshl_add_u64 v[18:19], s[76:77], 0, v[166:167]
	s_add_u32 s76, s8, s74
	s_mov_b32 m0, s53
	s_addc_u32 s77, s9, 0
	s_addk_i32 s75, 0x80
	global_load_lds_dwordx4 v[18:19], off
	v_lshl_add_u64 v[18:19], s[76:77], 0, v[168:169]
	s_mov_b32 m0, s56
	s_add_u32 s74, s8, s75
	global_load_lds_dwordx4 v[18:19], off
	v_lshl_add_u64 v[18:19], s[76:77], 0, v[166:167]
	s_mov_b32 m0, s57
	s_addc_u32 s75, s9, 0
	global_load_lds_dwordx4 v[18:19], off
	v_lshl_add_u64 v[18:19], s[74:75], 0, v[168:169]
	s_mov_b32 m0, s54
	s_nop 0
	global_load_lds_dwordx4 v[18:19], off
	v_lshl_add_u64 v[18:19], s[74:75], 0, v[166:167]
	s_mov_b32 m0, s55
	s_nop 0
	global_load_lds_dwordx4 v[18:19], off
	s_waitcnt vmcnt(8)
	s_waitcnt lgkmcnt(0)
	s_barrier
	s_setprio 1
	v_mfma_f32_16x16x128_f8f6f4 v[62:65], v[2:9], v[146:153], v[62:65]
	v_mfma_f32_16x16x128_f8f6f4 v[58:61], v[10:17], v[146:153], v[58:61]
	v_mfma_f32_16x16x128_f8f6f4 v[50:53], v[2:9], v[154:161], v[50:53]
	v_mfma_f32_16x16x128_f8f6f4 v[42:45], v[10:17], v[154:161], v[190:193]
	v_mfma_f32_16x16x128_f8f6f4 v[34:37], v[2:9], v[170:177], v[202:205]
	v_mfma_f32_16x16x128_f8f6f4 v[26:29], v[10:17], v[170:177], v[206:209]
	v_mfma_f32_16x16x128_f8f6f4 v[18:21], v[2:9], v[178:185], v[214:217]
	v_mfma_f32_16x16x128_f8f6f4 v[10:13], v[10:17], v[178:185], v[218:221]
	s_setprio 0
	s_setprio 1
	v_mfma_f32_16x16x128_f8f6f4 v[54:57], v[130:137], v[146:153], v[54:57]
	v_mfma_f32_16x16x128_f8f6f4 v[46:49], v[138:145], v[146:153], v[222:225]
	v_mfma_f32_16x16x128_f8f6f4 v[38:41], v[130:137], v[154:161], v[226:229]
	v_mfma_f32_16x16x128_f8f6f4 v[30:33], v[138:145], v[154:161], v[230:233]
	v_mfma_f32_16x16x128_f8f6f4 v[22:25], v[130:137], v[170:177], v[234:237]
	v_mfma_f32_16x16x128_f8f6f4 v[14:17], v[138:145], v[170:177], v[238:241]
	v_mfma_f32_16x16x128_f8f6f4 v[6:9], v[130:137], v[178:185], v[242:245]
	v_mfma_f32_16x16x128_f8f6f4 v[2:5], v[138:145], v[178:185], v[246:249]
	s_setprio 0
	s_barrier
	s_add_i32 s73, s73, 2
	s_addk_i32 s71, 0x100
	s_addk_i32 s72, 0x100
	s_cmp_gt_u32 s73, 5
	s_cbranch_scc0 .LBB0_2116
	s_and_b64 vcc, exec, s[12:13]
	s_cbranch_vccz .LBB0_2119
	s_barrier

; #define PG8_STAGE(bufoff, gbase, voff) do { _Pragma("unroll") for (int _i = 0; _i < 2; ++_i) \
;         __builtin_amdgcn_global_load_lds((const unsigned*)(wsb + (size_t)(gbase) + (voff)[_i]), (LAS unsigned*)(lds + (bufoff) + ldsw + _i * 8192), 16, 0, 0); } while (0)
; #define PG8_WAIT_V(n) asm volatile("s_waitcnt vmcnt(" #n ")" ::: "memory")
; #define PG8_WAIT_L(n) asm volatile("s_waitcnt lgkmcnt(" #n ")" ::: "memory")
; template <class Epi, class Sched, bool PERM, bool FP8 = false, bool GATHER = false>
; DI void gemm_phase(LAS unsigned char* lds, const unsigned char* wsb, const unsigned lda, const unsigned ldb, const int nt, const Sched& S, const Epi& E) {
;     ...
;         for (int t = 0; t < nt; t += 2) {
;             const bool last = (t == nt - 2);
;             const unsigned b2 = last ? nB : cB + (unsigned)(t + 2) * kstep, b3 = b2 + kstep;
;             const int k2 = last ? 0 : t + 2, k3 = k2 + 1;
;             PG8_LDB(B0, 0, 0); PG8_LDB(B1, 0, 1); PG8_SCHED; PG8_LDA(At, 0, 0); PG8_STAGEA(PG8_SA(1, 1), t + 1, 1, false);
;             if constexpr (GATHER) { if (last) {
;                 int tz = tid; asm volatile("" : "+v"(tz));
; #pragma unroll
;                 for (int i = 0; i < 2; ++i) { int R, C; stage_rc(tz * 16 + i * 8192, R, C);
; #pragma unroll
;                     for (int h = 0; h < 2; ++h) { const unsigned tk = (unsigned)tokt[h * HALF + R]; offC[h][i] = (tk < (unsigned)NTOK ? tk : (unsigned)(NTOK - 1)) * lda + (unsigned)C * 2u; } } } }
;             PG8_WAIT_V(8); PG8_WAIT_L(0); PG8_BAR; PG8_MMA(0, 0, At, B0); PG8_MMA(0, 1, At, B1); PG8_BAR; PG8_SCHED;
;             PG8_LDA(At, 0, 1); PG8_STAGE(PG8_SB(0, 0), b2, voffB); PG8_STAGE(PG8_SB(0, 1), b2 + hstepB, voffB); PG8_STAGEA(PG8_SA(0, 0), k2, 0, last);
;             PG8_WAIT_V(8); PG8_WAIT_L(0); PG8_BAR; PG8_MMA(1, 0, At, B0); PG8_MMA(1, 1, At, B1); PG8_BAR; PG8_SCHED;
;             PG8_LDB(B0, 1, 0); PG8_LDB(B1, 1, 1); PG8_SCHED; PG8_LDA(At, 1, 0); PG8_STAGEA(PG8_SA(0, 1), k2, 1, last);
;             PG8_WAIT_V(8); PG8_WAIT_L(0); PG8_BAR; PG8_MMA(0, 0, At, B0); PG8_MMA(0, 1, At, B1); PG8_BAR; PG8_SCHED;
;             PG8_LDA(At, 1, 1); PG8_STAGE(PG8_SB(1, 0), b3, voffB); PG8_STAGE(PG8_SB(1, 1), b3 + hstepB, voffB); PG8_STAGEA(PG8_SA(1, 0), k3, 0, last);
;             PG8_WAIT_V(8); PG8_WAIT_L(0); PG8_BAR; PG8_MMA(1, 0, At, B0); PG8_MMA(1, 1, At, B1); PG8_BAR; PG8_SCHED;
.LBB0_2544:
	s_waitcnt vmcnt(8)
	s_add_i32 s84, s80, s44
	s_waitcnt lgkmcnt(0)
	s_and_b64 s[82:83], s[46:47], exec
	s_cselect_b32 s82, s12, s84
	v_mov_b32_e32 v205, v197
	s_add_i32 s83, s82, 0x80
	s_barrier
	s_setprio 1
	v_mfma_f32_16x16x128_f8f6f4 v[190:193], v[18:25], v[58:65], v[190:193]
	v_mfma_f32_16x16x128_f8f6f4 v[186:189], v[26:33], v[58:65], v[186:189]
	v_mfma_f32_16x16x128_f8f6f4 v[174:177], v[18:25], v[50:57], v[174:177]
	v_mfma_f32_16x16x128_f8f6f4 v[166:169], v[26:33], v[50:57], v[166:169]
	v_mfma_f32_16x16x128_f8f6f4 v[158:161], v[18:25], v[42:49], v[158:161]
	v_mfma_f32_16x16x128_f8f6f4 v[150:153], v[26:33], v[42:49], v[150:153]
	v_mfma_f32_16x16x128_f8f6f4 v[142:145], v[18:25], v[34:41], v[142:145]
	v_mfma_f32_16x16x128_f8f6f4 v[134:137], v[26:33], v[34:41], v[134:137]
	s_setprio 0
	s_setprio 1
	v_mfma_f32_16x16x128_f8f6f4 v[182:185], v[2:9], v[58:65], v[182:185]
	v_mfma_f32_16x16x128_f8f6f4 v[178:181], v[10:17], v[58:65], v[178:181]
	v_mfma_f32_16x16x128_f8f6f4 v[170:173], v[2:9], v[50:57], v[170:173]
	v_mfma_f32_16x16x128_f8f6f4 v[162:165], v[10:17], v[50:57], v[162:165]
	v_mfma_f32_16x16x128_f8f6f4 v[154:157], v[2:9], v[42:49], v[154:157]
	v_mfma_f32_16x16x128_f8f6f4 v[146:149], v[10:17], v[42:49], v[146:149]
	v_mfma_f32_16x16x128_f8f6f4 v[138:141], v[2:9], v[34:41], v[138:141]
	v_mfma_f32_16x16x128_f8f6f4 v[130:133], v[10:17], v[34:41], v[130:133]
	s_setprio 0
	s_barrier
	s_add_u32 s84, s8, s82
	s_addc_u32 s85, s9, 0
	s_mov_b32 m0, s48
	v_lshl_add_u64 v[214:215], s[84:85], 0, v[198:199]
	ds_read_b128 v[34:37], v209 offset:16384
	ds_read_b128 v[38:41], v209 offset:17408
	ds_read_b128 v[42:45], v209 offset:18432
	ds_read_b128 v[46:49], v209 offset:19456
	ds_read_b128 v[50:53], v209 offset:20480
	ds_read_b128 v[54:57], v209 offset:21504
	ds_read_b128 v[58:61], v209 offset:22528
	ds_read_b128 v[62:65], v209 offset:23552
	global_load_lds_dwordx4 v[214:215], off
	v_lshl_add_u64 v[214:215], s[84:85], 0, v[200:201]
	s_add_i32 s84, s82, 0x20000
	s_add_u32 s84, s8, s84
	s_addc_u32 s85, s9, 0
	s_add_u32 s44, s44, 0x100
	s_mov_b32 m0, s49
	s_addc_u32 s45, s45, 0
	global_load_lds_dwordx4 v[214:215], off
	v_lshl_add_u64 v[214:215], s[84:85], 0, v[198:199]
	s_mov_b32 m0, s50
	s_and_b64 s[46:47], s[46:47], exec
	global_load_lds_dwordx4 v[214:215], off
	v_lshl_add_u64 v[214:215], s[84:85], 0, v[200:201]
	s_cselect_b32 s84, 0, s44
	s_mov_b32 m0, s51
	s_add_u32 s46, s10, s84
	global_load_lds_dwordx4 v[214:215], off
	s_addc_u32 s47, s11, 0
	s_mov_b32 m0, s39
	s_nop 0
	global_load_lds_dwordx4 v212, s[46:47]
	s_mov_b32 m0, s52
	s_nop 0
	global_load_lds_dwordx4 v202, s[46:47]
	s_waitcnt vmcnt(8)
	s_waitcnt lgkmcnt(0)
	s_barrier
	s_setprio 1
	v_mfma_f32_16x16x128_f8f6f4 v[126:129], v[18:25], v[34:41], v[126:129]
	v_mfma_f32_16x16x128_f8f6f4 v[118:121], v[26:33], v[34:41], v[118:121]
	v_mfma_f32_16x16x128_f8f6f4 v[110:113], v[18:25], v[42:49], v[110:113]
	v_mfma_f32_16x16x128_f8f6f4 v[102:105], v[26:33], v[42:49], v[102:105]
	v_mfma_f32_16x16x128_f8f6f4 v[94:97], v[18:25], v[50:57], v[94:97]
	v_mfma_f32_16x16x128_f8f6f4 v[86:89], v[26:33], v[50:57], v[86:89]
	v_mfma_f32_16x16x128_f8f6f4 v[78:81], v[18:25], v[58:65], v[78:81]
	v_mfma_f32_16x16x128_f8f6f4 v[70:73], v[26:33], v[58:65], v[70:73]
	s_setprio 0
	s_setprio 1
	v_mfma_f32_16x16x128_f8f6f4 v[122:125], v[2:9], v[34:41], v[122:125]
	v_mfma_f32_16x16x128_f8f6f4 v[114:117], v[10:17], v[34:41], v[114:117]
	v_mfma_f32_16x16x128_f8f6f4 v[106:109], v[2:9], v[42:49], v[106:109]
	v_mfma_f32_16x16x128_f8f6f4 v[98:101], v[10:17], v[42:49], v[98:101]
	v_mfma_f32_16x16x128_f8f6f4 v[90:93], v[2:9], v[50:57], v[90:93]
	v_mfma_f32_16x16x128_f8f6f4 v[82:85], v[10:17], v[50:57], v[82:85]
	v_mfma_f32_16x16x128_f8f6f4 v[74:77], v[2:9], v[58:65], v[74:77]
	v_mfma_f32_16x16x128_f8f6f4 v[66:69], v[10:17], v[58:65], v[66:69]
	s_setprio 0
	s_barrier
; #define PG8_STAGE(bufoff, gbase, voff) do { _Pragma("unroll") for (int _i = 0; _i < 2; ++_i) \
;         __builtin_amdgcn_global_load_lds((const unsigned*)(wsb + (size_t)(gbase) + (voff)[_i]), (LAS unsigned*)(lds + (bufoff) + ldsw + _i * 8192), 16, 0, 0); } while (0)
; #define PG8_WAIT_V(n) asm volatile("s_waitcnt vmcnt(" #n ")" ::: "memory")
; #define PG8_BAR __builtin_amdgcn_s_barrier()
; template <class Epi, class Sched, bool PERM, bool FP8 = false, bool GATHER = false>
; DI void gemm_phase(LAS unsigned char* lds, const unsigned char* wsb, const unsigned lda, const unsigned ldb, const int nt, const Sched& S, const Epi& E) {
;     ...
;         for (int t = 0; t < nt; t += 2) {
;             const bool last = (t == nt - 2);
;             const unsigned b2 = last ? nB : cB + (unsigned)(t + 2) * kstep, b3 = b2 + kstep;
;             const int k2 = last ? 0 : t + 2, k3 = k2 + 1;
;             PG8_LDB(B0, 0, 0); PG8_LDB(B1, 0, 1); PG8_SCHED; PG8_LDA(At, 0, 0); PG8_STAGEA(PG8_SA(1, 1), t + 1, 1, false);
;             if constexpr (GATHER) { if (last) {
;                 int tz = tid; asm volatile("" : "+v"(tz));
; #pragma unroll
;                 for (int i = 0; i < 2; ++i) { int R, C; stage_rc(tz * 16 + i * 8192, R, C);
; #pragma unroll
;                     for (int h = 0; h < 2; ++h) { const unsigned tk = (unsigned)tokt[h * HALF + R]; offC[h][i] = (tk < (unsigned)NTOK ? tk : (unsigned)(NTOK - 1)) * lda + (unsigned)C * 2u; } } } }
;             PG8_WAIT_V(8); PG8_WAIT_L(0); PG8_BAR; PG8_MMA(0, 0, At, B0); PG8_MMA(0, 1, At, B1); PG8_BAR; PG8_SCHED;
;             PG8_LDA(At, 0, 1); PG8_STAGE(PG8_SB(0, 0), b2, voffB); PG8_STAGE(PG8_SB(0, 1), b2 + hstepB, voffB); PG8_STAGEA(PG8_SA(0, 0), k2, 0, last);
;             PG8_WAIT_V(8); PG8_WAIT_L(0); PG8_BAR; PG8_MMA(1, 0, At, B0); PG8_MMA(1, 1, At, B1); PG8_BAR; PG8_SCHED;
;             PG8_LDB(B0, 1, 0); PG8_LDB(B1, 1, 1); PG8_SCHED; PG8_LDA(At, 1, 0); PG8_STAGEA(PG8_SA(0, 1), k2, 1, last);
;             PG8_WAIT_V(8); PG8_WAIT_L(0); PG8_BAR; PG8_MMA(0, 0, At, B0); PG8_MMA(0, 1, At, B1); PG8_BAR; PG8_SCHED;
;             PG8_LDA(At, 1, 1); PG8_STAGE(PG8_SB(1, 0), b3, voffB); PG8_STAGE(PG8_SB(1, 1), b3 + hstepB, voffB); PG8_STAGEA(PG8_SA(1, 0), k3, 0, last);
;             PG8_WAIT_V(8); PG8_WAIT_L(0); PG8_BAR; PG8_MMA(1, 0, At, B0); PG8_MMA(1, 1, At, B1); PG8_BAR; PG8_SCHED;
;         }
;         if (wr == 0) PG8_BAR;
	ds_read_b128 v[2:5], v210 offset:32768
	ds_read_b128 v[6:9], v210 offset:33792
	ds_read_b128 v[10:13], v210 offset:34816
	ds_read_b128 v[14:17], v210 offset:35840
	ds_read_b128 v[18:21], v210 offset:49152
	ds_read_b128 v[22:25], v210 offset:50176
	ds_read_b128 v[26:29], v210 offset:51200
	ds_read_b128 v[30:33], v210 offset:52224
	s_mov_b32 m0, s53
	v_lshl_add_u64 v[214:215], s[46:47], 0, v[196:197]
	ds_read_b128 v[34:37], v209 offset:32768
	ds_read_b128 v[38:41], v209 offset:33792
	ds_read_b128 v[42:45], v209 offset:34816
	ds_read_b128 v[46:49], v209 offset:35840
	ds_read_b128 v[50:53], v209 offset:36864
	ds_read_b128 v[54:57], v209 offset:37888
	ds_read_b128 v[58:61], v209 offset:38912
	ds_read_b128 v[62:65], v209 offset:39936
	global_load_lds_dwordx4 v[214:215], off
	v_lshl_add_u64 v[214:215], s[46:47], 0, v[204:205]
	s_mov_b32 m0, s54
	s_nop 0
	global_load_lds_dwordx4 v[214:215], off
	s_waitcnt vmcnt(8)
	s_waitcnt lgkmcnt(0)
	s_barrier
	s_setprio 1
	v_mfma_f32_16x16x128_f8f6f4 v[190:193], v[2:9], v[34:41], v[190:193]
	v_mfma_f32_16x16x128_f8f6f4 v[186:189], v[10:17], v[34:41], v[186:189]
	v_mfma_f32_16x16x128_f8f6f4 v[174:177], v[2:9], v[42:49], v[174:177]
	v_mfma_f32_16x16x128_f8f6f4 v[166:169], v[10:17], v[42:49], v[166:169]
	v_mfma_f32_16x16x128_f8f6f4 v[158:161], v[2:9], v[50:57], v[158:161]
	v_mfma_f32_16x16x128_f8f6f4 v[150:153], v[10:17], v[50:57], v[150:153]
	v_mfma_f32_16x16x128_f8f6f4 v[142:145], v[2:9], v[58:65], v[142:145]
	v_mfma_f32_16x16x128_f8f6f4 v[134:137], v[10:17], v[58:65], v[134:137]
	s_setprio 0
	s_setprio 1
	v_mfma_f32_16x16x128_f8f6f4 v[182:185], v[18:25], v[34:41], v[182:185]
	v_mfma_f32_16x16x128_f8f6f4 v[178:181], v[26:33], v[34:41], v[178:181]
	v_mfma_f32_16x16x128_f8f6f4 v[170:173], v[18:25], v[42:49], v[170:173]
	v_mfma_f32_16x16x128_f8f6f4 v[162:165], v[26:33], v[42:49], v[162:165]
	v_mfma_f32_16x16x128_f8f6f4 v[154:157], v[18:25], v[50:57], v[154:157]
	v_mfma_f32_16x16x128_f8f6f4 v[146:149], v[26:33], v[50:57], v[146:149]
	v_mfma_f32_16x16x128_f8f6f4 v[138:141], v[18:25], v[58:65], v[138:141]
	v_mfma_f32_16x16x128_f8f6f4 v[130:133], v[26:33], v[58:65], v[130:133]
	s_setprio 0
	s_barrier
	s_add_u32 s46, s8, s83
	s_addc_u32 s47, s9, 0
	s_mov_b32 m0, s58
	v_lshl_add_u64 v[214:215], s[46:47], 0, v[198:199]
	s_add_i32 s82, s82, 0x20080
	ds_read_b128 v[34:37], v209 offset:49152
	ds_read_b128 v[38:41], v209 offset:50176
	ds_read_b128 v[42:45], v209 offset:51200
	ds_read_b128 v[46:49], v209 offset:52224
	ds_read_b128 v[50:53], v209 offset:53248
	ds_read_b128 v[54:57], v209 offset:54272
	ds_read_b128 v[58:61], v209 offset:55296
	ds_read_b128 v[62:65], v209 offset:56320
	global_load_lds_dwordx4 v[214:215], off
	v_lshl_add_u64 v[214:215], s[46:47], 0, v[200:201]
	s_add_u32 s46, s8, s82
	s_mov_b32 m0, s59
	s_addc_u32 s47, s9, 0
	global_load_lds_dwordx4 v[214:215], off
	v_lshl_add_u64 v[214:215], s[46:47], 0, v[198:199]
	s_mov_b32 m0, s64
	s_nop 0
	global_load_lds_dwordx4 v[214:215], off
	v_lshl_add_u64 v[214:215], s[46:47], 0, v[200:201]
	s_add_u32 s46, s8, s84
	s_addc_u32 s47, s9, 0
	s_mov_b32 m0, s65
	s_add_u32 s46, s46, 0x5b9d4080
	global_load_lds_dwordx4 v[214:215], off
	s_addc_u32 s47, s47, 0
	s_mov_b32 m0, s60
	s_nop 0
	global_load_lds_dwordx4 v212, s[46:47]
	s_mov_b32 m0, s61
	s_nop 0
	global_load_lds_dwordx4 v202, s[46:47]
	s_waitcnt vmcnt(8)
	s_waitcnt lgkmcnt(0)
	s_barrier
	s_setprio 1
	v_mfma_f32_16x16x128_f8f6f4 v[126:129], v[2:9], v[34:41], v[126:129]
	v_mfma_f32_16x16x128_f8f6f4 v[118:121], v[10:17], v[34:41], v[118:121]
	v_mfma_f32_16x16x128_f8f6f4 v[110:113], v[2:9], v[42:49], v[110:113]
	v_mfma_f32_16x16x128_f8f6f4 v[102:105], v[10:17], v[42:49], v[102:105]
	v_mfma_f32_16x16x128_f8f6f4 v[94:97], v[2:9], v[50:57], v[94:97]
	v_mfma_f32_16x16x128_f8f6f4 v[86:89], v[10:17], v[50:57], v[86:89]
	v_mfma_f32_16x16x128_f8f6f4 v[78:81], v[2:9], v[58:65], v[78:81]
	v_mfma_f32_16x16x128_f8f6f4 v[70:73], v[10:17], v[58:65], v[70:73]
	s_setprio 0
	s_setprio 1
	v_mfma_f32_16x16x128_f8f6f4 v[122:125], v[18:25], v[34:41], v[122:125]
	v_mfma_f32_16x16x128_f8f6f4 v[114:117], v[26:33], v[34:41], v[114:117]
	v_mfma_f32_16x16x128_f8f6f4 v[106:109], v[18:25], v[42:49], v[106:109]
	v_mfma_f32_16x16x128_f8f6f4 v[98:101], v[26:33], v[42:49], v[98:101]
	v_mfma_f32_16x16x128_f8f6f4 v[90:93], v[18:25], v[50:57], v[90:93]
	v_mfma_f32_16x16x128_f8f6f4 v[82:85], v[26:33], v[50:57], v[82:85]
	v_mfma_f32_16x16x128_f8f6f4 v[74:77], v[18:25], v[58:65], v[74:77]
	v_mfma_f32_16x16x128_f8f6f4 v[66:69], v[26:33], v[58:65], v[66:69]
	s_setprio 0
	s_barrier
	s_add_i32 s81, s81, 2
	s_cmp_gt_u32 s81, 5
	s_cbranch_scc1 .LBB0_2547

; #define PG8_STAGE(bufoff, gbase, voff) do { _Pragma("unroll") for (int _i = 0; _i < 2; ++_i) \
;         __builtin_amdgcn_global_load_lds((const unsigned*)(wsb + (size_t)(gbase) + (voff)[_i]), (LAS unsigned*)(lds + (bufoff) + ldsw + _i * 8192), 16, 0, 0); } while (0)
; #define PG8_WAIT_V(n) asm volatile("s_waitcnt vmcnt(" #n ")" ::: "memory")
; #define PG8_WAIT_L(n) asm volatile("s_waitcnt lgkmcnt(" #n ")" ::: "memory")
; template <class Epi, class Sched, bool PERM, bool FP8 = false, bool GATHER = false>
; DI void gemm_phase(LAS unsigned char* lds, const unsigned char* wsb, const unsigned lda, const unsigned ldb, const int nt, const Sched& S, const Epi& E) {
;     ...
;         for (int t = 0; t < nt; t += 2) {
;             const bool last = (t == nt - 2);
;             const unsigned b2 = last ? nB : cB + (unsigned)(t + 2) * kstep, b3 = b2 + kstep;
;             const int k2 = last ? 0 : t + 2, k3 = k2 + 1;
;             PG8_LDB(B0, 0, 0); PG8_LDB(B1, 0, 1); PG8_SCHED; PG8_LDA(At, 0, 0); PG8_STAGEA(PG8_SA(1, 1), t + 1, 1, false);
;             if constexpr (GATHER) { if (last) {
;                 int tz = tid; asm volatile("" : "+v"(tz));
; #pragma unroll
;                 for (int i = 0; i < 2; ++i) { int R, C; stage_rc(tz * 16 + i * 8192, R, C);
; #pragma unroll
;                     for (int h = 0; h < 2; ++h) { const unsigned tk = (unsigned)tokt[h * HALF + R]; offC[h][i] = (tk < (unsigned)NTOK ? tk : (unsigned)(NTOK - 1)) * lda + (unsigned)C * 2u; } } } }
;             PG8_WAIT_V(8); PG8_WAIT_L(0); PG8_BAR; PG8_MMA(0, 0, At, B0); PG8_MMA(0, 1, At, B1); PG8_BAR; PG8_SCHED;
;             PG8_LDA(At, 0, 1); PG8_STAGE(PG8_SB(0, 0), b2, voffB); PG8_STAGE(PG8_SB(0, 1), b2 + hstepB, voffB); PG8_STAGEA(PG8_SA(0, 0), k2, 0, last);
;             PG8_WAIT_V(8); PG8_WAIT_L(0); PG8_BAR; PG8_MMA(1, 0, At, B0); PG8_MMA(1, 1, At, B1); PG8_BAR; PG8_SCHED;
;             PG8_LDB(B0, 1, 0); PG8_LDB(B1, 1, 1); PG8_SCHED; PG8_LDA(At, 1, 0); PG8_STAGEA(PG8_SA(0, 1), k2, 1, last);
;             PG8_WAIT_V(8); PG8_WAIT_L(0); PG8_BAR; PG8_MMA(0, 0, At, B0); PG8_MMA(0, 1, At, B1); PG8_BAR; PG8_SCHED;
;             PG8_LDA(At, 1, 1); PG8_STAGE(PG8_SB(1, 0), b3, voffB); PG8_STAGE(PG8_SB(1, 1), b3 + hstepB, voffB); PG8_STAGEA(PG8_SA(1, 0), k3, 0, last);
;             PG8_WAIT_V(8); PG8_WAIT_L(0); PG8_BAR; PG8_MMA(1, 0, At, B0); PG8_MMA(1, 1, At, B1); PG8_BAR; PG8_SCHED;
.LBB0_2652:
	ds_read_b128 v[130:133], v154
	ds_read_b128 v[134:137], v154 offset:1024
	ds_read_b128 v[138:141], v154 offset:2048
	ds_read_b128 v[142:145], v154 offset:3072
	ds_read_b128 v[158:161], v154 offset:16384
	ds_read_b128 v[162:165], v154 offset:17408
	ds_read_b128 v[166:169], v154 offset:18432
	ds_read_b128 v[170:173], v154 offset:19456
	s_add_i32 s70, s67, 0xfffe0080
	s_add_i32 s71, s70, s64
	s_cmp_eq_u32 s66, 4
	s_cselect_b64 s[24:25], -1, 0
	s_and_b64 s[68:69], s[24:25], exec
	s_cselect_b32 s68, s65, s71
	s_cselect_b32 s72, 0, s70
	s_add_i32 s69, s68, 0x80
	s_add_i32 s70, s62, s67
	s_add_u32 s70, s8, s70
	s_addc_u32 s71, s9, 0
	v_lshl_add_u64 v[150:151], s[70:71], 0, v[146:147]
	s_add_i32 m0, s26, 0xc000
	ds_read_b128 v[174:177], v153
	ds_read_b128 v[178:181], v153 offset:1024
	ds_read_b128 v[182:185], v153 offset:2048
	ds_read_b128 v[186:189], v153 offset:3072
	ds_read_b128 v[190:193], v153 offset:4096
	ds_read_b128 v[194:197], v153 offset:5120
	ds_read_b128 v[198:201], v153 offset:6144
	ds_read_b128 v[202:205], v153 offset:7168
	global_load_lds_dwordx4 v[150:151], off
	v_lshl_add_u64 v[150:151], s[70:71], 0, v[148:149]
	s_add_i32 m0, s26, 0xe000
	s_nop 0
	global_load_lds_dwordx4 v[150:151], off
	s_waitcnt vmcnt(8)
	s_waitcnt lgkmcnt(0)
	s_barrier
	s_setprio 1
	v_mfma_f32_16x16x128_f8f6f4 v[126:129], v[130:137], v[174:181], v[126:129]
	v_mfma_f32_16x16x128_f8f6f4 v[122:125], v[138:145], v[174:181], v[122:125]
	v_mfma_f32_16x16x128_f8f6f4 v[118:121], v[130:137], v[182:189], v[118:121]
	v_mfma_f32_16x16x128_f8f6f4 v[114:117], v[138:145], v[182:189], v[114:117]
	v_mfma_f32_16x16x128_f8f6f4 v[206:209], v[130:137], v[190:197], v[94:97]
	v_mfma_f32_16x16x128_f8f6f4 v[210:213], v[138:145], v[190:197], v[90:93]
	v_mfma_f32_16x16x128_f8f6f4 v[214:217], v[130:137], v[198:205], v[82:85]
	v_mfma_f32_16x16x128_f8f6f4 v[218:221], v[138:145], v[198:205], v[74:77]
	s_setprio 0
	s_setprio 1
	v_mfma_f32_16x16x128_f8f6f4 v[110:113], v[158:165], v[174:181], v[110:113]
	v_mfma_f32_16x16x128_f8f6f4 v[106:109], v[166:173], v[174:181], v[106:109]
	v_mfma_f32_16x16x128_f8f6f4 v[102:105], v[158:165], v[182:189], v[102:105]
	v_mfma_f32_16x16x128_f8f6f4 v[98:101], v[166:173], v[182:189], v[98:101]
	v_mfma_f32_16x16x128_f8f6f4 v[174:177], v[158:165], v[190:197], v[86:89]
	v_mfma_f32_16x16x128_f8f6f4 v[178:181], v[166:173], v[190:197], v[78:81]
	v_mfma_f32_16x16x128_f8f6f4 v[182:185], v[158:165], v[198:205], v[70:73]
	v_mfma_f32_16x16x128_f8f6f4 v[186:189], v[166:173], v[198:205], v[66:69]
	s_setprio 0
	s_barrier
	s_add_u32 s70, s8, s68
	s_addc_u32 s71, s9, 0
	s_mov_b32 m0, s27
	v_lshl_add_u64 v[150:151], s[70:71], 0, v[146:147]
	s_nop 0
	ds_read_b128 v[66:69], v153 offset:16384
	ds_read_b128 v[70:73], v153 offset:17408
	ds_read_b128 v[74:77], v153 offset:18432
	ds_read_b128 v[78:81], v153 offset:19456
	ds_read_b128 v[82:85], v153 offset:20480
	ds_read_b128 v[86:89], v153 offset:21504
	ds_read_b128 v[90:93], v153 offset:22528
	ds_read_b128 v[94:97], v153 offset:23552
	global_load_lds_dwordx4 v[150:151], off
	v_lshl_add_u64 v[150:151], s[70:71], 0, v[148:149]
	s_add_i32 s70, s68, 0x20000
	s_add_u32 s70, s8, s70
	s_addc_u32 s71, s9, 0
	s_and_b64 s[24:25], s[20:21], s[24:25]
	s_and_b64 s[24:25], s[24:25], exec
	s_mov_b32 m0, s28
	s_cselect_b32 s24, s58, s62
	global_load_lds_dwordx4 v[150:151], off
	v_lshl_add_u64 v[150:151], s[70:71], 0, v[146:147]
	s_mov_b32 m0, s29
	s_add_i32 s24, s72, s24
	global_load_lds_dwordx4 v[150:151], off
	v_lshl_add_u64 v[150:151], s[70:71], 0, v[148:149]
	s_add_u32 s70, s8, s24
	s_mov_b32 m0, s36
	s_addc_u32 s71, s9, 0
	global_load_lds_dwordx4 v[150:151], off
	v_lshl_add_u64 v[150:151], s[70:71], 0, v[146:147]
	s_mov_b32 m0, s26
	s_nop 0
	global_load_lds_dwordx4 v[150:151], off
	v_lshl_add_u64 v[150:151], s[70:71], 0, v[148:149]
	s_mov_b32 m0, s37
	s_nop 0
	global_load_lds_dwordx4 v[150:151], off
	s_waitcnt vmcnt(8)
	s_waitcnt lgkmcnt(0)
	s_barrier
	s_setprio 1
	v_mfma_f32_16x16x128_f8f6f4 v[62:65], v[130:137], v[66:73], v[62:65]
	v_mfma_f32_16x16x128_f8f6f4 v[58:61], v[138:145], v[66:73], v[58:61]
	v_mfma_f32_16x16x128_f8f6f4 v[50:53], v[130:137], v[74:81], v[50:53]
	v_mfma_f32_16x16x128_f8f6f4 v[190:193], v[138:145], v[74:81], v[42:45]
	v_mfma_f32_16x16x128_f8f6f4 v[194:197], v[130:137], v[82:89], v[34:37]
	v_mfma_f32_16x16x128_f8f6f4 v[198:201], v[138:145], v[82:89], v[26:29]
	v_mfma_f32_16x16x128_f8f6f4 v[202:205], v[130:137], v[90:97], v[18:21]
	v_mfma_f32_16x16x128_f8f6f4 v[222:225], v[138:145], v[90:97], v[10:13]
	s_setprio 0
	s_setprio 1
	v_mfma_f32_16x16x128_f8f6f4 v[54:57], v[158:165], v[66:73], v[54:57]
	v_mfma_f32_16x16x128_f8f6f4 v[226:229], v[166:173], v[66:73], v[46:49]
	v_mfma_f32_16x16x128_f8f6f4 v[230:233], v[158:165], v[74:81], v[38:41]
	v_mfma_f32_16x16x128_f8f6f4 v[234:237], v[166:173], v[74:81], v[30:33]
	v_mfma_f32_16x16x128_f8f6f4 v[238:241], v[158:165], v[82:89], v[22:25]
	v_mfma_f32_16x16x128_f8f6f4 v[242:245], v[166:173], v[82:89], v[14:17]
	v_mfma_f32_16x16x128_f8f6f4 v[246:249], v[158:165], v[90:97], v[6:9]
	v_mfma_f32_16x16x128_f8f6f4 v[250:253], v[166:173], v[90:97], v[2:5]
	s_setprio 0
	s_barrier
; #define PG8_STAGE(bufoff, gbase, voff) do { _Pragma("unroll") for (int _i = 0; _i < 2; ++_i) \
;         __builtin_amdgcn_global_load_lds((const unsigned*)(wsb + (size_t)(gbase) + (voff)[_i]), (LAS unsigned*)(lds + (bufoff) + ldsw + _i * 8192), 16, 0, 0); } while (0)
; #define PG8_WAIT_V(n) asm volatile("s_waitcnt vmcnt(" #n ")" ::: "memory")
; #define PG8_BAR __builtin_amdgcn_s_barrier()
; template <class Epi, class Sched, bool PERM, bool FP8 = false, bool GATHER = false>
; DI void gemm_phase(LAS unsigned char* lds, const unsigned char* wsb, const unsigned lda, const unsigned ldb, const int nt, const Sched& S, const Epi& E) {
;     ...
;         for (int t = 0; t < nt; t += 2) {
;             const bool last = (t == nt - 2);
;             const unsigned b2 = last ? nB : cB + (unsigned)(t + 2) * kstep, b3 = b2 + kstep;
;             const int k2 = last ? 0 : t + 2, k3 = k2 + 1;
;             PG8_LDB(B0, 0, 0); PG8_LDB(B1, 0, 1); PG8_SCHED; PG8_LDA(At, 0, 0); PG8_STAGEA(PG8_SA(1, 1), t + 1, 1, false);
;             if constexpr (GATHER) { if (last) {
;                 int tz = tid; asm volatile("" : "+v"(tz));
; #pragma unroll
;                 for (int i = 0; i < 2; ++i) { int R, C; stage_rc(tz * 16 + i * 8192, R, C);
; #pragma unroll
;                     for (int h = 0; h < 2; ++h) { const unsigned tk = (unsigned)tokt[h * HALF + R]; offC[h][i] = (tk < (unsigned)NTOK ? tk : (unsigned)(NTOK - 1)) * lda + (unsigned)C * 2u; } } } }
;             PG8_WAIT_V(8); PG8_WAIT_L(0); PG8_BAR; PG8_MMA(0, 0, At, B0); PG8_MMA(0, 1, At, B1); PG8_BAR; PG8_SCHED;
;             PG8_LDA(At, 0, 1); PG8_STAGE(PG8_SB(0, 0), b2, voffB); PG8_STAGE(PG8_SB(0, 1), b2 + hstepB, voffB); PG8_STAGEA(PG8_SA(0, 0), k2, 0, last);
;             PG8_WAIT_V(8); PG8_WAIT_L(0); PG8_BAR; PG8_MMA(1, 0, At, B0); PG8_MMA(1, 1, At, B1); PG8_BAR; PG8_SCHED;
;             PG8_LDB(B0, 1, 0); PG8_LDB(B1, 1, 1); PG8_SCHED; PG8_LDA(At, 1, 0); PG8_STAGEA(PG8_SA(0, 1), k2, 1, last);
;             PG8_WAIT_V(8); PG8_WAIT_L(0); PG8_BAR; PG8_MMA(0, 0, At, B0); PG8_MMA(0, 1, At, B1); PG8_BAR; PG8_SCHED;
;             PG8_LDA(At, 1, 1); PG8_STAGE(PG8_SB(1, 0), b3, voffB); PG8_STAGE(PG8_SB(1, 1), b3 + hstepB, voffB); PG8_STAGEA(PG8_SA(1, 0), k3, 0, last);
;             PG8_WAIT_V(8); PG8_WAIT_L(0); PG8_BAR; PG8_MMA(1, 0, At, B0); PG8_MMA(1, 1, At, B1); PG8_BAR; PG8_SCHED;
;         }
;         if (wr == 0) PG8_BAR;
	s_nop 4
	ds_read_b128 v[2:5], v154 offset:32768
	ds_read_b128 v[6:9], v154 offset:33792
	ds_read_b128 v[10:13], v154 offset:34816
	ds_read_b128 v[14:17], v154 offset:35840
	ds_read_b128 v[130:133], v154 offset:49152
	ds_read_b128 v[134:137], v154 offset:50176
	ds_read_b128 v[138:141], v154 offset:51200
	ds_read_b128 v[142:145], v154 offset:52224
	s_add_i32 s25, s24, 0x20000
	s_add_u32 s70, s8, s25
	s_addc_u32 s71, s9, 0
	s_mov_b32 m0, s38
	v_lshl_add_u64 v[66:67], s[70:71], 0, v[146:147]
	ds_read_b128 v[18:21], v153 offset:32768
	ds_read_b128 v[22:25], v153 offset:33792
	ds_read_b128 v[26:29], v153 offset:34816
	ds_read_b128 v[30:33], v153 offset:35840
	ds_read_b128 v[34:37], v153 offset:36864
	ds_read_b128 v[38:41], v153 offset:37888
	ds_read_b128 v[42:45], v153 offset:38912
	ds_read_b128 v[46:49], v153 offset:39936
	global_load_lds_dwordx4 v[66:67], off
	v_lshl_add_u64 v[66:67], s[70:71], 0, v[148:149]
	s_mov_b32 m0, s39
	s_nop 0
	global_load_lds_dwordx4 v[66:67], off
	s_waitcnt vmcnt(8)
	s_waitcnt lgkmcnt(0)
	s_barrier
	s_setprio 1
	v_mfma_f32_16x16x128_f8f6f4 v[126:129], v[2:9], v[18:25], v[126:129]
	v_mfma_f32_16x16x128_f8f6f4 v[122:125], v[10:17], v[18:25], v[122:125]
	v_mfma_f32_16x16x128_f8f6f4 v[118:121], v[2:9], v[26:33], v[118:121]
	v_mfma_f32_16x16x128_f8f6f4 v[114:117], v[10:17], v[26:33], v[114:117]
	v_mfma_f32_16x16x128_f8f6f4 v[94:97], v[2:9], v[34:41], v[206:209]
	v_mfma_f32_16x16x128_f8f6f4 v[90:93], v[10:17], v[34:41], v[210:213]
	v_mfma_f32_16x16x128_f8f6f4 v[82:85], v[2:9], v[42:49], v[214:217]
	v_mfma_f32_16x16x128_f8f6f4 v[74:77], v[10:17], v[42:49], v[218:221]
	s_setprio 0
	s_setprio 1
	v_mfma_f32_16x16x128_f8f6f4 v[110:113], v[130:137], v[18:25], v[110:113]
	v_mfma_f32_16x16x128_f8f6f4 v[106:109], v[138:145], v[18:25], v[106:109]
	v_mfma_f32_16x16x128_f8f6f4 v[102:105], v[130:137], v[26:33], v[102:105]
	v_mfma_f32_16x16x128_f8f6f4 v[98:101], v[138:145], v[26:33], v[98:101]
	v_mfma_f32_16x16x128_f8f6f4 v[86:89], v[130:137], v[34:41], v[174:177]
	v_mfma_f32_16x16x128_f8f6f4 v[78:81], v[138:145], v[34:41], v[178:181]
	v_mfma_f32_16x16x128_f8f6f4 v[70:73], v[130:137], v[42:49], v[182:185]
	v_mfma_f32_16x16x128_f8f6f4 v[66:69], v[138:145], v[42:49], v[186:189]
	s_setprio 0
	s_barrier
	s_add_u32 s70, s8, s69
	s_addc_u32 s71, s9, 0
	s_add_i32 s68, s68, 0x20080
	s_mov_b32 m0, s43
	v_lshl_add_u64 v[18:19], s[70:71], 0, v[146:147]
	s_add_u32 s68, s8, s68
	ds_read_b128 v[158:161], v153 offset:49152
	ds_read_b128 v[162:165], v153 offset:50176
	ds_read_b128 v[166:169], v153 offset:51200
	ds_read_b128 v[170:173], v153 offset:52224
	ds_read_b128 v[174:177], v153 offset:53248
	ds_read_b128 v[178:181], v153 offset:54272
	ds_read_b128 v[182:185], v153 offset:55296
	ds_read_b128 v[186:189], v153 offset:56320
	global_load_lds_dwordx4 v[18:19], off
	v_lshl_add_u64 v[18:19], s[70:71], 0, v[148:149]
	s_mov_b32 m0, s44
	s_addc_u32 s69, s9, 0
	s_addk_i32 s24, 0x80
	global_load_lds_dwordx4 v[18:19], off
	v_lshl_add_u64 v[18:19], s[68:69], 0, v[146:147]
	s_mov_b32 m0, s47
	s_add_u32 s24, s8, s24
	global_load_lds_dwordx4 v[18:19], off
	v_lshl_add_u64 v[18:19], s[68:69], 0, v[148:149]
	s_mov_b32 m0, s48
	s_addc_u32 s25, s9, 0
	global_load_lds_dwordx4 v[18:19], off
	v_lshl_add_u64 v[18:19], s[24:25], 0, v[146:147]
	s_mov_b32 m0, s45
	s_nop 0
	global_load_lds_dwordx4 v[18:19], off
	v_lshl_add_u64 v[18:19], s[24:25], 0, v[148:149]
	s_mov_b32 m0, s46
	s_nop 0
	global_load_lds_dwordx4 v[18:19], off
	s_waitcnt vmcnt(8)
	s_waitcnt lgkmcnt(0)
	s_barrier
	s_setprio 1
	v_mfma_f32_16x16x128_f8f6f4 v[62:65], v[2:9], v[158:165], v[62:65]
	v_mfma_f32_16x16x128_f8f6f4 v[58:61], v[10:17], v[158:165], v[58:61]
	v_mfma_f32_16x16x128_f8f6f4 v[50:53], v[2:9], v[166:173], v[50:53]
	v_mfma_f32_16x16x128_f8f6f4 v[42:45], v[10:17], v[166:173], v[190:193]
	v_mfma_f32_16x16x128_f8f6f4 v[34:37], v[2:9], v[174:181], v[194:197]
	v_mfma_f32_16x16x128_f8f6f4 v[26:29], v[10:17], v[174:181], v[198:201]
	v_mfma_f32_16x16x128_f8f6f4 v[18:21], v[2:9], v[182:189], v[202:205]
	v_mfma_f32_16x16x128_f8f6f4 v[10:13], v[10:17], v[182:189], v[222:225]
	s_setprio 0
	s_setprio 1
	v_mfma_f32_16x16x128_f8f6f4 v[54:57], v[130:137], v[158:165], v[54:57]
	v_mfma_f32_16x16x128_f8f6f4 v[46:49], v[138:145], v[158:165], v[226:229]
	v_mfma_f32_16x16x128_f8f6f4 v[38:41], v[130:137], v[166:173], v[230:233]
	v_mfma_f32_16x16x128_f8f6f4 v[30:33], v[138:145], v[166:173], v[234:237]
	v_mfma_f32_16x16x128_f8f6f4 v[22:25], v[130:137], v[174:181], v[238:241]
	v_mfma_f32_16x16x128_f8f6f4 v[14:17], v[138:145], v[174:181], v[242:245]
	v_mfma_f32_16x16x128_f8f6f4 v[6:9], v[130:137], v[182:189], v[246:249]
	v_mfma_f32_16x16x128_f8f6f4 v[2:5], v[138:145], v[182:189], v[250:253]
	s_setprio 0
	s_barrier
	s_add_i32 s66, s66, 2
	s_addk_i32 s67, 0x100
	s_cmp_gt_u32 s66, 5
	s_cbranch_scc0 .LBB0_2652
	s_and_b64 vcc, exec, s[12:13]
	s_cbranch_vccz .LBB0_2655
	s_barrier
